# GEMM K loops: LDS-DMA loads of each sub-phase issued before that sub-phase's ds_reads (more lookahead per stage)
# baseline (speedup 1.0000x reference)
.LBB0_229:
	s_add_i32 s73, s60, 2
	s_add_u32 s61, s58, 0xfffc0080
	s_addc_u32 s62, s59, -1
	s_add_i32 s74, 0, 0x10000
	s_cmp_eq_u32 s68, s60
	s_cselect_b32 s63, s39, s62
	s_cselect_b32 s62, s43, s61
	s_cselect_b32 s61, s47, s72
	s_cselect_b32 s60, s55, s71
	s_add_i32 s76, 0, 0x14000
	v_add_u32_e32 v156, s74, v165
	v_add_u32_e32 v166, s76, v165
	v_lshl_add_u64 v[216:217], s[58:59], 0, v[142:143]
	s_add_i32 m0, s8, 0xc000
	s_nop 0
	global_load_lds_dwordx4 v[216:217], off
	v_lshl_add_u64 v[216:217], s[58:59], 0, v[140:141]
	s_add_i32 m0, s8, 0xe000
	s_nop 0
	global_load_lds_dwordx4 v[216:217], off
	ds_read_b128 v[144:147], v156
	ds_read_b128 v[148:151], v156 offset:1024
	ds_read_b128 v[152:155], v156 offset:2048
	ds_read_b128 v[156:159], v156 offset:3072
	ds_read_b128 v[160:163], v166
	ds_read_b128 v[170:173], v166 offset:1024
	ds_read_b128 v[174:177], v166 offset:2048
	ds_read_b128 v[180:183], v166 offset:3072
	ds_read_b128 v[184:187], v178
	ds_read_b128 v[188:191], v178 offset:1024
	ds_read_b128 v[192:195], v178 offset:2048
	ds_read_b128 v[196:199], v178 offset:3072
	ds_read_b128 v[200:203], v178 offset:4096
	ds_read_b128 v[204:207], v178 offset:5120
	ds_read_b128 v[208:211], v178 offset:6144
	ds_read_b128 v[212:215], v178 offset:7168
	s_waitcnt vmcnt(8)
	s_waitcnt lgkmcnt(0)
	s_barrier
	s_setprio 1
	s_waitcnt lgkmcnt(0)
	v_mfma_f32_16x16x32_bf16 v[126:129], v[144:147], v[184:187], v[126:129]
	v_mfma_f32_16x16x32_bf16 v[122:125], v[152:155], v[184:187], v[122:125]
	v_mfma_f32_16x16x32_bf16 v[110:113], v[144:147], v[192:195], v[110:113]
	v_mfma_f32_16x16x32_bf16 v[106:109], v[152:155], v[192:195], v[106:109]
	v_mfma_f32_16x16x32_bf16 v[94:97], v[144:147], v[200:203], v[94:97]
	v_mfma_f32_16x16x32_bf16 v[90:93], v[152:155], v[200:203], v[90:93]
	v_mfma_f32_16x16x32_bf16 v[78:81], v[144:147], v[208:211], v[78:81]
	v_mfma_f32_16x16x32_bf16 v[74:77], v[152:155], v[208:211], v[74:77]
	v_mfma_f32_16x16x32_bf16 v[126:129], v[148:151], v[188:191], v[126:129]
	v_mfma_f32_16x16x32_bf16 v[122:125], v[156:159], v[188:191], v[122:125]
	v_mfma_f32_16x16x32_bf16 v[110:113], v[148:151], v[196:199], v[110:113]
	v_mfma_f32_16x16x32_bf16 v[106:109], v[156:159], v[196:199], v[106:109]
	v_mfma_f32_16x16x32_bf16 v[94:97], v[148:151], v[204:207], v[94:97]
	v_mfma_f32_16x16x32_bf16 v[90:93], v[156:159], v[204:207], v[90:93]
	v_mfma_f32_16x16x32_bf16 v[78:81], v[148:151], v[212:215], v[78:81]
	v_mfma_f32_16x16x32_bf16 v[74:77], v[156:159], v[212:215], v[74:77]
	s_setprio 0
	s_setprio 1
	v_mfma_f32_16x16x32_bf16 v[118:121], v[160:163], v[184:187], v[118:121]
	v_mfma_f32_16x16x32_bf16 v[114:117], v[174:177], v[184:187], v[114:117]
	v_mfma_f32_16x16x32_bf16 v[102:105], v[160:163], v[192:195], v[102:105]
	v_mfma_f32_16x16x32_bf16 v[98:101], v[174:177], v[192:195], v[98:101]
	v_mfma_f32_16x16x32_bf16 v[86:89], v[160:163], v[200:203], v[86:89]
	v_mfma_f32_16x16x32_bf16 v[82:85], v[174:177], v[200:203], v[82:85]
	v_mfma_f32_16x16x32_bf16 v[70:73], v[160:163], v[208:211], v[70:73]
	v_mfma_f32_16x16x32_bf16 v[66:69], v[174:177], v[208:211], v[66:69]
	v_mfma_f32_16x16x32_bf16 v[118:121], v[170:173], v[188:191], v[118:121]
	v_mfma_f32_16x16x32_bf16 v[114:117], v[180:183], v[188:191], v[114:117]
	v_mfma_f32_16x16x32_bf16 v[102:105], v[170:173], v[196:199], v[102:105]
	v_mfma_f32_16x16x32_bf16 v[98:101], v[180:183], v[196:199], v[98:101]
	v_mfma_f32_16x16x32_bf16 v[86:89], v[170:173], v[204:207], v[86:89]
	v_mfma_f32_16x16x32_bf16 v[82:85], v[180:183], v[204:207], v[82:85]
	v_mfma_f32_16x16x32_bf16 v[70:73], v[170:173], v[212:215], v[70:73]
	v_mfma_f32_16x16x32_bf16 v[66:69], v[180:183], v[212:215], v[66:69]
	s_setprio 0
	s_barrier
	s_add_i32 s74, s74, s1
	v_lshl_add_u64 v[216:217], s[60:61], 0, v[130:131]
	s_mov_b32 m0, s74
	s_nop 0
	global_load_lds_dwordx4 v[216:217], off
	s_add_i32 m0, s74, 0x2000
	s_add_u32 s74, s60, 0x40000
	v_lshl_add_u64 v[218:219], s[60:61], 0, v[132:133]
	s_addc_u32 s75, s61, 0
	s_add_i32 s76, s76, s1
	global_load_lds_dwordx4 v[218:219], off
	v_lshl_add_u64 v[220:221], s[74:75], 0, v[130:131]
	s_mov_b32 m0, s76
	v_lshl_add_u64 v[222:223], s[62:63], 0, v[136:137]
	global_load_lds_dwordx4 v[220:221], off
	v_lshl_add_u64 v[220:221], s[74:75], 0, v[132:133]
	s_add_i32 m0, s76, 0x2000
	s_nop 0
	global_load_lds_dwordx4 v[220:221], off
	v_lshl_add_u64 v[220:221], s[62:63], 0, v[134:135]
	s_mov_b32 m0, s8
	s_nop 0
	global_load_lds_dwordx4 v[220:221], off
	s_mov_b32 m0, s11
	s_nop 0
	global_load_lds_dwordx4 v[222:223], off
	ds_read_b128 v[184:187], v178 offset:16384
	ds_read_b128 v[188:191], v178 offset:17408
	ds_read_b128 v[192:195], v178 offset:18432
	ds_read_b128 v[196:199], v178 offset:19456
	ds_read_b128 v[200:203], v178 offset:20480
	ds_read_b128 v[204:207], v178 offset:21504
	ds_read_b128 v[208:211], v178 offset:22528
	ds_read_b128 v[212:215], v178 offset:23552
	s_waitcnt vmcnt(8)
	s_waitcnt lgkmcnt(0)
	s_barrier
	s_setprio 1
	s_waitcnt lgkmcnt(0)
	v_mfma_f32_16x16x32_bf16 v[62:65], v[144:147], v[184:187], v[62:65]
	v_mfma_f32_16x16x32_bf16 v[58:61], v[152:155], v[184:187], v[58:61]
	v_mfma_f32_16x16x32_bf16 v[46:49], v[144:147], v[192:195], v[46:49]
	v_mfma_f32_16x16x32_bf16 v[42:45], v[152:155], v[192:195], v[42:45]
	v_mfma_f32_16x16x32_bf16 v[30:33], v[144:147], v[200:203], v[30:33]
	v_mfma_f32_16x16x32_bf16 v[26:29], v[152:155], v[200:203], v[26:29]
	v_mfma_f32_16x16x32_bf16 v[14:17], v[144:147], v[208:211], v[14:17]
	v_mfma_f32_16x16x32_bf16 v[10:13], v[152:155], v[208:211], v[10:13]
	v_mfma_f32_16x16x32_bf16 v[62:65], v[148:151], v[188:191], v[62:65]
	v_mfma_f32_16x16x32_bf16 v[58:61], v[156:159], v[188:191], v[58:61]
	v_mfma_f32_16x16x32_bf16 v[46:49], v[148:151], v[196:199], v[46:49]
	v_mfma_f32_16x16x32_bf16 v[42:45], v[156:159], v[196:199], v[42:45]
	v_mfma_f32_16x16x32_bf16 v[30:33], v[148:151], v[204:207], v[30:33]
	v_mfma_f32_16x16x32_bf16 v[26:29], v[156:159], v[204:207], v[26:29]
	v_mfma_f32_16x16x32_bf16 v[14:17], v[148:151], v[212:215], v[14:17]
	v_mfma_f32_16x16x32_bf16 v[10:13], v[156:159], v[212:215], v[10:13]
	s_setprio 0
	s_setprio 1
	v_mfma_f32_16x16x32_bf16 v[54:57], v[160:163], v[184:187], v[54:57]
	v_mfma_f32_16x16x32_bf16 v[50:53], v[174:177], v[184:187], v[50:53]
	v_mfma_f32_16x16x32_bf16 v[38:41], v[160:163], v[192:195], v[38:41]
	v_mfma_f32_16x16x32_bf16 v[34:37], v[174:177], v[192:195], v[34:37]
	v_mfma_f32_16x16x32_bf16 v[22:25], v[160:163], v[200:203], v[22:25]
	v_mfma_f32_16x16x32_bf16 v[18:21], v[174:177], v[200:203], v[18:21]
	v_mfma_f32_16x16x32_bf16 v[6:9], v[160:163], v[208:211], v[6:9]
	v_mfma_f32_16x16x32_bf16 v[2:5], v[174:177], v[208:211], v[2:5]
	v_mfma_f32_16x16x32_bf16 v[54:57], v[170:173], v[188:191], v[54:57]
	v_mfma_f32_16x16x32_bf16 v[50:53], v[180:183], v[188:191], v[50:53]
	v_mfma_f32_16x16x32_bf16 v[38:41], v[170:173], v[196:199], v[38:41]
	v_mfma_f32_16x16x32_bf16 v[34:37], v[180:183], v[196:199], v[34:37]
	v_mfma_f32_16x16x32_bf16 v[22:25], v[170:173], v[204:207], v[22:25]
	v_mfma_f32_16x16x32_bf16 v[18:21], v[180:183], v[204:207], v[18:21]
	v_mfma_f32_16x16x32_bf16 v[6:9], v[170:173], v[212:215], v[6:9]
	v_mfma_f32_16x16x32_bf16 v[2:5], v[180:183], v[212:215], v[2:5]
	s_setprio 0
	s_barrier
	s_add_i32 s74, 0, 0x18000
	s_add_i32 s75, 0, 0x1c000
	v_add_u32_e32 v156, s74, v165
	v_add_u32_e32 v166, s75, v165
	s_add_u32 s62, s62, 0x40000
	s_addc_u32 s63, s63, 0
	s_mov_b32 m0, s16
	v_lshl_add_u64 v[232:233], s[62:63], 0, v[134:135]
	global_load_lds_dwordx4 v[232:233], off
	v_lshl_add_u64 v[232:233], s[62:63], 0, v[136:137]
	s_mov_b32 m0, s25
	s_nop 0
	global_load_lds_dwordx4 v[232:233], off
	ds_read_b128 v[144:147], v156
	ds_read_b128 v[148:151], v156 offset:1024
	ds_read_b128 v[152:155], v156 offset:2048
	ds_read_b128 v[156:159], v156 offset:3072
	ds_read_b128 v[160:163], v166
	ds_read_b128 v[170:173], v166 offset:1024
	ds_read_b128 v[174:177], v166 offset:2048
	ds_read_b128 v[180:183], v166 offset:3072
	ds_read_b128 v[184:187], v178 offset:32768
	ds_read_b128 v[188:191], v178 offset:33792
	ds_read_b128 v[192:195], v178 offset:34816
	ds_read_b128 v[196:199], v178 offset:35840
	ds_read_b128 v[200:203], v178 offset:36864
	ds_read_b128 v[204:207], v178 offset:37888
	ds_read_b128 v[208:211], v178 offset:38912
	ds_read_b128 v[212:215], v178 offset:39936
	s_waitcnt vmcnt(8)
	s_waitcnt lgkmcnt(0)
	s_barrier
	s_setprio 1
	s_waitcnt lgkmcnt(0)
	v_mfma_f32_16x16x32_bf16 v[126:129], v[144:147], v[184:187], v[126:129]
	v_mfma_f32_16x16x32_bf16 v[122:125], v[152:155], v[184:187], v[122:125]
	v_mfma_f32_16x16x32_bf16 v[110:113], v[144:147], v[192:195], v[110:113]
	v_mfma_f32_16x16x32_bf16 v[106:109], v[152:155], v[192:195], v[106:109]
	v_mfma_f32_16x16x32_bf16 v[94:97], v[144:147], v[200:203], v[94:97]
	v_mfma_f32_16x16x32_bf16 v[90:93], v[152:155], v[200:203], v[90:93]
	v_mfma_f32_16x16x32_bf16 v[78:81], v[144:147], v[208:211], v[78:81]
	v_mfma_f32_16x16x32_bf16 v[74:77], v[152:155], v[208:211], v[74:77]
	v_mfma_f32_16x16x32_bf16 v[126:129], v[148:151], v[188:191], v[126:129]
	v_mfma_f32_16x16x32_bf16 v[122:125], v[156:159], v[188:191], v[122:125]
	v_mfma_f32_16x16x32_bf16 v[110:113], v[148:151], v[196:199], v[110:113]
	v_mfma_f32_16x16x32_bf16 v[106:109], v[156:159], v[196:199], v[106:109]
	v_mfma_f32_16x16x32_bf16 v[94:97], v[148:151], v[204:207], v[94:97]
	v_mfma_f32_16x16x32_bf16 v[90:93], v[156:159], v[204:207], v[90:93]
	v_mfma_f32_16x16x32_bf16 v[78:81], v[148:151], v[212:215], v[78:81]
	v_mfma_f32_16x16x32_bf16 v[74:77], v[156:159], v[212:215], v[74:77]
	s_setprio 0
	s_setprio 1
	v_mfma_f32_16x16x32_bf16 v[118:121], v[160:163], v[184:187], v[118:121]
	v_mfma_f32_16x16x32_bf16 v[114:117], v[174:177], v[184:187], v[114:117]
	v_mfma_f32_16x16x32_bf16 v[102:105], v[160:163], v[192:195], v[102:105]
	v_mfma_f32_16x16x32_bf16 v[98:101], v[174:177], v[192:195], v[98:101]
	v_mfma_f32_16x16x32_bf16 v[86:89], v[160:163], v[200:203], v[86:89]
	v_mfma_f32_16x16x32_bf16 v[82:85], v[174:177], v[200:203], v[82:85]
	v_mfma_f32_16x16x32_bf16 v[70:73], v[160:163], v[208:211], v[70:73]
	v_mfma_f32_16x16x32_bf16 v[66:69], v[174:177], v[208:211], v[66:69]
	v_mfma_f32_16x16x32_bf16 v[118:121], v[170:173], v[188:191], v[118:121]
	v_mfma_f32_16x16x32_bf16 v[114:117], v[180:183], v[188:191], v[114:117]
	v_mfma_f32_16x16x32_bf16 v[102:105], v[170:173], v[196:199], v[102:105]
	v_mfma_f32_16x16x32_bf16 v[98:101], v[180:183], v[196:199], v[98:101]
	v_mfma_f32_16x16x32_bf16 v[86:89], v[170:173], v[204:207], v[86:89]
	v_mfma_f32_16x16x32_bf16 v[82:85], v[180:183], v[204:207], v[82:85]
	v_mfma_f32_16x16x32_bf16 v[70:73], v[170:173], v[212:215], v[70:73]
	v_mfma_f32_16x16x32_bf16 v[66:69], v[180:183], v[212:215], v[66:69]
	s_setprio 0
	s_barrier
	s_add_i32 s62, s74, s1
	v_lshl_add_u64 v[216:217], v[216:217], 0, s[56:57]
	s_mov_b32 m0, s62
	s_nop 0
	global_load_lds_dwordx4 v[216:217], off
	s_add_i32 m0, s62, 0x2000
	s_add_u32 s60, s60, 0x40080
	v_lshl_add_u64 v[216:217], v[218:219], 0, s[56:57]
	s_addc_u32 s61, s61, 0
	s_add_i32 s62, s75, s1
	global_load_lds_dwordx4 v[216:217], off
	v_lshl_add_u64 v[216:217], s[60:61], 0, v[130:131]
	s_mov_b32 m0, s62
	s_nop 0
	global_load_lds_dwordx4 v[216:217], off
	v_lshl_add_u64 v[216:217], s[60:61], 0, v[132:133]
	s_add_i32 m0, s62, 0x2000
	s_nop 0
	global_load_lds_dwordx4 v[216:217], off
	v_lshl_add_u64 v[216:217], v[220:221], 0, s[56:57]
	s_mov_b32 m0, s64
	s_nop 0
	global_load_lds_dwordx4 v[216:217], off
	v_lshl_add_u64 v[216:217], v[222:223], 0, s[56:57]
	s_mov_b32 m0, s65
	s_nop 0
	global_load_lds_dwordx4 v[216:217], off
	ds_read_b128 v[184:187], v178 offset:49152
	ds_read_b128 v[188:191], v178 offset:50176
	ds_read_b128 v[192:195], v178 offset:51200
	ds_read_b128 v[196:199], v178 offset:52224
	ds_read_b128 v[200:203], v178 offset:53248
	ds_read_b128 v[204:207], v178 offset:54272
	ds_read_b128 v[208:211], v178 offset:55296
	ds_read_b128 v[212:215], v178 offset:56320
	s_waitcnt vmcnt(8)
	s_waitcnt lgkmcnt(0)
	s_barrier
	s_setprio 1
	s_waitcnt lgkmcnt(0)
	v_mfma_f32_16x16x32_bf16 v[62:65], v[144:147], v[184:187], v[62:65]
	v_mfma_f32_16x16x32_bf16 v[58:61], v[152:155], v[184:187], v[58:61]
	v_mfma_f32_16x16x32_bf16 v[46:49], v[144:147], v[192:195], v[46:49]
	v_mfma_f32_16x16x32_bf16 v[42:45], v[152:155], v[192:195], v[42:45]
	v_mfma_f32_16x16x32_bf16 v[30:33], v[144:147], v[200:203], v[30:33]
	v_mfma_f32_16x16x32_bf16 v[26:29], v[152:155], v[200:203], v[26:29]
	v_mfma_f32_16x16x32_bf16 v[14:17], v[144:147], v[208:211], v[14:17]
	v_mfma_f32_16x16x32_bf16 v[10:13], v[152:155], v[208:211], v[10:13]
	v_mfma_f32_16x16x32_bf16 v[62:65], v[148:151], v[188:191], v[62:65]
	v_mfma_f32_16x16x32_bf16 v[58:61], v[156:159], v[188:191], v[58:61]
	v_mfma_f32_16x16x32_bf16 v[46:49], v[148:151], v[196:199], v[46:49]
	v_mfma_f32_16x16x32_bf16 v[42:45], v[156:159], v[196:199], v[42:45]
	v_mfma_f32_16x16x32_bf16 v[30:33], v[148:151], v[204:207], v[30:33]
	v_mfma_f32_16x16x32_bf16 v[26:29], v[156:159], v[204:207], v[26:29]
	v_mfma_f32_16x16x32_bf16 v[14:17], v[148:151], v[212:215], v[14:17]
	v_mfma_f32_16x16x32_bf16 v[10:13], v[156:159], v[212:215], v[10:13]
	s_setprio 0
	s_setprio 1
	v_mfma_f32_16x16x32_bf16 v[54:57], v[160:163], v[184:187], v[54:57]
	v_mfma_f32_16x16x32_bf16 v[50:53], v[174:177], v[184:187], v[50:53]
	v_mfma_f32_16x16x32_bf16 v[38:41], v[160:163], v[192:195], v[38:41]
	v_mfma_f32_16x16x32_bf16 v[34:37], v[174:177], v[192:195], v[34:37]
	v_mfma_f32_16x16x32_bf16 v[22:25], v[160:163], v[200:203], v[22:25]
	v_mfma_f32_16x16x32_bf16 v[18:21], v[174:177], v[200:203], v[18:21]
	v_mfma_f32_16x16x32_bf16 v[6:9], v[160:163], v[208:211], v[6:9]
	v_mfma_f32_16x16x32_bf16 v[2:5], v[174:177], v[208:211], v[2:5]
	v_mfma_f32_16x16x32_bf16 v[54:57], v[170:173], v[188:191], v[54:57]
	v_mfma_f32_16x16x32_bf16 v[50:53], v[180:183], v[188:191], v[50:53]
	v_mfma_f32_16x16x32_bf16 v[38:41], v[170:173], v[196:199], v[38:41]
	v_mfma_f32_16x16x32_bf16 v[34:37], v[180:183], v[196:199], v[34:37]
	v_mfma_f32_16x16x32_bf16 v[22:25], v[170:173], v[204:207], v[22:25]
	v_mfma_f32_16x16x32_bf16 v[18:21], v[180:183], v[204:207], v[18:21]
	v_mfma_f32_16x16x32_bf16 v[6:9], v[170:173], v[212:215], v[6:9]
	v_mfma_f32_16x16x32_bf16 v[2:5], v[180:183], v[212:215], v[2:5]
	s_setprio 0
	s_barrier
	s_add_u32 s71, s71, 0x100
	s_addc_u32 s72, s72, 0
	s_add_u32 s58, s58, 0x100
	s_addc_u32 s59, s59, 0
	s_cmp_ge_i32 s73, s0
	s_mov_b32 s60, s73
	s_cbranch_scc0 .LBB0_229
	s_mov_b64 s[72:73], 0xe800000
	v_mov_b32_e32 v209, v1
	s_and_b64 vcc, exec, s[34:35]
	s_cbranch_vccz .LBB0_232

.LBB0_298:
	s_add_i32 s71, s58, 2
	s_add_u32 s59, s54, 0xfffe0080
	s_addc_u32 s60, s55, -1
	s_add_i32 s72, 0, 0x10000
	s_cmp_eq_u32 s65, s58
	s_cselect_b32 s61, s39, s60
	s_cselect_b32 s60, s41, s59
	s_cselect_b32 s59, s43, s70
	s_cselect_b32 s58, s53, s69
	s_add_i32 s73, 0, 0x14000
	v_add_u32_e32 v2, s72, v198
	v_add_u32_e32 v6, s73, v198
	v_lshl_add_u64 v[170:171], s[54:55], 0, v[186:187]
	s_add_i32 m0, s8, 0xc000
	s_nop 0
	global_load_lds_dwordx4 v[170:171], off
	v_lshl_add_u64 v[170:171], s[54:55], 0, v[184:185]
	s_add_i32 m0, s8, 0xe000
	s_nop 0
	global_load_lds_dwordx4 v[170:171], off
	ds_read_b128 v[26:29], v2
	ds_read_b128 v[30:33], v2 offset:1024
	ds_read_b128 v[18:21], v2 offset:2048
	ds_read_b128 v[22:25], v2 offset:3072
	ds_read_b128 v[10:13], v6
	ds_read_b128 v[14:17], v6 offset:1024
	ds_read_b128 v[2:5], v6 offset:2048
	ds_read_b128 v[6:9], v6 offset:3072
	ds_read_b128 v[188:191], v200
	ds_read_b128 v[192:195], v200 offset:1024
	ds_read_b128 v[202:205], v200 offset:2048
	ds_read_b128 v[206:209], v200 offset:3072
	ds_read_b128 v[210:213], v200 offset:4096
	ds_read_b128 v[214:217], v200 offset:5120
	ds_read_b128 v[236:239], v200 offset:6144
	ds_read_b128 v[240:243], v200 offset:7168
	s_waitcnt vmcnt(8)
	s_waitcnt lgkmcnt(0)
	s_barrier
	s_setprio 1
	s_waitcnt lgkmcnt(0)
	v_mfma_scale_f32_16x16x128_f8f6f4 v[158:161], v[26:33], v[188:195], v[158:161], v196, v169 op_sel_hi:[0,0,0]
	v_mfma_scale_f32_16x16x128_f8f6f4 v[154:157], v[18:25], v[188:195], v[154:157], v196, v169 op_sel_hi:[0,0,0]
	v_mfma_scale_f32_16x16x128_f8f6f4 v[142:145], v[26:33], v[202:209], v[142:145], v196, v169 op_sel_hi:[0,0,0]
	v_mfma_scale_f32_16x16x128_f8f6f4 v[138:141], v[18:25], v[202:209], v[138:141], v196, v169 op_sel_hi:[0,0,0]
	v_mfma_scale_f32_16x16x128_f8f6f4 v[126:129], v[26:33], v[210:217], v[126:129], v196, v169 op_sel_hi:[0,0,0]
	v_mfma_scale_f32_16x16x128_f8f6f4 v[122:125], v[18:25], v[210:217], v[122:125], v196, v169 op_sel_hi:[0,0,0]
	v_mfma_scale_f32_16x16x128_f8f6f4 v[110:113], v[26:33], v[236:243], v[110:113], v196, v169 op_sel_hi:[0,0,0]
	v_mfma_scale_f32_16x16x128_f8f6f4 v[106:109], v[18:25], v[236:243], v[106:109], v196, v169 op_sel_hi:[0,0,0]
	s_setprio 0
	s_setprio 1
	v_mfma_scale_f32_16x16x128_f8f6f4 v[150:153], v[10:17], v[188:195], v[150:153], v196, v169 op_sel_hi:[0,0,0]
	v_mfma_scale_f32_16x16x128_f8f6f4 v[146:149], v[2:9], v[188:195], v[146:149], v196, v169 op_sel_hi:[0,0,0]
	v_mfma_scale_f32_16x16x128_f8f6f4 v[134:137], v[10:17], v[202:209], v[134:137], v196, v169 op_sel_hi:[0,0,0]
	v_mfma_scale_f32_16x16x128_f8f6f4 v[130:133], v[2:9], v[202:209], v[130:133], v196, v169 op_sel_hi:[0,0,0]
	v_mfma_scale_f32_16x16x128_f8f6f4 v[118:121], v[10:17], v[210:217], v[118:121], v196, v169 op_sel_hi:[0,0,0]
	v_mfma_scale_f32_16x16x128_f8f6f4 v[114:117], v[2:9], v[210:217], v[114:117], v196, v169 op_sel_hi:[0,0,0]
	v_mfma_scale_f32_16x16x128_f8f6f4 v[102:105], v[10:17], v[236:243], v[102:105], v196, v169 op_sel_hi:[0,0,0]
	v_mfma_scale_f32_16x16x128_f8f6f4 v[98:101], v[2:9], v[236:243], v[98:101], v196, v169 op_sel_hi:[0,0,0]
	s_setprio 0
	s_barrier
	s_add_i32 s72, s72, s1
	v_lshl_add_u64 v[188:189], s[58:59], 0, v[162:163]
	s_mov_b32 m0, s72
	s_nop 0
	global_load_lds_dwordx4 v[188:189], off
	s_add_i32 m0, s72, 0x2000
	s_add_u32 s74, s58, 0x20000
	v_lshl_add_u64 v[190:191], s[58:59], 0, v[164:165]
	s_addc_u32 s75, s59, 0
	s_add_i32 s72, s73, s1
	global_load_lds_dwordx4 v[190:191], off
	v_lshl_add_u64 v[170:171], s[74:75], 0, v[162:163]
	s_mov_b32 m0, s72
	v_lshl_add_u64 v[192:193], s[60:61], 0, v[178:179]
	global_load_lds_dwordx4 v[170:171], off
	v_lshl_add_u64 v[170:171], s[74:75], 0, v[164:165]
	s_add_i32 m0, s72, 0x2000
	v_lshl_add_u64 v[194:195], s[60:61], 0, v[180:181]
	global_load_lds_dwordx4 v[170:171], off
	s_mov_b32 m0, s8
	s_nop 0
	global_load_lds_dwordx4 v[192:193], off
	s_mov_b32 m0, s11
	s_nop 0
	global_load_lds_dwordx4 v[194:195], off
	ds_read_b128 v[202:205], v200 offset:16384
	ds_read_b128 v[206:209], v200 offset:17408
	ds_read_b128 v[210:213], v200 offset:18432
	ds_read_b128 v[214:217], v200 offset:19456
	ds_read_b128 v[236:239], v200 offset:20480
	ds_read_b128 v[240:243], v200 offset:21504
	ds_read_b128 v[244:247], v200 offset:22528
	ds_read_b128 v[248:251], v200 offset:23552
	s_waitcnt vmcnt(8)
	s_waitcnt lgkmcnt(0)
	s_barrier
	s_setprio 1
	s_waitcnt lgkmcnt(0)
	v_mfma_scale_f32_16x16x128_f8f6f4 v[94:97], v[26:33], v[202:209], v[94:97], v196, v169 op_sel_hi:[0,0,0]
	v_mfma_scale_f32_16x16x128_f8f6f4 v[90:93], v[18:25], v[202:209], v[90:93], v196, v169 op_sel_hi:[0,0,0]
	v_mfma_scale_f32_16x16x128_f8f6f4 v[78:81], v[26:33], v[210:217], v[78:81], v196, v169 op_sel_hi:[0,0,0]
	v_mfma_scale_f32_16x16x128_f8f6f4 v[74:77], v[18:25], v[210:217], v[74:77], v196, v169 op_sel_hi:[0,0,0]
	v_mfma_scale_f32_16x16x128_f8f6f4 v[62:65], v[26:33], v[236:243], v[62:65], v196, v169 op_sel_hi:[0,0,0]
	v_mfma_scale_f32_16x16x128_f8f6f4 v[58:61], v[18:25], v[236:243], v[58:61], v196, v169 op_sel_hi:[0,0,0]
	v_mfma_scale_f32_16x16x128_f8f6f4 v[46:49], v[26:33], v[244:251], v[46:49], v196, v169 op_sel_hi:[0,0,0]
	v_mfma_scale_f32_16x16x128_f8f6f4 v[42:45], v[18:25], v[244:251], v[42:45], v196, v169 op_sel_hi:[0,0,0]
	s_setprio 0
	s_setprio 1
	v_mfma_scale_f32_16x16x128_f8f6f4 v[86:89], v[10:17], v[202:209], v[86:89], v196, v169 op_sel_hi:[0,0,0]
	v_mfma_scale_f32_16x16x128_f8f6f4 v[82:85], v[2:9], v[202:209], v[82:85], v196, v169 op_sel_hi:[0,0,0]
	v_mfma_scale_f32_16x16x128_f8f6f4 v[70:73], v[10:17], v[210:217], v[70:73], v196, v169 op_sel_hi:[0,0,0]
	v_mfma_scale_f32_16x16x128_f8f6f4 v[66:69], v[2:9], v[210:217], v[66:69], v196, v169 op_sel_hi:[0,0,0]
	v_mfma_scale_f32_16x16x128_f8f6f4 v[54:57], v[10:17], v[236:243], v[54:57], v196, v169 op_sel_hi:[0,0,0]
	v_mfma_scale_f32_16x16x128_f8f6f4 v[50:53], v[2:9], v[236:243], v[50:53], v196, v169 op_sel_hi:[0,0,0]
	v_mfma_scale_f32_16x16x128_f8f6f4 v[38:41], v[10:17], v[244:251], v[38:41], v196, v169 op_sel_hi:[0,0,0]
	v_mfma_scale_f32_16x16x128_f8f6f4 v[34:37], v[2:9], v[244:251], v[34:37], v196, v169 op_sel_hi:[0,0,0]
	s_setprio 0
	s_barrier
	s_add_i32 s72, 0, 0x18000
	s_add_i32 s73, 0, 0x1c000
	v_add_u32_e32 v2, s72, v198
	v_add_u32_e32 v6, s73, v198
	s_add_u32 s60, s60, 0x20000
	s_addc_u32 s61, s61, 0
	s_mov_b32 m0, s16
	v_lshl_add_u64 v[170:171], s[60:61], 0, v[178:179]
	global_load_lds_dwordx4 v[170:171], off
	v_lshl_add_u64 v[170:171], s[60:61], 0, v[180:181]
	s_mov_b32 m0, s25
	s_nop 0
	global_load_lds_dwordx4 v[170:171], off
	ds_read_b128 v[26:29], v2
	ds_read_b128 v[30:33], v2 offset:1024
	ds_read_b128 v[18:21], v2 offset:2048
	ds_read_b128 v[22:25], v2 offset:3072
	ds_read_b128 v[10:13], v6
	ds_read_b128 v[14:17], v6 offset:1024
	ds_read_b128 v[2:5], v6 offset:2048
	ds_read_b128 v[6:9], v6 offset:3072
	ds_read_b128 v[202:205], v200 offset:32768
	ds_read_b128 v[206:209], v200 offset:33792
	ds_read_b128 v[210:213], v200 offset:34816
	ds_read_b128 v[214:217], v200 offset:35840
	ds_read_b128 v[236:239], v200 offset:36864
	ds_read_b128 v[240:243], v200 offset:37888
	ds_read_b128 v[244:247], v200 offset:38912
	ds_read_b128 v[248:251], v200 offset:39936
	s_waitcnt vmcnt(8)
	s_waitcnt lgkmcnt(0)
	s_barrier
	s_setprio 1
	s_waitcnt lgkmcnt(0)
	v_mfma_scale_f32_16x16x128_f8f6f4 v[158:161], v[26:33], v[202:209], v[158:161], v196, v169 op_sel_hi:[0,0,0]
	v_mfma_scale_f32_16x16x128_f8f6f4 v[154:157], v[18:25], v[202:209], v[154:157], v196, v169 op_sel_hi:[0,0,0]
	v_mfma_scale_f32_16x16x128_f8f6f4 v[142:145], v[26:33], v[210:217], v[142:145], v196, v169 op_sel_hi:[0,0,0]
	v_mfma_scale_f32_16x16x128_f8f6f4 v[138:141], v[18:25], v[210:217], v[138:141], v196, v169 op_sel_hi:[0,0,0]
	v_mfma_scale_f32_16x16x128_f8f6f4 v[126:129], v[26:33], v[236:243], v[126:129], v196, v169 op_sel_hi:[0,0,0]
	v_mfma_scale_f32_16x16x128_f8f6f4 v[122:125], v[18:25], v[236:243], v[122:125], v196, v169 op_sel_hi:[0,0,0]
	v_mfma_scale_f32_16x16x128_f8f6f4 v[110:113], v[26:33], v[244:251], v[110:113], v196, v169 op_sel_hi:[0,0,0]
	v_mfma_scale_f32_16x16x128_f8f6f4 v[106:109], v[18:25], v[244:251], v[106:109], v196, v169 op_sel_hi:[0,0,0]
	s_setprio 0
	s_setprio 1
	v_mfma_scale_f32_16x16x128_f8f6f4 v[150:153], v[10:17], v[202:209], v[150:153], v196, v169 op_sel_hi:[0,0,0]
	v_mfma_scale_f32_16x16x128_f8f6f4 v[146:149], v[2:9], v[202:209], v[146:149], v196, v169 op_sel_hi:[0,0,0]
	v_mfma_scale_f32_16x16x128_f8f6f4 v[134:137], v[10:17], v[210:217], v[134:137], v196, v169 op_sel_hi:[0,0,0]
	v_mfma_scale_f32_16x16x128_f8f6f4 v[130:133], v[2:9], v[210:217], v[130:133], v196, v169 op_sel_hi:[0,0,0]
	v_mfma_scale_f32_16x16x128_f8f6f4 v[118:121], v[10:17], v[236:243], v[118:121], v196, v169 op_sel_hi:[0,0,0]
	v_mfma_scale_f32_16x16x128_f8f6f4 v[114:117], v[2:9], v[236:243], v[114:117], v196, v169 op_sel_hi:[0,0,0]
	v_mfma_scale_f32_16x16x128_f8f6f4 v[102:105], v[10:17], v[244:251], v[102:105], v196, v169 op_sel_hi:[0,0,0]
	v_mfma_scale_f32_16x16x128_f8f6f4 v[98:101], v[2:9], v[244:251], v[98:101], v196, v169 op_sel_hi:[0,0,0]
	s_setprio 0
	s_barrier
	s_add_i32 s60, s72, s1
	v_lshl_add_u64 v[170:171], v[188:189], 0, s[56:57]
	s_mov_b32 m0, s60
	s_nop 0
	global_load_lds_dwordx4 v[170:171], off
	s_add_i32 m0, s60, 0x2000
	s_add_u32 s58, s58, 0x20080
	v_lshl_add_u64 v[170:171], v[190:191], 0, s[56:57]
	s_addc_u32 s59, s59, 0
	s_add_i32 s60, s73, s1
	global_load_lds_dwordx4 v[170:171], off
	v_lshl_add_u64 v[170:171], s[58:59], 0, v[162:163]
	s_mov_b32 m0, s60
	s_nop 0
	global_load_lds_dwordx4 v[170:171], off
	v_lshl_add_u64 v[170:171], s[58:59], 0, v[164:165]
	s_add_i32 m0, s60, 0x2000
	s_nop 0
	global_load_lds_dwordx4 v[170:171], off
	v_lshl_add_u64 v[170:171], v[192:193], 0, s[56:57]
	s_mov_b32 m0, s62
	s_nop 0
	global_load_lds_dwordx4 v[170:171], off
	v_lshl_add_u64 v[170:171], v[194:195], 0, s[56:57]
	s_mov_b32 m0, s63
	s_nop 0
	global_load_lds_dwordx4 v[170:171], off
	ds_read_b128 v[202:205], v200 offset:49152
	ds_read_b128 v[206:209], v200 offset:50176
	ds_read_b128 v[210:213], v200 offset:51200
	ds_read_b128 v[214:217], v200 offset:52224
	ds_read_b128 v[236:239], v200 offset:53248
	ds_read_b128 v[240:243], v200 offset:54272
	ds_read_b128 v[244:247], v200 offset:55296
	ds_read_b128 v[248:251], v200 offset:56320
	s_waitcnt vmcnt(8)
	s_waitcnt lgkmcnt(0)
	s_barrier
	s_setprio 1
	s_waitcnt lgkmcnt(0)
	v_mfma_scale_f32_16x16x128_f8f6f4 v[94:97], v[26:33], v[202:209], v[94:97], v196, v169 op_sel_hi:[0,0,0]
	v_mfma_scale_f32_16x16x128_f8f6f4 v[90:93], v[18:25], v[202:209], v[90:93], v196, v169 op_sel_hi:[0,0,0]
	v_mfma_scale_f32_16x16x128_f8f6f4 v[78:81], v[26:33], v[210:217], v[78:81], v196, v169 op_sel_hi:[0,0,0]
	v_mfma_scale_f32_16x16x128_f8f6f4 v[74:77], v[18:25], v[210:217], v[74:77], v196, v169 op_sel_hi:[0,0,0]
	v_mfma_scale_f32_16x16x128_f8f6f4 v[62:65], v[26:33], v[236:243], v[62:65], v196, v169 op_sel_hi:[0,0,0]
	v_mfma_scale_f32_16x16x128_f8f6f4 v[58:61], v[18:25], v[236:243], v[58:61], v196, v169 op_sel_hi:[0,0,0]
	v_mfma_scale_f32_16x16x128_f8f6f4 v[46:49], v[26:33], v[244:251], v[46:49], v196, v169 op_sel_hi:[0,0,0]
	v_mfma_scale_f32_16x16x128_f8f6f4 v[42:45], v[18:25], v[244:251], v[42:45], v196, v169 op_sel_hi:[0,0,0]
	s_setprio 0
	s_setprio 1
	v_mfma_scale_f32_16x16x128_f8f6f4 v[86:89], v[10:17], v[202:209], v[86:89], v196, v169 op_sel_hi:[0,0,0]
	v_mfma_scale_f32_16x16x128_f8f6f4 v[82:85], v[2:9], v[202:209], v[82:85], v196, v169 op_sel_hi:[0,0,0]
	v_mfma_scale_f32_16x16x128_f8f6f4 v[70:73], v[10:17], v[210:217], v[70:73], v196, v169 op_sel_hi:[0,0,0]
	v_mfma_scale_f32_16x16x128_f8f6f4 v[66:69], v[2:9], v[210:217], v[66:69], v196, v169 op_sel_hi:[0,0,0]
	v_mfma_scale_f32_16x16x128_f8f6f4 v[54:57], v[10:17], v[236:243], v[54:57], v196, v169 op_sel_hi:[0,0,0]
	v_mfma_scale_f32_16x16x128_f8f6f4 v[50:53], v[2:9], v[236:243], v[50:53], v196, v169 op_sel_hi:[0,0,0]
	v_mfma_scale_f32_16x16x128_f8f6f4 v[38:41], v[10:17], v[244:251], v[38:41], v196, v169 op_sel_hi:[0,0,0]
	v_mfma_scale_f32_16x16x128_f8f6f4 v[34:37], v[2:9], v[244:251], v[34:37], v196, v169 op_sel_hi:[0,0,0]
	s_setprio 0
	s_barrier
	s_add_u32 s69, s69, 0x100
	s_addc_u32 s70, s70, 0
	s_add_u32 s54, s54, 0x100
	s_addc_u32 s55, s55, 0
	s_cmp_ge_i32 s71, s0
	s_mov_b32 s58, s71
	s_cbranch_scc0 .LBB0_298
	s_mov_b64 s[72:73], 0xe800000
	s_mov_b64 s[70:71], 0xe800800
	v_mov_b32_e32 v209, v1
	s_and_b64 vcc, exec, s[34:35]
	s_cbranch_vccz .LBB0_301

.LBB0_469:
	s_add_i32 s73, s68, 2
	s_add_u32 s69, s64, 0xfffc0080
	s_addc_u32 s70, s65, -1
	s_add_i32 s74, 0, 0x10000
	s_cmp_eq_u32 s24, s68
	s_cselect_b32 s71, s59, s70
	s_cselect_b32 s70, s58, s69
	s_cselect_b32 s69, s51, s72
	s_cselect_b32 s68, s53, s66
	s_add_i32 s76, 0, 0x14000
	v_add_u32_e32 v152, s74, v220
	v_add_u32_e32 v164, s76, v220
	ds_read_b128 v[106:109], v152
	ds_read_b128 v[110:113], v152 offset:1024
	ds_read_b128 v[114:117], v152 offset:2048
	ds_read_b128 v[152:155], v152 offset:3072
	ds_read_b128 v[156:159], v164
	ds_read_b128 v[160:163], v164 offset:1024
	ds_read_b128 v[170:173], v164 offset:2048
	ds_read_b128 v[174:177], v164 offset:3072
	v_lshl_add_u64 v[164:165], s[64:65], 0, v[150:151]
	s_add_i32 m0, s14, 0xc000
	ds_read_b128 v[178:181], v222
	ds_read_b128 v[182:185], v222 offset:1024
	ds_read_b128 v[186:189], v222 offset:2048
	ds_read_b128 v[190:193], v222 offset:3072
	ds_read_b128 v[194:197], v222 offset:4096
	ds_read_b128 v[198:201], v222 offset:5120
	ds_read_b128 v[202:205], v222 offset:6144
	ds_read_b128 v[206:209], v222 offset:7168
	global_load_lds_dwordx4 v[164:165], off
	v_lshl_add_u64 v[164:165], s[64:65], 0, v[148:149]
	s_add_i32 m0, s14, 0xe000
	s_nop 0
	global_load_lds_dwordx4 v[164:165], off
	s_waitcnt vmcnt(8)
	s_waitcnt lgkmcnt(0)
	s_barrier
	s_setprio 1
	s_waitcnt lgkmcnt(0)
	v_mfma_f32_16x16x32_bf16 v[138:141], v[106:109], v[178:181], v[138:141]
	v_mfma_f32_16x16x32_bf16 v[62:65], v[114:117], v[178:181], v[62:65]
	v_mfma_f32_16x16x32_bf16 v[130:133], v[106:109], v[186:189], v[130:133]
	v_mfma_f32_16x16x32_bf16 v[54:57], v[114:117], v[186:189], v[54:57]
	v_mfma_f32_16x16x32_bf16 v[122:125], v[106:109], v[194:197], v[122:125]
	v_mfma_f32_16x16x32_bf16 v[46:49], v[114:117], v[194:197], v[46:49]
	v_mfma_f32_16x16x32_bf16 v[102:105], v[106:109], v[202:205], v[102:105]
	v_mfma_f32_16x16x32_bf16 v[38:41], v[114:117], v[202:205], v[38:41]
	v_mfma_f32_16x16x32_bf16 v[138:141], v[110:113], v[182:185], v[138:141]
	v_mfma_f32_16x16x32_bf16 v[62:65], v[152:155], v[182:185], v[62:65]
	v_mfma_f32_16x16x32_bf16 v[130:133], v[110:113], v[190:193], v[130:133]
	v_mfma_f32_16x16x32_bf16 v[54:57], v[152:155], v[190:193], v[54:57]
	v_mfma_f32_16x16x32_bf16 v[122:125], v[110:113], v[198:201], v[122:125]
	v_mfma_f32_16x16x32_bf16 v[46:49], v[152:155], v[198:201], v[46:49]
	v_mfma_f32_16x16x32_bf16 v[102:105], v[110:113], v[206:209], v[102:105]
	v_mfma_f32_16x16x32_bf16 v[38:41], v[152:155], v[206:209], v[38:41]
	s_setprio 0
	s_setprio 1
	v_mfma_f32_16x16x32_bf16 v[134:137], v[156:159], v[178:181], v[134:137]
	v_mfma_f32_16x16x32_bf16 v[58:61], v[170:173], v[178:181], v[58:61]
	v_mfma_f32_16x16x32_bf16 v[126:129], v[156:159], v[186:189], v[126:129]
	v_mfma_f32_16x16x32_bf16 v[50:53], v[170:173], v[186:189], v[50:53]
	v_mfma_f32_16x16x32_bf16 v[118:121], v[156:159], v[194:197], v[118:121]
	v_mfma_f32_16x16x32_bf16 v[42:45], v[170:173], v[194:197], v[42:45]
	v_mfma_f32_16x16x32_bf16 v[98:101], v[156:159], v[202:205], v[98:101]
	v_mfma_f32_16x16x32_bf16 v[34:37], v[170:173], v[202:205], v[34:37]
	v_mfma_f32_16x16x32_bf16 v[134:137], v[160:163], v[182:185], v[134:137]
	v_mfma_f32_16x16x32_bf16 v[58:61], v[174:177], v[182:185], v[58:61]
	v_mfma_f32_16x16x32_bf16 v[126:129], v[160:163], v[190:193], v[126:129]
	v_mfma_f32_16x16x32_bf16 v[50:53], v[174:177], v[190:193], v[50:53]
	v_mfma_f32_16x16x32_bf16 v[118:121], v[160:163], v[198:201], v[118:121]
	v_mfma_f32_16x16x32_bf16 v[42:45], v[174:177], v[198:201], v[42:45]
	v_mfma_f32_16x16x32_bf16 v[98:101], v[160:163], v[206:209], v[98:101]
	v_mfma_f32_16x16x32_bf16 v[34:37], v[174:177], v[206:209], v[34:37]
	s_setprio 0
	s_barrier
	s_add_i32 s74, s74, s13
	v_lshl_add_u64 v[164:165], s[68:69], 0, v[166:167]
	s_mov_b32 m0, s74
	s_nop 0
	global_load_lds_dwordx4 v[164:165], off
	s_add_i32 m0, s74, 0x2000
	s_add_u32 s74, s68, 0x8000
	v_lshl_add_u64 v[210:211], s[68:69], 0, v[142:143]
	s_addc_u32 s75, s69, 0
	s_add_i32 s76, s76, s13
	global_load_lds_dwordx4 v[210:211], off
	v_lshl_add_u64 v[212:213], s[74:75], 0, v[166:167]
	s_mov_b32 m0, s76
	v_lshl_add_u64 v[214:215], s[70:71], 0, v[146:147]
	global_load_lds_dwordx4 v[212:213], off
	v_lshl_add_u64 v[212:213], s[74:75], 0, v[142:143]
	s_add_i32 m0, s76, 0x2000
	s_nop 0
	global_load_lds_dwordx4 v[212:213], off
	v_lshl_add_u64 v[212:213], s[70:71], 0, v[144:145]
	s_mov_b32 m0, s14
	s_nop 0
	global_load_lds_dwordx4 v[212:213], off
	s_mov_b32 m0, s15
	s_nop 0
	global_load_lds_dwordx4 v[214:215], off
	ds_read_b128 v[178:181], v222 offset:16384
	ds_read_b128 v[182:185], v222 offset:17408
	ds_read_b128 v[186:189], v222 offset:18432
	ds_read_b128 v[190:193], v222 offset:19456
	ds_read_b128 v[194:197], v222 offset:20480
	ds_read_b128 v[198:201], v222 offset:21504
	ds_read_b128 v[202:205], v222 offset:22528
	ds_read_b128 v[206:209], v222 offset:23552
	s_waitcnt vmcnt(8)
	s_waitcnt lgkmcnt(0)
	s_barrier
	s_setprio 1
	s_waitcnt lgkmcnt(0)
	v_mfma_f32_16x16x32_bf16 v[94:97], v[106:109], v[178:181], v[94:97]
	v_mfma_f32_16x16x32_bf16 v[30:33], v[114:117], v[178:181], v[30:33]
	v_mfma_f32_16x16x32_bf16 v[86:89], v[106:109], v[186:189], v[86:89]
	v_mfma_f32_16x16x32_bf16 v[22:25], v[114:117], v[186:189], v[22:25]
	v_mfma_f32_16x16x32_bf16 v[78:81], v[106:109], v[194:197], v[78:81]
	v_mfma_f32_16x16x32_bf16 v[14:17], v[114:117], v[194:197], v[14:17]
	v_mfma_f32_16x16x32_bf16 v[70:73], v[106:109], v[202:205], v[70:73]
	v_mfma_f32_16x16x32_bf16 v[6:9], v[114:117], v[202:205], v[6:9]
	v_mfma_f32_16x16x32_bf16 v[94:97], v[110:113], v[182:185], v[94:97]
	v_mfma_f32_16x16x32_bf16 v[30:33], v[152:155], v[182:185], v[30:33]
	v_mfma_f32_16x16x32_bf16 v[86:89], v[110:113], v[190:193], v[86:89]
	v_mfma_f32_16x16x32_bf16 v[22:25], v[152:155], v[190:193], v[22:25]
	v_mfma_f32_16x16x32_bf16 v[78:81], v[110:113], v[198:201], v[78:81]
	v_mfma_f32_16x16x32_bf16 v[14:17], v[152:155], v[198:201], v[14:17]
	v_mfma_f32_16x16x32_bf16 v[70:73], v[110:113], v[206:209], v[70:73]
	v_mfma_f32_16x16x32_bf16 v[6:9], v[152:155], v[206:209], v[6:9]
	s_setprio 0
	s_setprio 1
	v_mfma_f32_16x16x32_bf16 v[90:93], v[156:159], v[178:181], v[90:93]
	v_mfma_f32_16x16x32_bf16 v[26:29], v[170:173], v[178:181], v[26:29]
	v_mfma_f32_16x16x32_bf16 v[82:85], v[156:159], v[186:189], v[82:85]
	v_mfma_f32_16x16x32_bf16 v[18:21], v[170:173], v[186:189], v[18:21]
	v_mfma_f32_16x16x32_bf16 v[74:77], v[156:159], v[194:197], v[74:77]
	v_mfma_f32_16x16x32_bf16 v[10:13], v[170:173], v[194:197], v[10:13]
	v_mfma_f32_16x16x32_bf16 v[66:69], v[156:159], v[202:205], v[66:69]
	v_mfma_f32_16x16x32_bf16 v[2:5], v[170:173], v[202:205], v[2:5]
	v_mfma_f32_16x16x32_bf16 v[90:93], v[160:163], v[182:185], v[90:93]
	v_mfma_f32_16x16x32_bf16 v[26:29], v[174:177], v[182:185], v[26:29]
	v_mfma_f32_16x16x32_bf16 v[82:85], v[160:163], v[190:193], v[82:85]
	v_mfma_f32_16x16x32_bf16 v[18:21], v[174:177], v[190:193], v[18:21]
	v_mfma_f32_16x16x32_bf16 v[74:77], v[160:163], v[198:201], v[74:77]
	v_mfma_f32_16x16x32_bf16 v[10:13], v[174:177], v[198:201], v[10:13]
	v_mfma_f32_16x16x32_bf16 v[66:69], v[160:163], v[206:209], v[66:69]
	v_mfma_f32_16x16x32_bf16 v[2:5], v[174:177], v[206:209], v[2:5]
	s_setprio 0
	s_barrier
	s_add_i32 s74, 0, 0x18000
	s_add_i32 s75, 0, 0x1c000
	v_add_u32_e32 v152, s74, v220
	v_add_u32_e32 v174, s75, v220
	s_add_u32 s70, s70, 0x40000
	s_addc_u32 s71, s71, 0
	s_mov_b32 m0, s16
	v_lshl_add_u64 v[216:217], s[70:71], 0, v[144:145]
	global_load_lds_dwordx4 v[216:217], off
	v_lshl_add_u64 v[216:217], s[70:71], 0, v[146:147]
	s_mov_b32 m0, s20
	s_nop 0
	global_load_lds_dwordx4 v[216:217], off
	ds_read_b128 v[106:109], v152
	ds_read_b128 v[110:113], v152 offset:1024
	ds_read_b128 v[114:117], v152 offset:2048
	ds_read_b128 v[152:155], v152 offset:3072
	ds_read_b128 v[156:159], v174
	ds_read_b128 v[160:163], v174 offset:1024
	ds_read_b128 v[170:173], v174 offset:2048
	ds_read_b128 v[174:177], v174 offset:3072
	ds_read_b128 v[178:181], v222 offset:32768
	ds_read_b128 v[182:185], v222 offset:33792
	ds_read_b128 v[186:189], v222 offset:34816
	ds_read_b128 v[190:193], v222 offset:35840
	ds_read_b128 v[194:197], v222 offset:36864
	ds_read_b128 v[198:201], v222 offset:37888
	ds_read_b128 v[202:205], v222 offset:38912
	ds_read_b128 v[206:209], v222 offset:39936
	s_waitcnt vmcnt(8)
	s_waitcnt lgkmcnt(0)
	s_barrier
	s_setprio 1
	s_waitcnt lgkmcnt(0)
	v_mfma_f32_16x16x32_bf16 v[138:141], v[106:109], v[178:181], v[138:141]
	v_mfma_f32_16x16x32_bf16 v[62:65], v[114:117], v[178:181], v[62:65]
	v_mfma_f32_16x16x32_bf16 v[130:133], v[106:109], v[186:189], v[130:133]
	v_mfma_f32_16x16x32_bf16 v[54:57], v[114:117], v[186:189], v[54:57]
	v_mfma_f32_16x16x32_bf16 v[122:125], v[106:109], v[194:197], v[122:125]
	v_mfma_f32_16x16x32_bf16 v[46:49], v[114:117], v[194:197], v[46:49]
	v_mfma_f32_16x16x32_bf16 v[102:105], v[106:109], v[202:205], v[102:105]
	v_mfma_f32_16x16x32_bf16 v[38:41], v[114:117], v[202:205], v[38:41]
	v_mfma_f32_16x16x32_bf16 v[138:141], v[110:113], v[182:185], v[138:141]
	v_mfma_f32_16x16x32_bf16 v[62:65], v[152:155], v[182:185], v[62:65]
	v_mfma_f32_16x16x32_bf16 v[130:133], v[110:113], v[190:193], v[130:133]
	v_mfma_f32_16x16x32_bf16 v[54:57], v[152:155], v[190:193], v[54:57]
	v_mfma_f32_16x16x32_bf16 v[122:125], v[110:113], v[198:201], v[122:125]
	v_mfma_f32_16x16x32_bf16 v[46:49], v[152:155], v[198:201], v[46:49]
	v_mfma_f32_16x16x32_bf16 v[102:105], v[110:113], v[206:209], v[102:105]
	v_mfma_f32_16x16x32_bf16 v[38:41], v[152:155], v[206:209], v[38:41]
	s_setprio 0
	s_setprio 1
	v_mfma_f32_16x16x32_bf16 v[134:137], v[156:159], v[178:181], v[134:137]
	v_mfma_f32_16x16x32_bf16 v[58:61], v[170:173], v[178:181], v[58:61]
	v_mfma_f32_16x16x32_bf16 v[126:129], v[156:159], v[186:189], v[126:129]
	v_mfma_f32_16x16x32_bf16 v[50:53], v[170:173], v[186:189], v[50:53]
	v_mfma_f32_16x16x32_bf16 v[118:121], v[156:159], v[194:197], v[118:121]
	v_mfma_f32_16x16x32_bf16 v[42:45], v[170:173], v[194:197], v[42:45]
	v_mfma_f32_16x16x32_bf16 v[98:101], v[156:159], v[202:205], v[98:101]
	v_mfma_f32_16x16x32_bf16 v[34:37], v[170:173], v[202:205], v[34:37]
	v_mfma_f32_16x16x32_bf16 v[134:137], v[160:163], v[182:185], v[134:137]
	v_mfma_f32_16x16x32_bf16 v[58:61], v[174:177], v[182:185], v[58:61]
	v_mfma_f32_16x16x32_bf16 v[126:129], v[160:163], v[190:193], v[126:129]
	v_mfma_f32_16x16x32_bf16 v[50:53], v[174:177], v[190:193], v[50:53]
	v_mfma_f32_16x16x32_bf16 v[118:121], v[160:163], v[198:201], v[118:121]
	v_mfma_f32_16x16x32_bf16 v[42:45], v[174:177], v[198:201], v[42:45]
	v_mfma_f32_16x16x32_bf16 v[98:101], v[160:163], v[206:209], v[98:101]
	v_mfma_f32_16x16x32_bf16 v[34:37], v[174:177], v[206:209], v[34:37]
	s_setprio 0
	s_barrier
	s_add_i32 s70, s74, s13
	v_lshl_add_u64 v[164:165], v[164:165], 0, s[56:57]
	s_mov_b32 m0, s70
	s_nop 0
	global_load_lds_dwordx4 v[164:165], off
	s_add_i32 m0, s70, 0x2000
	s_add_u32 s68, s68, 0x8080
	v_lshl_add_u64 v[164:165], v[210:211], 0, s[56:57]
	s_addc_u32 s69, s69, 0
	s_add_i32 s70, s75, s13
	global_load_lds_dwordx4 v[164:165], off
	v_lshl_add_u64 v[164:165], s[68:69], 0, v[166:167]
	s_mov_b32 m0, s70
	s_nop 0
	global_load_lds_dwordx4 v[164:165], off
	v_lshl_add_u64 v[164:165], s[68:69], 0, v[142:143]
	s_add_i32 m0, s70, 0x2000
	s_nop 0
	global_load_lds_dwordx4 v[164:165], off
	v_lshl_add_u64 v[164:165], v[212:213], 0, s[56:57]
	s_mov_b32 m0, s21
	s_nop 0
	global_load_lds_dwordx4 v[164:165], off
	v_lshl_add_u64 v[164:165], v[214:215], 0, s[56:57]
	s_mov_b32 m0, s22
	s_nop 0
	global_load_lds_dwordx4 v[164:165], off
	ds_read_b128 v[178:181], v222 offset:49152
	ds_read_b128 v[182:185], v222 offset:50176
	ds_read_b128 v[186:189], v222 offset:51200
	ds_read_b128 v[190:193], v222 offset:52224
	ds_read_b128 v[194:197], v222 offset:53248
	ds_read_b128 v[198:201], v222 offset:54272
	ds_read_b128 v[202:205], v222 offset:55296
	ds_read_b128 v[206:209], v222 offset:56320
	s_waitcnt vmcnt(8)
	s_waitcnt lgkmcnt(0)
	s_barrier
	s_setprio 1
	s_waitcnt lgkmcnt(0)
	v_mfma_f32_16x16x32_bf16 v[94:97], v[106:109], v[178:181], v[94:97]
	v_mfma_f32_16x16x32_bf16 v[30:33], v[114:117], v[178:181], v[30:33]
	v_mfma_f32_16x16x32_bf16 v[86:89], v[106:109], v[186:189], v[86:89]
	v_mfma_f32_16x16x32_bf16 v[22:25], v[114:117], v[186:189], v[22:25]
	v_mfma_f32_16x16x32_bf16 v[78:81], v[106:109], v[194:197], v[78:81]
	v_mfma_f32_16x16x32_bf16 v[14:17], v[114:117], v[194:197], v[14:17]
	v_mfma_f32_16x16x32_bf16 v[70:73], v[106:109], v[202:205], v[70:73]
	v_mfma_f32_16x16x32_bf16 v[6:9], v[114:117], v[202:205], v[6:9]
	v_mfma_f32_16x16x32_bf16 v[94:97], v[110:113], v[182:185], v[94:97]
	v_mfma_f32_16x16x32_bf16 v[30:33], v[152:155], v[182:185], v[30:33]
	v_mfma_f32_16x16x32_bf16 v[86:89], v[110:113], v[190:193], v[86:89]
	v_mfma_f32_16x16x32_bf16 v[22:25], v[152:155], v[190:193], v[22:25]
	v_mfma_f32_16x16x32_bf16 v[78:81], v[110:113], v[198:201], v[78:81]
	v_mfma_f32_16x16x32_bf16 v[14:17], v[152:155], v[198:201], v[14:17]
	v_mfma_f32_16x16x32_bf16 v[70:73], v[110:113], v[206:209], v[70:73]
	v_mfma_f32_16x16x32_bf16 v[6:9], v[152:155], v[206:209], v[6:9]
	s_setprio 0
	s_setprio 1
	v_mfma_f32_16x16x32_bf16 v[90:93], v[156:159], v[178:181], v[90:93]
	v_mfma_f32_16x16x32_bf16 v[26:29], v[170:173], v[178:181], v[26:29]
	v_mfma_f32_16x16x32_bf16 v[82:85], v[156:159], v[186:189], v[82:85]
	v_mfma_f32_16x16x32_bf16 v[18:21], v[170:173], v[186:189], v[18:21]
	v_mfma_f32_16x16x32_bf16 v[74:77], v[156:159], v[194:197], v[74:77]
	v_mfma_f32_16x16x32_bf16 v[10:13], v[170:173], v[194:197], v[10:13]
	v_mfma_f32_16x16x32_bf16 v[66:69], v[156:159], v[202:205], v[66:69]
	v_mfma_f32_16x16x32_bf16 v[2:5], v[170:173], v[202:205], v[2:5]
	v_mfma_f32_16x16x32_bf16 v[90:93], v[160:163], v[182:185], v[90:93]
	v_mfma_f32_16x16x32_bf16 v[26:29], v[174:177], v[182:185], v[26:29]
	v_mfma_f32_16x16x32_bf16 v[82:85], v[160:163], v[190:193], v[82:85]
	v_mfma_f32_16x16x32_bf16 v[18:21], v[174:177], v[190:193], v[18:21]
	v_mfma_f32_16x16x32_bf16 v[74:77], v[160:163], v[198:201], v[74:77]
	v_mfma_f32_16x16x32_bf16 v[10:13], v[174:177], v[198:201], v[10:13]
	v_mfma_f32_16x16x32_bf16 v[66:69], v[160:163], v[206:209], v[66:69]
	v_mfma_f32_16x16x32_bf16 v[2:5], v[174:177], v[206:209], v[2:5]
	s_setprio 0
	s_barrier
	s_add_u32 s66, s66, 0x100
	s_addc_u32 s72, s72, 0
	s_add_u32 s64, s64, 0x100
	s_addc_u32 s65, s65, 0
	s_cmp_ge_i32 s73, s1
	s_mov_b32 s68, s73
	s_cbranch_scc0 .LBB0_469
	s_branch .LBB0_471

.LBB0_664:
	s_add_i32 s84, s68, 2
	s_add_u32 s69, s74, 0xfffc0080
	s_addc_u32 s70, s75, -1
	s_add_i32 s88, 0, 0x10000
	s_cmp_eq_u32 s72, s68
	s_cselect_b32 s71, s29, s70
	s_cselect_b32 s70, s43, s69
	s_cselect_b32 s69, s55, s79
	s_cselect_b32 s68, s59, s77
	s_add_i32 s92, 0, 0x14000
	v_add_u32_e32 v78, s88, v204
	v_add_u32_e32 v170, s92, v204
	v_lshl_add_u64 v[202:203], s[74:75], 0, v[180:181]
	s_add_i32 m0, s15, 0xc000
	s_nop 0
	global_load_lds_dwordx4 v[202:203], off
	v_lshl_add_u64 v[202:203], s[74:75], 0, v[178:179]
	s_add_i32 m0, s15, 0xe000
	s_nop 0
	global_load_lds_dwordx4 v[202:203], off
	ds_read_b128 v[58:61], v78
	ds_read_b128 v[62:65], v78 offset:1024
	ds_read_b128 v[74:77], v78 offset:2048
	ds_read_b128 v[78:81], v78 offset:3072
	ds_read_b128 v[146:149], v170
	ds_read_b128 v[150:153], v170 offset:1024
	ds_read_b128 v[154:157], v170 offset:2048
	ds_read_b128 v[170:173], v170 offset:3072
	ds_read_b128 v[174:177], v208
	ds_read_b128 v[182:185], v208 offset:1024
	ds_read_b128 v[186:189], v208 offset:2048
	ds_read_b128 v[190:193], v208 offset:3072
	ds_read_b128 v[194:197], v208 offset:4096
	ds_read_b128 v[198:201], v208 offset:5120
	ds_read_b128 v[210:213], v208 offset:6144
	ds_read_b128 v[214:217], v208 offset:7168
	s_waitcnt vmcnt(8)
	s_waitcnt lgkmcnt(0)
	s_barrier
	s_setprio 1
	s_waitcnt lgkmcnt(0)
	v_mfma_f32_16x16x32_bf16 v[142:145], v[58:61], v[174:177], v[142:145]
	v_mfma_f32_16x16x32_bf16 v[138:141], v[74:77], v[174:177], v[138:141]
	v_mfma_f32_16x16x32_bf16 v[126:129], v[58:61], v[186:189], v[126:129]
	v_mfma_f32_16x16x32_bf16 v[122:125], v[74:77], v[186:189], v[122:125]
	v_mfma_f32_16x16x32_bf16 v[110:113], v[58:61], v[194:197], v[110:113]
	v_mfma_f32_16x16x32_bf16 v[106:109], v[74:77], v[194:197], v[106:109]
	v_mfma_f32_16x16x32_bf16 v[94:97], v[58:61], v[210:213], v[94:97]
	v_mfma_f32_16x16x32_bf16 v[90:93], v[74:77], v[210:213], v[90:93]
	v_mfma_f32_16x16x32_bf16 v[142:145], v[62:65], v[182:185], v[142:145]
	v_mfma_f32_16x16x32_bf16 v[138:141], v[78:81], v[182:185], v[138:141]
	v_mfma_f32_16x16x32_bf16 v[126:129], v[62:65], v[190:193], v[126:129]
	v_mfma_f32_16x16x32_bf16 v[122:125], v[78:81], v[190:193], v[122:125]
	v_mfma_f32_16x16x32_bf16 v[110:113], v[62:65], v[198:201], v[110:113]
	v_mfma_f32_16x16x32_bf16 v[106:109], v[78:81], v[198:201], v[106:109]
	v_mfma_f32_16x16x32_bf16 v[94:97], v[62:65], v[214:217], v[94:97]
	v_mfma_f32_16x16x32_bf16 v[90:93], v[78:81], v[214:217], v[90:93]
	s_setprio 0
	s_setprio 1
	v_mfma_f32_16x16x32_bf16 v[134:137], v[146:149], v[174:177], v[134:137]
	v_mfma_f32_16x16x32_bf16 v[130:133], v[154:157], v[174:177], v[130:133]
	v_mfma_f32_16x16x32_bf16 v[118:121], v[146:149], v[186:189], v[118:121]
	v_mfma_f32_16x16x32_bf16 v[114:117], v[154:157], v[186:189], v[114:117]
	v_mfma_f32_16x16x32_bf16 v[102:105], v[146:149], v[194:197], v[102:105]
	v_mfma_f32_16x16x32_bf16 v[98:101], v[154:157], v[194:197], v[98:101]
	v_mfma_f32_16x16x32_bf16 v[86:89], v[146:149], v[210:213], v[86:89]
	v_mfma_f32_16x16x32_bf16 v[82:85], v[154:157], v[210:213], v[82:85]
	v_mfma_f32_16x16x32_bf16 v[134:137], v[150:153], v[182:185], v[134:137]
	v_mfma_f32_16x16x32_bf16 v[130:133], v[170:173], v[182:185], v[130:133]
	v_mfma_f32_16x16x32_bf16 v[118:121], v[150:153], v[190:193], v[118:121]
	v_mfma_f32_16x16x32_bf16 v[114:117], v[170:173], v[190:193], v[114:117]
	v_mfma_f32_16x16x32_bf16 v[102:105], v[150:153], v[198:201], v[102:105]
	v_mfma_f32_16x16x32_bf16 v[98:101], v[170:173], v[198:201], v[98:101]
	v_mfma_f32_16x16x32_bf16 v[86:89], v[150:153], v[214:217], v[86:89]
	v_mfma_f32_16x16x32_bf16 v[82:85], v[170:173], v[214:217], v[82:85]
	s_setprio 0
	s_barrier
	s_add_i32 s88, s88, s14
	v_lshl_add_u64 v[202:203], s[68:69], 0, v[166:167]
	s_mov_b32 m0, s88
	s_nop 0
	global_load_lds_dwordx4 v[202:203], off
	s_add_i32 m0, s88, 0x2000
	s_add_u32 s90, s68, 0x40000
	v_lshl_add_u64 v[218:219], s[68:69], 0, v[158:159]
	s_addc_u32 s91, s69, 0
	s_add_i32 s88, s92, s14
	global_load_lds_dwordx4 v[218:219], off
	v_lshl_add_u64 v[220:221], s[90:91], 0, v[166:167]
	s_mov_b32 m0, s88
	v_lshl_add_u64 v[222:223], s[70:71], 0, v[162:163]
	global_load_lds_dwordx4 v[220:221], off
	v_lshl_add_u64 v[220:221], s[90:91], 0, v[158:159]
	s_add_i32 m0, s88, 0x2000
	s_nop 0
	global_load_lds_dwordx4 v[220:221], off
	v_lshl_add_u64 v[220:221], s[70:71], 0, v[160:161]
	s_mov_b32 m0, s15
	s_nop 0
	global_load_lds_dwordx4 v[220:221], off
	s_mov_b32 m0, s16
	s_nop 0
	global_load_lds_dwordx4 v[222:223], off
	ds_read_b128 v[174:177], v208 offset:16384
	ds_read_b128 v[182:185], v208 offset:17408
	ds_read_b128 v[186:189], v208 offset:18432
	ds_read_b128 v[190:193], v208 offset:19456
	ds_read_b128 v[194:197], v208 offset:20480
	ds_read_b128 v[198:201], v208 offset:21504
	ds_read_b128 v[210:213], v208 offset:22528
	ds_read_b128 v[214:217], v208 offset:23552
	s_waitcnt vmcnt(8)
	s_waitcnt lgkmcnt(0)
	s_barrier
	s_setprio 1
	s_waitcnt lgkmcnt(0)
	v_mfma_f32_16x16x32_bf16 v[70:73], v[58:61], v[174:177], v[70:73]
	v_mfma_f32_16x16x32_bf16 v[66:69], v[74:77], v[174:177], v[66:69]
	v_mfma_f32_16x16x32_bf16 v[46:49], v[58:61], v[186:189], v[46:49]
	v_mfma_f32_16x16x32_bf16 v[42:45], v[74:77], v[186:189], v[42:45]
	v_mfma_f32_16x16x32_bf16 v[30:33], v[58:61], v[194:197], v[30:33]
	v_mfma_f32_16x16x32_bf16 v[26:29], v[74:77], v[194:197], v[26:29]
	v_mfma_f32_16x16x32_bf16 v[14:17], v[58:61], v[210:213], v[14:17]
	v_mfma_f32_16x16x32_bf16 v[10:13], v[74:77], v[210:213], v[10:13]
	v_mfma_f32_16x16x32_bf16 v[70:73], v[62:65], v[182:185], v[70:73]
	v_mfma_f32_16x16x32_bf16 v[66:69], v[78:81], v[182:185], v[66:69]
	v_mfma_f32_16x16x32_bf16 v[46:49], v[62:65], v[190:193], v[46:49]
	v_mfma_f32_16x16x32_bf16 v[42:45], v[78:81], v[190:193], v[42:45]
	v_mfma_f32_16x16x32_bf16 v[30:33], v[62:65], v[198:201], v[30:33]
	v_mfma_f32_16x16x32_bf16 v[26:29], v[78:81], v[198:201], v[26:29]
	v_mfma_f32_16x16x32_bf16 v[14:17], v[62:65], v[214:217], v[14:17]
	v_mfma_f32_16x16x32_bf16 v[10:13], v[78:81], v[214:217], v[10:13]
	s_setprio 0
	s_setprio 1
	v_mfma_f32_16x16x32_bf16 v[54:57], v[146:149], v[174:177], v[54:57]
	v_mfma_f32_16x16x32_bf16 v[50:53], v[154:157], v[174:177], v[50:53]
	v_mfma_f32_16x16x32_bf16 v[38:41], v[146:149], v[186:189], v[38:41]
	v_mfma_f32_16x16x32_bf16 v[34:37], v[154:157], v[186:189], v[34:37]
	v_mfma_f32_16x16x32_bf16 v[22:25], v[146:149], v[194:197], v[22:25]
	v_mfma_f32_16x16x32_bf16 v[18:21], v[154:157], v[194:197], v[18:21]
	v_mfma_f32_16x16x32_bf16 v[6:9], v[146:149], v[210:213], v[6:9]
	v_mfma_f32_16x16x32_bf16 v[2:5], v[154:157], v[210:213], v[2:5]
	v_mfma_f32_16x16x32_bf16 v[54:57], v[150:153], v[182:185], v[54:57]
	v_mfma_f32_16x16x32_bf16 v[50:53], v[170:173], v[182:185], v[50:53]
	v_mfma_f32_16x16x32_bf16 v[38:41], v[150:153], v[190:193], v[38:41]
	v_mfma_f32_16x16x32_bf16 v[34:37], v[170:173], v[190:193], v[34:37]
	v_mfma_f32_16x16x32_bf16 v[22:25], v[150:153], v[198:201], v[22:25]
	v_mfma_f32_16x16x32_bf16 v[18:21], v[170:173], v[198:201], v[18:21]
	v_mfma_f32_16x16x32_bf16 v[6:9], v[150:153], v[214:217], v[6:9]
	v_mfma_f32_16x16x32_bf16 v[2:5], v[170:173], v[214:217], v[2:5]
	s_setprio 0
	s_barrier
	s_add_i32 s88, 0, 0x18000
	s_add_i32 s90, 0, 0x1c000
	v_add_u32_e32 v78, s88, v204
	v_add_u32_e32 v170, s90, v204
	s_add_u32 s70, s70, 0x40000
	s_addc_u32 s71, s71, 0
	s_mov_b32 m0, s20
	v_lshl_add_u64 v[232:233], s[70:71], 0, v[160:161]
	global_load_lds_dwordx4 v[232:233], off
	v_lshl_add_u64 v[232:233], s[70:71], 0, v[162:163]
	s_mov_b32 m0, s21
	s_nop 0
	global_load_lds_dwordx4 v[232:233], off
	ds_read_b128 v[58:61], v78
	ds_read_b128 v[62:65], v78 offset:1024
	ds_read_b128 v[74:77], v78 offset:2048
	ds_read_b128 v[78:81], v78 offset:3072
	ds_read_b128 v[146:149], v170
	ds_read_b128 v[150:153], v170 offset:1024
	ds_read_b128 v[154:157], v170 offset:2048
	ds_read_b128 v[170:173], v170 offset:3072
	ds_read_b128 v[174:177], v208 offset:32768
	ds_read_b128 v[182:185], v208 offset:33792
	ds_read_b128 v[186:189], v208 offset:34816
	ds_read_b128 v[190:193], v208 offset:35840
	ds_read_b128 v[194:197], v208 offset:36864
	ds_read_b128 v[198:201], v208 offset:37888
	ds_read_b128 v[210:213], v208 offset:38912
	ds_read_b128 v[214:217], v208 offset:39936
	s_waitcnt vmcnt(8)
	s_waitcnt lgkmcnt(0)
	s_barrier
	s_setprio 1
	s_waitcnt lgkmcnt(0)
	v_mfma_f32_16x16x32_bf16 v[142:145], v[58:61], v[174:177], v[142:145]
	v_mfma_f32_16x16x32_bf16 v[138:141], v[74:77], v[174:177], v[138:141]
	v_mfma_f32_16x16x32_bf16 v[126:129], v[58:61], v[186:189], v[126:129]
	v_mfma_f32_16x16x32_bf16 v[122:125], v[74:77], v[186:189], v[122:125]
	v_mfma_f32_16x16x32_bf16 v[110:113], v[58:61], v[194:197], v[110:113]
	v_mfma_f32_16x16x32_bf16 v[106:109], v[74:77], v[194:197], v[106:109]
	v_mfma_f32_16x16x32_bf16 v[94:97], v[58:61], v[210:213], v[94:97]
	v_mfma_f32_16x16x32_bf16 v[90:93], v[74:77], v[210:213], v[90:93]
	v_mfma_f32_16x16x32_bf16 v[142:145], v[62:65], v[182:185], v[142:145]
	v_mfma_f32_16x16x32_bf16 v[138:141], v[78:81], v[182:185], v[138:141]
	v_mfma_f32_16x16x32_bf16 v[126:129], v[62:65], v[190:193], v[126:129]
	v_mfma_f32_16x16x32_bf16 v[122:125], v[78:81], v[190:193], v[122:125]
	v_mfma_f32_16x16x32_bf16 v[110:113], v[62:65], v[198:201], v[110:113]
	v_mfma_f32_16x16x32_bf16 v[106:109], v[78:81], v[198:201], v[106:109]
	v_mfma_f32_16x16x32_bf16 v[94:97], v[62:65], v[214:217], v[94:97]
	v_mfma_f32_16x16x32_bf16 v[90:93], v[78:81], v[214:217], v[90:93]
	s_setprio 0
	s_setprio 1
	v_mfma_f32_16x16x32_bf16 v[134:137], v[146:149], v[174:177], v[134:137]
	v_mfma_f32_16x16x32_bf16 v[130:133], v[154:157], v[174:177], v[130:133]
	v_mfma_f32_16x16x32_bf16 v[118:121], v[146:149], v[186:189], v[118:121]
	v_mfma_f32_16x16x32_bf16 v[114:117], v[154:157], v[186:189], v[114:117]
	v_mfma_f32_16x16x32_bf16 v[102:105], v[146:149], v[194:197], v[102:105]
	v_mfma_f32_16x16x32_bf16 v[98:101], v[154:157], v[194:197], v[98:101]
	v_mfma_f32_16x16x32_bf16 v[86:89], v[146:149], v[210:213], v[86:89]
	v_mfma_f32_16x16x32_bf16 v[82:85], v[154:157], v[210:213], v[82:85]
	v_mfma_f32_16x16x32_bf16 v[134:137], v[150:153], v[182:185], v[134:137]
	v_mfma_f32_16x16x32_bf16 v[130:133], v[170:173], v[182:185], v[130:133]
	v_mfma_f32_16x16x32_bf16 v[118:121], v[150:153], v[190:193], v[118:121]
	v_mfma_f32_16x16x32_bf16 v[114:117], v[170:173], v[190:193], v[114:117]
	v_mfma_f32_16x16x32_bf16 v[102:105], v[150:153], v[198:201], v[102:105]
	v_mfma_f32_16x16x32_bf16 v[98:101], v[170:173], v[198:201], v[98:101]
	v_mfma_f32_16x16x32_bf16 v[86:89], v[150:153], v[214:217], v[86:89]
	v_mfma_f32_16x16x32_bf16 v[82:85], v[170:173], v[214:217], v[82:85]
	s_setprio 0
	s_barrier
	s_add_i32 s70, s88, s14
	v_lshl_add_u64 v[202:203], v[202:203], 0, s[56:57]
	s_mov_b32 m0, s70
	s_nop 0
	global_load_lds_dwordx4 v[202:203], off
	s_add_i32 m0, s70, 0x2000
	s_add_u32 s68, s68, 0x40080
	v_lshl_add_u64 v[202:203], v[218:219], 0, s[56:57]
	s_addc_u32 s69, s69, 0
	s_add_i32 s70, s90, s14
	global_load_lds_dwordx4 v[202:203], off
	v_lshl_add_u64 v[202:203], s[68:69], 0, v[166:167]
	s_mov_b32 m0, s70
	s_nop 0
	global_load_lds_dwordx4 v[202:203], off
	v_lshl_add_u64 v[202:203], s[68:69], 0, v[158:159]
	s_add_i32 m0, s70, 0x2000
	s_nop 0
	global_load_lds_dwordx4 v[202:203], off
	v_lshl_add_u64 v[202:203], v[220:221], 0, s[56:57]
	s_mov_b32 m0, s24
	s_nop 0
	global_load_lds_dwordx4 v[202:203], off
	v_lshl_add_u64 v[202:203], v[222:223], 0, s[56:57]
	s_mov_b32 m0, s25
	s_nop 0
	global_load_lds_dwordx4 v[202:203], off
	ds_read_b128 v[174:177], v208 offset:49152
	ds_read_b128 v[182:185], v208 offset:50176
	ds_read_b128 v[186:189], v208 offset:51200
	ds_read_b128 v[190:193], v208 offset:52224
	ds_read_b128 v[194:197], v208 offset:53248
	ds_read_b128 v[198:201], v208 offset:54272
	ds_read_b128 v[210:213], v208 offset:55296
	ds_read_b128 v[214:217], v208 offset:56320
	s_waitcnt vmcnt(8)
	s_waitcnt lgkmcnt(0)
	s_barrier
	s_setprio 1
	s_waitcnt lgkmcnt(0)
	v_mfma_f32_16x16x32_bf16 v[70:73], v[58:61], v[174:177], v[70:73]
	v_mfma_f32_16x16x32_bf16 v[66:69], v[74:77], v[174:177], v[66:69]
	v_mfma_f32_16x16x32_bf16 v[46:49], v[58:61], v[186:189], v[46:49]
	v_mfma_f32_16x16x32_bf16 v[42:45], v[74:77], v[186:189], v[42:45]
	v_mfma_f32_16x16x32_bf16 v[30:33], v[58:61], v[194:197], v[30:33]
	v_mfma_f32_16x16x32_bf16 v[26:29], v[74:77], v[194:197], v[26:29]
	v_mfma_f32_16x16x32_bf16 v[14:17], v[58:61], v[210:213], v[14:17]
	v_mfma_f32_16x16x32_bf16 v[10:13], v[74:77], v[210:213], v[10:13]
	v_mfma_f32_16x16x32_bf16 v[70:73], v[62:65], v[182:185], v[70:73]
	v_mfma_f32_16x16x32_bf16 v[66:69], v[78:81], v[182:185], v[66:69]
	v_mfma_f32_16x16x32_bf16 v[46:49], v[62:65], v[190:193], v[46:49]
	v_mfma_f32_16x16x32_bf16 v[42:45], v[78:81], v[190:193], v[42:45]
	v_mfma_f32_16x16x32_bf16 v[30:33], v[62:65], v[198:201], v[30:33]
	v_mfma_f32_16x16x32_bf16 v[26:29], v[78:81], v[198:201], v[26:29]
	v_mfma_f32_16x16x32_bf16 v[14:17], v[62:65], v[214:217], v[14:17]
	v_mfma_f32_16x16x32_bf16 v[10:13], v[78:81], v[214:217], v[10:13]
	s_setprio 0
	s_setprio 1
	v_mfma_f32_16x16x32_bf16 v[54:57], v[146:149], v[174:177], v[54:57]
	v_mfma_f32_16x16x32_bf16 v[50:53], v[154:157], v[174:177], v[50:53]
	v_mfma_f32_16x16x32_bf16 v[38:41], v[146:149], v[186:189], v[38:41]
	v_mfma_f32_16x16x32_bf16 v[34:37], v[154:157], v[186:189], v[34:37]
	v_mfma_f32_16x16x32_bf16 v[22:25], v[146:149], v[194:197], v[22:25]
	v_mfma_f32_16x16x32_bf16 v[18:21], v[154:157], v[194:197], v[18:21]
	v_mfma_f32_16x16x32_bf16 v[6:9], v[146:149], v[210:213], v[6:9]
	v_mfma_f32_16x16x32_bf16 v[2:5], v[154:157], v[210:213], v[2:5]
	v_mfma_f32_16x16x32_bf16 v[54:57], v[150:153], v[182:185], v[54:57]
	v_mfma_f32_16x16x32_bf16 v[50:53], v[170:173], v[182:185], v[50:53]
	v_mfma_f32_16x16x32_bf16 v[38:41], v[150:153], v[190:193], v[38:41]
	v_mfma_f32_16x16x32_bf16 v[34:37], v[170:173], v[190:193], v[34:37]
	v_mfma_f32_16x16x32_bf16 v[22:25], v[150:153], v[198:201], v[22:25]
	v_mfma_f32_16x16x32_bf16 v[18:21], v[170:173], v[198:201], v[18:21]
	v_mfma_f32_16x16x32_bf16 v[6:9], v[150:153], v[214:217], v[6:9]
	v_mfma_f32_16x16x32_bf16 v[2:5], v[170:173], v[214:217], v[2:5]
	s_setprio 0
	s_barrier
	s_add_u32 s77, s77, 0x100
	s_addc_u32 s79, s79, 0
	s_add_u32 s74, s74, 0x100
	s_addc_u32 s75, s75, 0
	s_cmp_ge_i32 s84, s1
	s_mov_b32 s68, s84
	s_cbranch_scc0 .LBB0_664
	s_movk_i32 s79, 0x1ff
	s_mov_b32 s84, 0xf800000
	s_mov_b32 s88, 0xe800000
	s_and_b64 vcc, exec, s[48:49]
	s_cbranch_vccz .LBB0_667

.LBB0_817:
	s_add_i32 s69, s58, 2
	s_add_u32 s59, s54, 0xfffc0080
	s_addc_u32 s60, s55, -1
	s_add_i32 s70, 0, 0x10000
	s_cmp_eq_u32 s53, s58
	s_cselect_b32 s61, s43, s60
	s_cselect_b32 s60, s45, s59
	v_add_u32_e32 v146, s70, v151
	s_cselect_b32 s59, s64, s68
	s_cselect_b32 s58, s65, s66
	s_add_i32 s72, 0, 0x14000
	ds_read_b128 v[142:145], v146
	ds_read_b128 v[156:159], v146 offset:1024
	ds_read_b128 v[160:163], v146 offset:2048
	ds_read_b128 v[170:173], v146 offset:3072
	v_add_u32_e32 v146, s72, v151
	ds_read_b128 v[174:177], v146
	ds_read_b128 v[178:181], v146 offset:1024
	ds_read_b128 v[182:185], v146 offset:2048
	ds_read_b128 v[186:189], v146 offset:3072
	v_lshl_add_u64 v[146:147], s[54:55], 0, v[140:141]
	s_add_i32 m0, s16, 0xc000
	ds_read_b128 v[190:193], v154
	ds_read_b128 v[194:197], v154 offset:1024
	ds_read_b128 v[198:201], v154 offset:2048
	ds_read_b128 v[202:205], v154 offset:3072
	ds_read_b128 v[206:209], v154 offset:4096
	ds_read_b128 v[210:213], v154 offset:5120
	ds_read_b128 v[214:217], v154 offset:6144
	ds_read_b128 v[218:221], v154 offset:7168
	global_load_lds_dwordx4 v[146:147], off
	v_lshl_add_u64 v[146:147], s[54:55], 0, v[138:139]
	s_add_i32 m0, s16, 0xe000
	s_nop 0
	global_load_lds_dwordx4 v[146:147], off
	s_waitcnt vmcnt(8)
	s_waitcnt lgkmcnt(0)
	s_barrier
	s_setprio 1
	s_waitcnt lgkmcnt(0)
	v_mfma_f32_16x16x32_bf16 v[126:129], v[142:145], v[190:193], v[126:129]
	v_mfma_f32_16x16x32_bf16 v[118:121], v[160:163], v[190:193], v[118:121]
	v_mfma_f32_16x16x32_bf16 v[110:113], v[142:145], v[198:201], v[110:113]
	v_mfma_f32_16x16x32_bf16 v[102:105], v[160:163], v[198:201], v[102:105]
	v_mfma_f32_16x16x32_bf16 v[94:97], v[142:145], v[206:209], v[94:97]
	v_mfma_f32_16x16x32_bf16 v[86:89], v[160:163], v[206:209], v[86:89]
	v_mfma_f32_16x16x32_bf16 v[78:81], v[142:145], v[214:217], v[78:81]
	v_mfma_f32_16x16x32_bf16 v[70:73], v[160:163], v[214:217], v[70:73]
	v_mfma_f32_16x16x32_bf16 v[126:129], v[156:159], v[194:197], v[126:129]
	v_mfma_f32_16x16x32_bf16 v[118:121], v[170:173], v[194:197], v[118:121]
	v_mfma_f32_16x16x32_bf16 v[110:113], v[156:159], v[202:205], v[110:113]
	v_mfma_f32_16x16x32_bf16 v[102:105], v[170:173], v[202:205], v[102:105]
	v_mfma_f32_16x16x32_bf16 v[94:97], v[156:159], v[210:213], v[94:97]
	v_mfma_f32_16x16x32_bf16 v[86:89], v[170:173], v[210:213], v[86:89]
	v_mfma_f32_16x16x32_bf16 v[78:81], v[156:159], v[218:221], v[78:81]
	v_mfma_f32_16x16x32_bf16 v[70:73], v[170:173], v[218:221], v[70:73]
	s_setprio 0
	s_setprio 1
	v_mfma_f32_16x16x32_bf16 v[122:125], v[174:177], v[190:193], v[122:125]
	v_mfma_f32_16x16x32_bf16 v[114:117], v[182:185], v[190:193], v[114:117]
	v_mfma_f32_16x16x32_bf16 v[106:109], v[174:177], v[198:201], v[106:109]
	v_mfma_f32_16x16x32_bf16 v[98:101], v[182:185], v[198:201], v[98:101]
	v_mfma_f32_16x16x32_bf16 v[90:93], v[174:177], v[206:209], v[90:93]
	v_mfma_f32_16x16x32_bf16 v[82:85], v[182:185], v[206:209], v[82:85]
	v_mfma_f32_16x16x32_bf16 v[74:77], v[174:177], v[214:217], v[74:77]
	v_mfma_f32_16x16x32_bf16 v[66:69], v[182:185], v[214:217], v[66:69]
	v_mfma_f32_16x16x32_bf16 v[122:125], v[178:181], v[194:197], v[122:125]
	v_mfma_f32_16x16x32_bf16 v[114:117], v[186:189], v[194:197], v[114:117]
	v_mfma_f32_16x16x32_bf16 v[106:109], v[178:181], v[202:205], v[106:109]
	v_mfma_f32_16x16x32_bf16 v[98:101], v[186:189], v[202:205], v[98:101]
	v_mfma_f32_16x16x32_bf16 v[90:93], v[178:181], v[210:213], v[90:93]
	v_mfma_f32_16x16x32_bf16 v[82:85], v[186:189], v[210:213], v[82:85]
	v_mfma_f32_16x16x32_bf16 v[74:77], v[178:181], v[218:221], v[74:77]
	v_mfma_f32_16x16x32_bf16 v[66:69], v[186:189], v[218:221], v[66:69]
	s_setprio 0
	s_barrier
	s_add_i32 s70, s70, s14
	v_lshl_add_u64 v[146:147], s[58:59], 0, v[166:167]
	s_mov_b32 m0, s70
	s_nop 0
	global_load_lds_dwordx4 v[146:147], off
	s_add_i32 m0, s70, 0x2000
	s_add_u32 s70, s58, 0x40000
	v_lshl_add_u64 v[164:165], s[58:59], 0, v[134:135]
	s_addc_u32 s71, s59, 0
	s_add_i32 s72, s72, s14
	global_load_lds_dwordx4 v[164:165], off
	v_lshl_add_u64 v[222:223], s[70:71], 0, v[166:167]
	s_mov_b32 m0, s72
	v_lshl_add_u64 v[232:233], s[60:61], 0, v[130:131]
	global_load_lds_dwordx4 v[222:223], off
	v_lshl_add_u64 v[222:223], s[70:71], 0, v[134:135]
	s_add_i32 m0, s72, 0x2000
	s_nop 0
	global_load_lds_dwordx4 v[222:223], off
	v_lshl_add_u64 v[222:223], s[60:61], 0, v[132:133]
	s_mov_b32 m0, s16
	s_nop 0
	global_load_lds_dwordx4 v[222:223], off
	s_mov_b32 m0, s20
	s_nop 0
	global_load_lds_dwordx4 v[232:233], off
	ds_read_b128 v[190:193], v154 offset:16384
	ds_read_b128 v[194:197], v154 offset:17408
	ds_read_b128 v[198:201], v154 offset:18432
	ds_read_b128 v[202:205], v154 offset:19456
	ds_read_b128 v[206:209], v154 offset:20480
	ds_read_b128 v[210:213], v154 offset:21504
	ds_read_b128 v[214:217], v154 offset:22528
	ds_read_b128 v[218:221], v154 offset:23552
	s_waitcnt vmcnt(8)
	s_waitcnt lgkmcnt(0)
	s_barrier
	s_setprio 1
	s_waitcnt lgkmcnt(0)
	v_mfma_f32_16x16x32_bf16 v[62:65], v[142:145], v[190:193], v[62:65]
	v_mfma_f32_16x16x32_bf16 v[54:57], v[160:163], v[190:193], v[54:57]
	v_mfma_f32_16x16x32_bf16 v[46:49], v[142:145], v[198:201], v[46:49]
	v_mfma_f32_16x16x32_bf16 v[38:41], v[160:163], v[198:201], v[38:41]
	v_mfma_f32_16x16x32_bf16 v[30:33], v[142:145], v[206:209], v[30:33]
	v_mfma_f32_16x16x32_bf16 v[22:25], v[160:163], v[206:209], v[22:25]
	v_mfma_f32_16x16x32_bf16 v[14:17], v[142:145], v[214:217], v[14:17]
	v_mfma_f32_16x16x32_bf16 v[6:9], v[160:163], v[214:217], v[6:9]
	v_mfma_f32_16x16x32_bf16 v[62:65], v[156:159], v[194:197], v[62:65]
	v_mfma_f32_16x16x32_bf16 v[54:57], v[170:173], v[194:197], v[54:57]
	v_mfma_f32_16x16x32_bf16 v[46:49], v[156:159], v[202:205], v[46:49]
	v_mfma_f32_16x16x32_bf16 v[38:41], v[170:173], v[202:205], v[38:41]
	v_mfma_f32_16x16x32_bf16 v[30:33], v[156:159], v[210:213], v[30:33]
	v_mfma_f32_16x16x32_bf16 v[22:25], v[170:173], v[210:213], v[22:25]
	v_mfma_f32_16x16x32_bf16 v[14:17], v[156:159], v[218:221], v[14:17]
	v_mfma_f32_16x16x32_bf16 v[6:9], v[170:173], v[218:221], v[6:9]
	s_setprio 0
	s_setprio 1
	v_mfma_f32_16x16x32_bf16 v[58:61], v[174:177], v[190:193], v[58:61]
	v_mfma_f32_16x16x32_bf16 v[50:53], v[182:185], v[190:193], v[50:53]
	v_mfma_f32_16x16x32_bf16 v[42:45], v[174:177], v[198:201], v[42:45]
	v_mfma_f32_16x16x32_bf16 v[34:37], v[182:185], v[198:201], v[34:37]
	v_mfma_f32_16x16x32_bf16 v[26:29], v[174:177], v[206:209], v[26:29]
	v_mfma_f32_16x16x32_bf16 v[18:21], v[182:185], v[206:209], v[18:21]
	v_mfma_f32_16x16x32_bf16 v[10:13], v[174:177], v[214:217], v[10:13]
	v_mfma_f32_16x16x32_bf16 v[2:5], v[182:185], v[214:217], v[2:5]
	v_mfma_f32_16x16x32_bf16 v[58:61], v[178:181], v[194:197], v[58:61]
	v_mfma_f32_16x16x32_bf16 v[50:53], v[186:189], v[194:197], v[50:53]
	v_mfma_f32_16x16x32_bf16 v[42:45], v[178:181], v[202:205], v[42:45]
	v_mfma_f32_16x16x32_bf16 v[34:37], v[186:189], v[202:205], v[34:37]
	v_mfma_f32_16x16x32_bf16 v[26:29], v[178:181], v[210:213], v[26:29]
	v_mfma_f32_16x16x32_bf16 v[18:21], v[186:189], v[210:213], v[18:21]
	v_mfma_f32_16x16x32_bf16 v[10:13], v[178:181], v[218:221], v[10:13]
	v_mfma_f32_16x16x32_bf16 v[2:5], v[186:189], v[218:221], v[2:5]
	s_setprio 0
	s_barrier
	s_add_i32 s70, 0, 0x18000
	v_add_u32_e32 v148, s70, v151
	s_add_i32 s71, 0, 0x1c000
	s_add_u32 s60, s60, 0x40000
	s_addc_u32 s61, s61, 0
	s_mov_b32 m0, s21
	v_lshl_add_u64 v[234:235], s[60:61], 0, v[132:133]
	global_load_lds_dwordx4 v[234:235], off
	v_lshl_add_u64 v[234:235], s[60:61], 0, v[130:131]
	s_mov_b32 m0, s22
	s_nop 0
	global_load_lds_dwordx4 v[234:235], off
	ds_read_b128 v[142:145], v148
	ds_read_b128 v[156:159], v148 offset:1024
	ds_read_b128 v[160:163], v148 offset:2048
	ds_read_b128 v[170:173], v148 offset:3072
	v_add_u32_e32 v148, s71, v151
	ds_read_b128 v[174:177], v148
	ds_read_b128 v[178:181], v148 offset:1024
	ds_read_b128 v[182:185], v148 offset:2048
	ds_read_b128 v[186:189], v148 offset:3072
	ds_read_b128 v[190:193], v154 offset:32768
	ds_read_b128 v[194:197], v154 offset:33792
	ds_read_b128 v[198:201], v154 offset:34816
	ds_read_b128 v[202:205], v154 offset:35840
	ds_read_b128 v[206:209], v154 offset:36864
	ds_read_b128 v[210:213], v154 offset:37888
	ds_read_b128 v[214:217], v154 offset:38912
	ds_read_b128 v[218:221], v154 offset:39936
	s_waitcnt vmcnt(8)
	s_waitcnt lgkmcnt(0)
	s_barrier
	s_setprio 1
	s_waitcnt lgkmcnt(0)
	v_mfma_f32_16x16x32_bf16 v[126:129], v[142:145], v[190:193], v[126:129]
	v_mfma_f32_16x16x32_bf16 v[118:121], v[160:163], v[190:193], v[118:121]
	v_mfma_f32_16x16x32_bf16 v[110:113], v[142:145], v[198:201], v[110:113]
	v_mfma_f32_16x16x32_bf16 v[102:105], v[160:163], v[198:201], v[102:105]
	v_mfma_f32_16x16x32_bf16 v[94:97], v[142:145], v[206:209], v[94:97]
	v_mfma_f32_16x16x32_bf16 v[86:89], v[160:163], v[206:209], v[86:89]
	v_mfma_f32_16x16x32_bf16 v[78:81], v[142:145], v[214:217], v[78:81]
	v_mfma_f32_16x16x32_bf16 v[70:73], v[160:163], v[214:217], v[70:73]
	v_mfma_f32_16x16x32_bf16 v[126:129], v[156:159], v[194:197], v[126:129]
	v_mfma_f32_16x16x32_bf16 v[118:121], v[170:173], v[194:197], v[118:121]
	v_mfma_f32_16x16x32_bf16 v[110:113], v[156:159], v[202:205], v[110:113]
	v_mfma_f32_16x16x32_bf16 v[102:105], v[170:173], v[202:205], v[102:105]
	v_mfma_f32_16x16x32_bf16 v[94:97], v[156:159], v[210:213], v[94:97]
	v_mfma_f32_16x16x32_bf16 v[86:89], v[170:173], v[210:213], v[86:89]
	v_mfma_f32_16x16x32_bf16 v[78:81], v[156:159], v[218:221], v[78:81]
	v_mfma_f32_16x16x32_bf16 v[70:73], v[170:173], v[218:221], v[70:73]
	s_setprio 0
	s_setprio 1
	v_mfma_f32_16x16x32_bf16 v[122:125], v[174:177], v[190:193], v[122:125]
	v_mfma_f32_16x16x32_bf16 v[114:117], v[182:185], v[190:193], v[114:117]
	v_mfma_f32_16x16x32_bf16 v[106:109], v[174:177], v[198:201], v[106:109]
	v_mfma_f32_16x16x32_bf16 v[98:101], v[182:185], v[198:201], v[98:101]
	v_mfma_f32_16x16x32_bf16 v[90:93], v[174:177], v[206:209], v[90:93]
	v_mfma_f32_16x16x32_bf16 v[82:85], v[182:185], v[206:209], v[82:85]
	v_mfma_f32_16x16x32_bf16 v[74:77], v[174:177], v[214:217], v[74:77]
	v_mfma_f32_16x16x32_bf16 v[66:69], v[182:185], v[214:217], v[66:69]
	v_mfma_f32_16x16x32_bf16 v[122:125], v[178:181], v[194:197], v[122:125]
	v_mfma_f32_16x16x32_bf16 v[114:117], v[186:189], v[194:197], v[114:117]
	v_mfma_f32_16x16x32_bf16 v[106:109], v[178:181], v[202:205], v[106:109]
	v_mfma_f32_16x16x32_bf16 v[98:101], v[186:189], v[202:205], v[98:101]
	v_mfma_f32_16x16x32_bf16 v[90:93], v[178:181], v[210:213], v[90:93]
	v_mfma_f32_16x16x32_bf16 v[82:85], v[186:189], v[210:213], v[82:85]
	v_mfma_f32_16x16x32_bf16 v[74:77], v[178:181], v[218:221], v[74:77]
	v_mfma_f32_16x16x32_bf16 v[66:69], v[186:189], v[218:221], v[66:69]
	s_setprio 0
	s_barrier
	s_add_i32 s60, s70, s14
	v_lshl_add_u64 v[146:147], v[146:147], 0, s[56:57]
	s_mov_b32 m0, s60
	s_nop 0
	global_load_lds_dwordx4 v[146:147], off
	s_add_i32 m0, s60, 0x2000
	s_add_u32 s58, s58, 0x40080
	v_lshl_add_u64 v[146:147], v[164:165], 0, s[56:57]
	s_addc_u32 s59, s59, 0
	s_add_i32 s60, s71, s14
	global_load_lds_dwordx4 v[146:147], off
	v_lshl_add_u64 v[146:147], s[58:59], 0, v[166:167]
	s_mov_b32 m0, s60
	s_nop 0
	global_load_lds_dwordx4 v[146:147], off
	v_lshl_add_u64 v[146:147], s[58:59], 0, v[134:135]
	s_add_i32 m0, s60, 0x2000
	s_nop 0
	global_load_lds_dwordx4 v[146:147], off
	v_lshl_add_u64 v[146:147], v[222:223], 0, s[56:57]
	s_mov_b32 m0, s23
	s_nop 0
	global_load_lds_dwordx4 v[146:147], off
	v_lshl_add_u64 v[146:147], v[232:233], 0, s[56:57]
	s_mov_b32 m0, s24
	s_nop 0
	global_load_lds_dwordx4 v[146:147], off
	ds_read_b128 v[190:193], v154 offset:49152
	ds_read_b128 v[194:197], v154 offset:50176
	ds_read_b128 v[198:201], v154 offset:51200
	ds_read_b128 v[202:205], v154 offset:52224
	ds_read_b128 v[206:209], v154 offset:53248
	ds_read_b128 v[210:213], v154 offset:54272
	ds_read_b128 v[214:217], v154 offset:55296
	ds_read_b128 v[218:221], v154 offset:56320
	s_waitcnt vmcnt(8)
	s_waitcnt lgkmcnt(0)
	s_barrier
	s_setprio 1
	s_waitcnt lgkmcnt(0)
	v_mfma_f32_16x16x32_bf16 v[62:65], v[142:145], v[190:193], v[62:65]
	v_mfma_f32_16x16x32_bf16 v[54:57], v[160:163], v[190:193], v[54:57]
	v_mfma_f32_16x16x32_bf16 v[46:49], v[142:145], v[198:201], v[46:49]
	v_mfma_f32_16x16x32_bf16 v[38:41], v[160:163], v[198:201], v[38:41]
	v_mfma_f32_16x16x32_bf16 v[30:33], v[142:145], v[206:209], v[30:33]
	v_mfma_f32_16x16x32_bf16 v[22:25], v[160:163], v[206:209], v[22:25]
	v_mfma_f32_16x16x32_bf16 v[14:17], v[142:145], v[214:217], v[14:17]
	v_mfma_f32_16x16x32_bf16 v[6:9], v[160:163], v[214:217], v[6:9]
	v_mfma_f32_16x16x32_bf16 v[62:65], v[156:159], v[194:197], v[62:65]
	v_mfma_f32_16x16x32_bf16 v[54:57], v[170:173], v[194:197], v[54:57]
	v_mfma_f32_16x16x32_bf16 v[46:49], v[156:159], v[202:205], v[46:49]
	v_mfma_f32_16x16x32_bf16 v[38:41], v[170:173], v[202:205], v[38:41]
	v_mfma_f32_16x16x32_bf16 v[30:33], v[156:159], v[210:213], v[30:33]
	v_mfma_f32_16x16x32_bf16 v[22:25], v[170:173], v[210:213], v[22:25]
	v_mfma_f32_16x16x32_bf16 v[14:17], v[156:159], v[218:221], v[14:17]
	v_mfma_f32_16x16x32_bf16 v[6:9], v[170:173], v[218:221], v[6:9]
	s_setprio 0
	s_setprio 1
	v_mfma_f32_16x16x32_bf16 v[58:61], v[174:177], v[190:193], v[58:61]
	v_mfma_f32_16x16x32_bf16 v[50:53], v[182:185], v[190:193], v[50:53]
	v_mfma_f32_16x16x32_bf16 v[42:45], v[174:177], v[198:201], v[42:45]
	v_mfma_f32_16x16x32_bf16 v[34:37], v[182:185], v[198:201], v[34:37]
	v_mfma_f32_16x16x32_bf16 v[26:29], v[174:177], v[206:209], v[26:29]
	v_mfma_f32_16x16x32_bf16 v[18:21], v[182:185], v[206:209], v[18:21]
	v_mfma_f32_16x16x32_bf16 v[10:13], v[174:177], v[214:217], v[10:13]
	v_mfma_f32_16x16x32_bf16 v[2:5], v[182:185], v[214:217], v[2:5]
	v_mfma_f32_16x16x32_bf16 v[58:61], v[178:181], v[194:197], v[58:61]
	v_mfma_f32_16x16x32_bf16 v[50:53], v[186:189], v[194:197], v[50:53]
	v_mfma_f32_16x16x32_bf16 v[42:45], v[178:181], v[202:205], v[42:45]
	v_mfma_f32_16x16x32_bf16 v[34:37], v[186:189], v[202:205], v[34:37]
	v_mfma_f32_16x16x32_bf16 v[26:29], v[178:181], v[210:213], v[26:29]
	v_mfma_f32_16x16x32_bf16 v[18:21], v[186:189], v[210:213], v[18:21]
	v_mfma_f32_16x16x32_bf16 v[10:13], v[178:181], v[218:221], v[10:13]
	v_mfma_f32_16x16x32_bf16 v[2:5], v[186:189], v[218:221], v[2:5]
	s_setprio 0
	s_barrier
	s_add_u32 s66, s66, 0x100
	s_addc_u32 s68, s68, 0
	s_add_u32 s54, s54, 0x100
	s_addc_u32 s55, s55, 0
	s_cmp_ge_i32 s69, s13
	s_mov_b32 s58, s69
	s_cbranch_scc0 .LBB0_817
	s_mov_b64 s[72:73], 0xe800000
	s_mov_b64 s[70:71], 0xe800800
	v_mov_b32_e32 v209, v1
	s_and_b64 vcc, exec, s[36:37]
	s_cbranch_vccz .LBB0_820

.LBB0_842:
	s_add_i32 s66, s54, 2
	s_add_u32 s55, s52, 0xfffe0080
	s_addc_u32 s58, s53, -1
	s_add_i32 s68, 0, 0x10000
	s_cmp_eq_u32 s51, s54
	s_cselect_b32 s59, s41, s58
	s_cselect_b32 s58, s43, s55
	s_cselect_b32 s55, s62, s65
	s_cselect_b32 s54, s63, s64
	s_add_i32 s69, 0, 0x14000
	v_add_u32_e32 v2, s68, v196
	v_add_u32_e32 v6, s69, v196
	v_lshl_add_u64 v[170:171], s[52:53], 0, v[184:185]
	s_add_i32 m0, s16, 0xc000
	s_nop 0
	global_load_lds_dwordx4 v[170:171], off
	v_lshl_add_u64 v[170:171], s[52:53], 0, v[182:183]
	s_add_i32 m0, s16, 0xe000
	s_nop 0
	global_load_lds_dwordx4 v[170:171], off
	ds_read_b128 v[26:29], v2
	ds_read_b128 v[30:33], v2 offset:1024
	ds_read_b128 v[18:21], v2 offset:2048
	ds_read_b128 v[22:25], v2 offset:3072
	ds_read_b128 v[10:13], v6
	ds_read_b128 v[14:17], v6 offset:1024
	ds_read_b128 v[2:5], v6 offset:2048
	ds_read_b128 v[6:9], v6 offset:3072
	ds_read_b128 v[186:189], v198
	ds_read_b128 v[190:193], v198 offset:1024
	ds_read_b128 v[200:203], v198 offset:2048
	ds_read_b128 v[204:207], v198 offset:3072
	ds_read_b128 v[208:211], v198 offset:4096
	ds_read_b128 v[212:215], v198 offset:5120
	ds_read_b128 v[216:219], v198 offset:6144
	ds_read_b128 v[220:223], v198 offset:7168
	s_waitcnt vmcnt(8)
	s_waitcnt lgkmcnt(0)
	s_barrier
	s_setprio 1
	s_waitcnt lgkmcnt(0)
	v_mfma_scale_f32_16x16x128_f8f6f4 v[158:161], v[26:33], v[186:193], v[158:161], v194, v169 op_sel_hi:[0,0,0]
	v_mfma_scale_f32_16x16x128_f8f6f4 v[150:153], v[18:25], v[186:193], v[150:153], v194, v169 op_sel_hi:[0,0,0]
	v_mfma_scale_f32_16x16x128_f8f6f4 v[142:145], v[26:33], v[200:207], v[142:145], v194, v169 op_sel_hi:[0,0,0]
	v_mfma_scale_f32_16x16x128_f8f6f4 v[134:137], v[18:25], v[200:207], v[134:137], v194, v169 op_sel_hi:[0,0,0]
	v_mfma_scale_f32_16x16x128_f8f6f4 v[126:129], v[26:33], v[208:215], v[126:129], v194, v169 op_sel_hi:[0,0,0]
	v_mfma_scale_f32_16x16x128_f8f6f4 v[118:121], v[18:25], v[208:215], v[118:121], v194, v169 op_sel_hi:[0,0,0]
	v_mfma_scale_f32_16x16x128_f8f6f4 v[110:113], v[26:33], v[216:223], v[110:113], v194, v169 op_sel_hi:[0,0,0]
	v_mfma_scale_f32_16x16x128_f8f6f4 v[102:105], v[18:25], v[216:223], v[102:105], v194, v169 op_sel_hi:[0,0,0]
	s_setprio 0
	s_setprio 1
	v_mfma_scale_f32_16x16x128_f8f6f4 v[154:157], v[10:17], v[186:193], v[154:157], v194, v169 op_sel_hi:[0,0,0]
	v_mfma_scale_f32_16x16x128_f8f6f4 v[146:149], v[2:9], v[186:193], v[146:149], v194, v169 op_sel_hi:[0,0,0]
	v_mfma_scale_f32_16x16x128_f8f6f4 v[138:141], v[10:17], v[200:207], v[138:141], v194, v169 op_sel_hi:[0,0,0]
	v_mfma_scale_f32_16x16x128_f8f6f4 v[130:133], v[2:9], v[200:207], v[130:133], v194, v169 op_sel_hi:[0,0,0]
	v_mfma_scale_f32_16x16x128_f8f6f4 v[122:125], v[10:17], v[208:215], v[122:125], v194, v169 op_sel_hi:[0,0,0]
	v_mfma_scale_f32_16x16x128_f8f6f4 v[114:117], v[2:9], v[208:215], v[114:117], v194, v169 op_sel_hi:[0,0,0]
	v_mfma_scale_f32_16x16x128_f8f6f4 v[106:109], v[10:17], v[216:223], v[106:109], v194, v169 op_sel_hi:[0,0,0]
	v_mfma_scale_f32_16x16x128_f8f6f4 v[98:101], v[2:9], v[216:223], v[98:101], v194, v169 op_sel_hi:[0,0,0]
	s_setprio 0
	s_barrier
	s_add_i32 s68, s68, s14
	v_lshl_add_u64 v[186:187], s[54:55], 0, v[166:167]
	s_mov_b32 m0, s68
	s_nop 0
	global_load_lds_dwordx4 v[186:187], off
	s_add_i32 m0, s68, 0x2000
	s_add_u32 s70, s54, 0x20000
	v_lshl_add_u64 v[188:189], s[54:55], 0, v[178:179]
	s_addc_u32 s71, s55, 0
	s_add_i32 s68, s69, s14
	global_load_lds_dwordx4 v[188:189], off
	v_lshl_add_u64 v[170:171], s[70:71], 0, v[166:167]
	s_mov_b32 m0, s68
	v_lshl_add_u64 v[190:191], s[58:59], 0, v[164:165]
	global_load_lds_dwordx4 v[170:171], off
	v_lshl_add_u64 v[170:171], s[70:71], 0, v[178:179]
	s_add_i32 m0, s68, 0x2000
	v_lshl_add_u64 v[192:193], s[58:59], 0, v[162:163]
	global_load_lds_dwordx4 v[170:171], off
	s_mov_b32 m0, s16
	s_nop 0
	global_load_lds_dwordx4 v[190:191], off
	s_mov_b32 m0, s20
	s_nop 0
	global_load_lds_dwordx4 v[192:193], off
	ds_read_b128 v[200:203], v198 offset:16384
	ds_read_b128 v[204:207], v198 offset:17408
	ds_read_b128 v[208:211], v198 offset:18432
	ds_read_b128 v[212:215], v198 offset:19456
	ds_read_b128 v[216:219], v198 offset:20480
	ds_read_b128 v[220:223], v198 offset:21504
	ds_read_b128 v[236:239], v198 offset:22528
	ds_read_b128 v[240:243], v198 offset:23552
	s_waitcnt vmcnt(8)
	s_waitcnt lgkmcnt(0)
	s_barrier
	s_setprio 1
	s_waitcnt lgkmcnt(0)
	v_mfma_scale_f32_16x16x128_f8f6f4 v[94:97], v[26:33], v[200:207], v[94:97], v194, v169 op_sel_hi:[0,0,0]
	v_mfma_scale_f32_16x16x128_f8f6f4 v[86:89], v[18:25], v[200:207], v[86:89], v194, v169 op_sel_hi:[0,0,0]
	v_mfma_scale_f32_16x16x128_f8f6f4 v[78:81], v[26:33], v[208:215], v[78:81], v194, v169 op_sel_hi:[0,0,0]
	v_mfma_scale_f32_16x16x128_f8f6f4 v[70:73], v[18:25], v[208:215], v[70:73], v194, v169 op_sel_hi:[0,0,0]
	v_mfma_scale_f32_16x16x128_f8f6f4 v[62:65], v[26:33], v[216:223], v[62:65], v194, v169 op_sel_hi:[0,0,0]
	v_mfma_scale_f32_16x16x128_f8f6f4 v[54:57], v[18:25], v[216:223], v[54:57], v194, v169 op_sel_hi:[0,0,0]
	v_mfma_scale_f32_16x16x128_f8f6f4 v[46:49], v[26:33], v[236:243], v[46:49], v194, v169 op_sel_hi:[0,0,0]
	v_mfma_scale_f32_16x16x128_f8f6f4 v[38:41], v[18:25], v[236:243], v[38:41], v194, v169 op_sel_hi:[0,0,0]
	s_setprio 0
	s_setprio 1
	v_mfma_scale_f32_16x16x128_f8f6f4 v[90:93], v[10:17], v[200:207], v[90:93], v194, v169 op_sel_hi:[0,0,0]
	v_mfma_scale_f32_16x16x128_f8f6f4 v[82:85], v[2:9], v[200:207], v[82:85], v194, v169 op_sel_hi:[0,0,0]
	v_mfma_scale_f32_16x16x128_f8f6f4 v[74:77], v[10:17], v[208:215], v[74:77], v194, v169 op_sel_hi:[0,0,0]
	v_mfma_scale_f32_16x16x128_f8f6f4 v[66:69], v[2:9], v[208:215], v[66:69], v194, v169 op_sel_hi:[0,0,0]
	v_mfma_scale_f32_16x16x128_f8f6f4 v[58:61], v[10:17], v[216:223], v[58:61], v194, v169 op_sel_hi:[0,0,0]
	v_mfma_scale_f32_16x16x128_f8f6f4 v[50:53], v[2:9], v[216:223], v[50:53], v194, v169 op_sel_hi:[0,0,0]
	v_mfma_scale_f32_16x16x128_f8f6f4 v[42:45], v[10:17], v[236:243], v[42:45], v194, v169 op_sel_hi:[0,0,0]
	v_mfma_scale_f32_16x16x128_f8f6f4 v[34:37], v[2:9], v[236:243], v[34:37], v194, v169 op_sel_hi:[0,0,0]
	s_setprio 0
	s_barrier
	s_add_i32 s68, 0, 0x18000
	s_add_i32 s69, 0, 0x1c000
	v_add_u32_e32 v2, s68, v196
	v_add_u32_e32 v6, s69, v196
	s_add_u32 s58, s58, 0x20000
	s_addc_u32 s59, s59, 0
	s_mov_b32 m0, s21
	v_lshl_add_u64 v[170:171], s[58:59], 0, v[164:165]
	global_load_lds_dwordx4 v[170:171], off
	v_lshl_add_u64 v[170:171], s[58:59], 0, v[162:163]
	s_mov_b32 m0, s22
	s_nop 0
	global_load_lds_dwordx4 v[170:171], off
	ds_read_b128 v[26:29], v2
	ds_read_b128 v[30:33], v2 offset:1024
	ds_read_b128 v[18:21], v2 offset:2048
	ds_read_b128 v[22:25], v2 offset:3072
	ds_read_b128 v[10:13], v6
	ds_read_b128 v[14:17], v6 offset:1024
	ds_read_b128 v[2:5], v6 offset:2048
	ds_read_b128 v[6:9], v6 offset:3072
	ds_read_b128 v[200:203], v198 offset:32768
	ds_read_b128 v[204:207], v198 offset:33792
	ds_read_b128 v[208:211], v198 offset:34816
	ds_read_b128 v[212:215], v198 offset:35840
	ds_read_b128 v[216:219], v198 offset:36864
	ds_read_b128 v[220:223], v198 offset:37888
	ds_read_b128 v[236:239], v198 offset:38912
	ds_read_b128 v[240:243], v198 offset:39936
	s_waitcnt vmcnt(8)
	s_waitcnt lgkmcnt(0)
	s_barrier
	s_setprio 1
	s_waitcnt lgkmcnt(0)
	v_mfma_scale_f32_16x16x128_f8f6f4 v[158:161], v[26:33], v[200:207], v[158:161], v194, v169 op_sel_hi:[0,0,0]
	v_mfma_scale_f32_16x16x128_f8f6f4 v[150:153], v[18:25], v[200:207], v[150:153], v194, v169 op_sel_hi:[0,0,0]
	v_mfma_scale_f32_16x16x128_f8f6f4 v[142:145], v[26:33], v[208:215], v[142:145], v194, v169 op_sel_hi:[0,0,0]
	v_mfma_scale_f32_16x16x128_f8f6f4 v[134:137], v[18:25], v[208:215], v[134:137], v194, v169 op_sel_hi:[0,0,0]
	v_mfma_scale_f32_16x16x128_f8f6f4 v[126:129], v[26:33], v[216:223], v[126:129], v194, v169 op_sel_hi:[0,0,0]
	v_mfma_scale_f32_16x16x128_f8f6f4 v[118:121], v[18:25], v[216:223], v[118:121], v194, v169 op_sel_hi:[0,0,0]
	v_mfma_scale_f32_16x16x128_f8f6f4 v[110:113], v[26:33], v[236:243], v[110:113], v194, v169 op_sel_hi:[0,0,0]
	v_mfma_scale_f32_16x16x128_f8f6f4 v[102:105], v[18:25], v[236:243], v[102:105], v194, v169 op_sel_hi:[0,0,0]
	s_setprio 0
	s_setprio 1
	v_mfma_scale_f32_16x16x128_f8f6f4 v[154:157], v[10:17], v[200:207], v[154:157], v194, v169 op_sel_hi:[0,0,0]
	v_mfma_scale_f32_16x16x128_f8f6f4 v[146:149], v[2:9], v[200:207], v[146:149], v194, v169 op_sel_hi:[0,0,0]
	v_mfma_scale_f32_16x16x128_f8f6f4 v[138:141], v[10:17], v[208:215], v[138:141], v194, v169 op_sel_hi:[0,0,0]
	v_mfma_scale_f32_16x16x128_f8f6f4 v[130:133], v[2:9], v[208:215], v[130:133], v194, v169 op_sel_hi:[0,0,0]
	v_mfma_scale_f32_16x16x128_f8f6f4 v[122:125], v[10:17], v[216:223], v[122:125], v194, v169 op_sel_hi:[0,0,0]
	v_mfma_scale_f32_16x16x128_f8f6f4 v[114:117], v[2:9], v[216:223], v[114:117], v194, v169 op_sel_hi:[0,0,0]
	v_mfma_scale_f32_16x16x128_f8f6f4 v[106:109], v[10:17], v[236:243], v[106:109], v194, v169 op_sel_hi:[0,0,0]
	v_mfma_scale_f32_16x16x128_f8f6f4 v[98:101], v[2:9], v[236:243], v[98:101], v194, v169 op_sel_hi:[0,0,0]
	s_setprio 0
	s_barrier
	s_add_i32 s58, s68, s14
	v_lshl_add_u64 v[170:171], v[186:187], 0, s[56:57]
	s_mov_b32 m0, s58
	s_nop 0
	global_load_lds_dwordx4 v[170:171], off
	s_add_i32 m0, s58, 0x2000
	s_add_u32 s54, s54, 0x20080
	v_lshl_add_u64 v[170:171], v[188:189], 0, s[56:57]
	s_addc_u32 s55, s55, 0
	s_add_i32 s58, s69, s14
	global_load_lds_dwordx4 v[170:171], off
	v_lshl_add_u64 v[170:171], s[54:55], 0, v[166:167]
	s_mov_b32 m0, s58
	s_nop 0
	global_load_lds_dwordx4 v[170:171], off
	v_lshl_add_u64 v[170:171], s[54:55], 0, v[178:179]
	s_add_i32 m0, s58, 0x2000
	s_nop 0
	global_load_lds_dwordx4 v[170:171], off
	v_lshl_add_u64 v[170:171], v[190:191], 0, s[56:57]
	s_mov_b32 m0, s23
	s_nop 0
	global_load_lds_dwordx4 v[170:171], off
	v_lshl_add_u64 v[170:171], v[192:193], 0, s[56:57]
	s_mov_b32 m0, s24
	s_nop 0
	global_load_lds_dwordx4 v[170:171], off
	ds_read_b128 v[200:203], v198 offset:49152
	ds_read_b128 v[204:207], v198 offset:50176
	ds_read_b128 v[208:211], v198 offset:51200
	ds_read_b128 v[212:215], v198 offset:52224
	ds_read_b128 v[216:219], v198 offset:53248
	ds_read_b128 v[220:223], v198 offset:54272
	ds_read_b128 v[236:239], v198 offset:55296
	ds_read_b128 v[240:243], v198 offset:56320
	s_waitcnt vmcnt(8)
	s_waitcnt lgkmcnt(0)
	s_barrier
	s_setprio 1
	s_waitcnt lgkmcnt(0)
	v_mfma_scale_f32_16x16x128_f8f6f4 v[94:97], v[26:33], v[200:207], v[94:97], v194, v169 op_sel_hi:[0,0,0]
	v_mfma_scale_f32_16x16x128_f8f6f4 v[86:89], v[18:25], v[200:207], v[86:89], v194, v169 op_sel_hi:[0,0,0]
	v_mfma_scale_f32_16x16x128_f8f6f4 v[78:81], v[26:33], v[208:215], v[78:81], v194, v169 op_sel_hi:[0,0,0]
	v_mfma_scale_f32_16x16x128_f8f6f4 v[70:73], v[18:25], v[208:215], v[70:73], v194, v169 op_sel_hi:[0,0,0]
	v_mfma_scale_f32_16x16x128_f8f6f4 v[62:65], v[26:33], v[216:223], v[62:65], v194, v169 op_sel_hi:[0,0,0]
	v_mfma_scale_f32_16x16x128_f8f6f4 v[54:57], v[18:25], v[216:223], v[54:57], v194, v169 op_sel_hi:[0,0,0]
	v_mfma_scale_f32_16x16x128_f8f6f4 v[46:49], v[26:33], v[236:243], v[46:49], v194, v169 op_sel_hi:[0,0,0]
	v_mfma_scale_f32_16x16x128_f8f6f4 v[38:41], v[18:25], v[236:243], v[38:41], v194, v169 op_sel_hi:[0,0,0]
	s_setprio 0
	s_setprio 1
	v_mfma_scale_f32_16x16x128_f8f6f4 v[90:93], v[10:17], v[200:207], v[90:93], v194, v169 op_sel_hi:[0,0,0]
	v_mfma_scale_f32_16x16x128_f8f6f4 v[82:85], v[2:9], v[200:207], v[82:85], v194, v169 op_sel_hi:[0,0,0]
	v_mfma_scale_f32_16x16x128_f8f6f4 v[74:77], v[10:17], v[208:215], v[74:77], v194, v169 op_sel_hi:[0,0,0]
	v_mfma_scale_f32_16x16x128_f8f6f4 v[66:69], v[2:9], v[208:215], v[66:69], v194, v169 op_sel_hi:[0,0,0]
	v_mfma_scale_f32_16x16x128_f8f6f4 v[58:61], v[10:17], v[216:223], v[58:61], v194, v169 op_sel_hi:[0,0,0]
	v_mfma_scale_f32_16x16x128_f8f6f4 v[50:53], v[2:9], v[216:223], v[50:53], v194, v169 op_sel_hi:[0,0,0]
	v_mfma_scale_f32_16x16x128_f8f6f4 v[42:45], v[10:17], v[236:243], v[42:45], v194, v169 op_sel_hi:[0,0,0]
	v_mfma_scale_f32_16x16x128_f8f6f4 v[34:37], v[2:9], v[236:243], v[34:37], v194, v169 op_sel_hi:[0,0,0]
	s_setprio 0
	s_barrier
	s_add_u32 s64, s64, 0x100
	s_addc_u32 s65, s65, 0
	s_add_u32 s52, s52, 0x100
	s_addc_u32 s53, s53, 0
	s_cmp_ge_i32 s66, s13
	s_mov_b32 s54, s66
	s_cbranch_scc0 .LBB0_842
	s_mov_b64 s[70:71], 0xe800800
	v_mov_b32_e32 v209, v1
	s_and_b64 vcc, exec, s[36:37]
	s_cbranch_vccz .LBB0_845

.LBB0_924:
	s_add_i32 s75, s62, 2
	s_add_u32 s60, s58, 0x100
	s_addc_u32 s61, s59, 0
	s_add_i32 s76, 0, 0x10000
	s_cmp_eq_u32 s68, s62
	s_cselect_b32 s65, s53, s61
	s_cselect_b32 s64, s52, s60
	s_cselect_b32 s63, s55, s74
	s_cselect_b32 s62, s54, s73
	s_add_i32 s77, 0, 0x14000
	v_add_u32_e32 v2, s76, v200
	v_add_u32_e32 v6, s77, v200
	v_lshl_add_u64 v[170:171], s[58:59], 0, v[184:185]
	s_add_i32 m0, s15, 0xc000
	s_nop 0
	global_load_lds_dwordx4 v[170:171], off
	v_lshl_add_u64 v[170:171], s[58:59], 0, v[182:183]
	s_add_i32 m0, s15, 0xe000
	s_nop 0
	global_load_lds_dwordx4 v[170:171], off
	ds_read_b128 v[26:29], v2
	ds_read_b128 v[30:33], v2 offset:1024
	ds_read_b128 v[18:21], v2 offset:2048
	ds_read_b128 v[22:25], v2 offset:3072
	ds_read_b128 v[10:13], v6
	ds_read_b128 v[14:17], v6 offset:1024
	s_waitcnt lgkmcnt(0)
	ds_read_b128 v[2:5], v6 offset:2048
	ds_read_b128 v[6:9], v6 offset:3072
	ds_read_b128 v[186:189], v204
	ds_read_b128 v[190:193], v204 offset:1024
	ds_read_b128 v[206:209], v204 offset:2048
	ds_read_b128 v[210:213], v204 offset:3072
	ds_read_b128 v[214:217], v204 offset:4096
	ds_read_b128 v[218:221], v204 offset:5120
	ds_read_b128 v[236:239], v204 offset:6144
	ds_read_b128 v[240:243], v204 offset:7168
	s_waitcnt vmcnt(8)
	s_waitcnt lgkmcnt(0)
	s_barrier
	s_setprio 1
	s_waitcnt lgkmcnt(0)
	v_mfma_scale_f32_16x16x128_f8f6f4 v[158:161], v[26:33], v[186:193], v[158:161], v198, v169 op_sel_hi:[0,0,0]
	v_mfma_scale_f32_16x16x128_f8f6f4 v[154:157], v[18:25], v[186:193], v[154:157], v198, v169 op_sel_hi:[0,0,0]
	v_mfma_scale_f32_16x16x128_f8f6f4 v[142:145], v[26:33], v[206:213], v[142:145], v198, v169 op_sel_hi:[0,0,0]
	v_mfma_scale_f32_16x16x128_f8f6f4 v[138:141], v[18:25], v[206:213], v[138:141], v198, v169 op_sel_hi:[0,0,0]
	v_mfma_scale_f32_16x16x128_f8f6f4 v[126:129], v[26:33], v[214:221], v[126:129], v198, v169 op_sel_hi:[0,0,0]
	v_mfma_scale_f32_16x16x128_f8f6f4 v[122:125], v[18:25], v[214:221], v[122:125], v198, v169 op_sel_hi:[0,0,0]
	v_mfma_scale_f32_16x16x128_f8f6f4 v[110:113], v[26:33], v[236:243], v[110:113], v198, v169 op_sel_hi:[0,0,0]
	v_mfma_scale_f32_16x16x128_f8f6f4 v[106:109], v[18:25], v[236:243], v[106:109], v198, v169 op_sel_hi:[0,0,0]
	s_setprio 0
	s_setprio 1
	v_mfma_scale_f32_16x16x128_f8f6f4 v[150:153], v[10:17], v[186:193], v[150:153], v198, v169 op_sel_hi:[0,0,0]
	v_mfma_scale_f32_16x16x128_f8f6f4 v[146:149], v[2:9], v[186:193], v[146:149], v198, v169 op_sel_hi:[0,0,0]
	v_mfma_scale_f32_16x16x128_f8f6f4 v[134:137], v[10:17], v[206:213], v[134:137], v198, v169 op_sel_hi:[0,0,0]
	v_mfma_scale_f32_16x16x128_f8f6f4 v[130:133], v[2:9], v[206:213], v[130:133], v198, v169 op_sel_hi:[0,0,0]
	v_mfma_scale_f32_16x16x128_f8f6f4 v[118:121], v[10:17], v[214:221], v[118:121], v198, v169 op_sel_hi:[0,0,0]
	v_mfma_scale_f32_16x16x128_f8f6f4 v[114:117], v[2:9], v[214:221], v[114:117], v198, v169 op_sel_hi:[0,0,0]
	v_mfma_scale_f32_16x16x128_f8f6f4 v[102:105], v[10:17], v[236:243], v[102:105], v198, v169 op_sel_hi:[0,0,0]
	v_mfma_scale_f32_16x16x128_f8f6f4 v[98:101], v[2:9], v[236:243], v[98:101], v198, v169 op_sel_hi:[0,0,0]
	s_setprio 0
	s_barrier
	s_add_i32 s58, s76, s14
	v_lshl_add_u64 v[186:187], s[62:63], 0, v[166:167]
	s_mov_b32 m0, s58
	s_nop 0
	global_load_lds_dwordx4 v[186:187], off
	s_add_i32 m0, s58, 0x2000
	s_add_u32 s58, s62, 0x70000
	v_lshl_add_u64 v[188:189], s[62:63], 0, v[162:163]
	s_addc_u32 s59, s63, 0
	s_add_i32 s76, s77, s14
	global_load_lds_dwordx4 v[188:189], off
	v_lshl_add_u64 v[170:171], s[58:59], 0, v[166:167]
	s_mov_b32 m0, s76
	v_lshl_add_u64 v[190:191], s[64:65], 0, v[164:165]
	global_load_lds_dwordx4 v[170:171], off
	v_lshl_add_u64 v[170:171], s[58:59], 0, v[162:163]
	s_add_i32 m0, s76, 0x2000
	v_lshl_add_u64 v[192:193], s[64:65], 0, v[178:179]
	global_load_lds_dwordx4 v[170:171], off
	s_mov_b32 m0, s15
	s_nop 0
	global_load_lds_dwordx4 v[190:191], off
	s_mov_b32 m0, s16
	s_nop 0
	global_load_lds_dwordx4 v[192:193], off
	ds_read_b128 v[206:209], v204 offset:16384
	ds_read_b128 v[210:213], v204 offset:17408
	ds_read_b128 v[214:217], v204 offset:18432
	ds_read_b128 v[218:221], v204 offset:19456
	ds_read_b128 v[236:239], v204 offset:20480
	ds_read_b128 v[240:243], v204 offset:21504
	ds_read_b128 v[244:247], v204 offset:22528
	ds_read_b128 v[248:251], v204 offset:23552
	s_waitcnt vmcnt(8)
	s_waitcnt lgkmcnt(0)
	s_barrier
	s_setprio 1
	s_waitcnt lgkmcnt(0)
	v_mfma_scale_f32_16x16x128_f8f6f4 v[94:97], v[26:33], v[206:213], v[94:97], v198, v169 op_sel_hi:[0,0,0]
	v_mfma_scale_f32_16x16x128_f8f6f4 v[90:93], v[18:25], v[206:213], v[90:93], v198, v169 op_sel_hi:[0,0,0]
	v_mfma_scale_f32_16x16x128_f8f6f4 v[78:81], v[26:33], v[214:221], v[78:81], v198, v169 op_sel_hi:[0,0,0]
	v_mfma_scale_f32_16x16x128_f8f6f4 v[74:77], v[18:25], v[214:221], v[74:77], v198, v169 op_sel_hi:[0,0,0]
	v_mfma_scale_f32_16x16x128_f8f6f4 v[62:65], v[26:33], v[236:243], v[62:65], v198, v169 op_sel_hi:[0,0,0]
	v_mfma_scale_f32_16x16x128_f8f6f4 v[58:61], v[18:25], v[236:243], v[58:61], v198, v169 op_sel_hi:[0,0,0]
	v_mfma_scale_f32_16x16x128_f8f6f4 v[46:49], v[26:33], v[244:251], v[46:49], v198, v169 op_sel_hi:[0,0,0]
	v_mfma_scale_f32_16x16x128_f8f6f4 v[42:45], v[18:25], v[244:251], v[42:45], v198, v169 op_sel_hi:[0,0,0]
	s_setprio 0
	s_setprio 1
	v_mfma_scale_f32_16x16x128_f8f6f4 v[86:89], v[10:17], v[206:213], v[86:89], v198, v169 op_sel_hi:[0,0,0]
	v_mfma_scale_f32_16x16x128_f8f6f4 v[82:85], v[2:9], v[206:213], v[82:85], v198, v169 op_sel_hi:[0,0,0]
	v_mfma_scale_f32_16x16x128_f8f6f4 v[70:73], v[10:17], v[214:221], v[70:73], v198, v169 op_sel_hi:[0,0,0]
	v_mfma_scale_f32_16x16x128_f8f6f4 v[66:69], v[2:9], v[214:221], v[66:69], v198, v169 op_sel_hi:[0,0,0]
	v_mfma_scale_f32_16x16x128_f8f6f4 v[54:57], v[10:17], v[236:243], v[54:57], v198, v169 op_sel_hi:[0,0,0]
	v_mfma_scale_f32_16x16x128_f8f6f4 v[50:53], v[2:9], v[236:243], v[50:53], v198, v169 op_sel_hi:[0,0,0]
	v_mfma_scale_f32_16x16x128_f8f6f4 v[38:41], v[10:17], v[244:251], v[38:41], v198, v169 op_sel_hi:[0,0,0]
	v_mfma_scale_f32_16x16x128_f8f6f4 v[34:37], v[2:9], v[244:251], v[34:37], v198, v169 op_sel_hi:[0,0,0]
	s_setprio 0
	s_barrier
	s_add_i32 s76, 0, 0x18000
	s_add_i32 s77, 0, 0x1c000
	v_add_u32_e32 v2, s76, v200
	v_add_u32_e32 v6, s77, v200
	s_add_u32 s58, s64, 0x70000
	s_addc_u32 s59, s65, 0
	s_mov_b32 m0, s20
	v_lshl_add_u64 v[170:171], s[58:59], 0, v[164:165]
	global_load_lds_dwordx4 v[170:171], off
	v_lshl_add_u64 v[170:171], s[58:59], 0, v[178:179]
	s_mov_b32 m0, s21
	s_nop 0
	global_load_lds_dwordx4 v[170:171], off
	ds_read_b128 v[26:29], v2
	ds_read_b128 v[30:33], v2 offset:1024
	ds_read_b128 v[18:21], v2 offset:2048
	ds_read_b128 v[22:25], v2 offset:3072
	ds_read_b128 v[10:13], v6
	ds_read_b128 v[14:17], v6 offset:1024
	ds_read_b128 v[2:5], v6 offset:2048
	ds_read_b128 v[6:9], v6 offset:3072
	ds_read_b128 v[206:209], v204 offset:32768
	ds_read_b128 v[210:213], v204 offset:33792
	ds_read_b128 v[214:217], v204 offset:34816
	ds_read_b128 v[218:221], v204 offset:35840
	ds_read_b128 v[236:239], v204 offset:36864
	ds_read_b128 v[240:243], v204 offset:37888
	ds_read_b128 v[244:247], v204 offset:38912
	ds_read_b128 v[248:251], v204 offset:39936
	s_waitcnt vmcnt(8)
	s_waitcnt lgkmcnt(0)
	s_barrier
	s_setprio 1
	s_waitcnt lgkmcnt(0)
	v_mfma_scale_f32_16x16x128_f8f6f4 v[158:161], v[26:33], v[206:213], v[158:161], v198, v169 op_sel_hi:[0,0,0]
	v_mfma_scale_f32_16x16x128_f8f6f4 v[154:157], v[18:25], v[206:213], v[154:157], v198, v169 op_sel_hi:[0,0,0]
	v_mfma_scale_f32_16x16x128_f8f6f4 v[142:145], v[26:33], v[214:221], v[142:145], v198, v169 op_sel_hi:[0,0,0]
	v_mfma_scale_f32_16x16x128_f8f6f4 v[138:141], v[18:25], v[214:221], v[138:141], v198, v169 op_sel_hi:[0,0,0]
	v_mfma_scale_f32_16x16x128_f8f6f4 v[126:129], v[26:33], v[236:243], v[126:129], v198, v169 op_sel_hi:[0,0,0]
	v_mfma_scale_f32_16x16x128_f8f6f4 v[122:125], v[18:25], v[236:243], v[122:125], v198, v169 op_sel_hi:[0,0,0]
	v_mfma_scale_f32_16x16x128_f8f6f4 v[110:113], v[26:33], v[244:251], v[110:113], v198, v169 op_sel_hi:[0,0,0]
	v_mfma_scale_f32_16x16x128_f8f6f4 v[106:109], v[18:25], v[244:251], v[106:109], v198, v169 op_sel_hi:[0,0,0]
	s_setprio 0
	s_setprio 1
	v_mfma_scale_f32_16x16x128_f8f6f4 v[150:153], v[10:17], v[206:213], v[150:153], v198, v169 op_sel_hi:[0,0,0]
	v_mfma_scale_f32_16x16x128_f8f6f4 v[146:149], v[2:9], v[206:213], v[146:149], v198, v169 op_sel_hi:[0,0,0]
	v_mfma_scale_f32_16x16x128_f8f6f4 v[134:137], v[10:17], v[214:221], v[134:137], v198, v169 op_sel_hi:[0,0,0]
	v_mfma_scale_f32_16x16x128_f8f6f4 v[130:133], v[2:9], v[214:221], v[130:133], v198, v169 op_sel_hi:[0,0,0]
	v_mfma_scale_f32_16x16x128_f8f6f4 v[118:121], v[10:17], v[236:243], v[118:121], v198, v169 op_sel_hi:[0,0,0]
	v_mfma_scale_f32_16x16x128_f8f6f4 v[114:117], v[2:9], v[236:243], v[114:117], v198, v169 op_sel_hi:[0,0,0]
	v_mfma_scale_f32_16x16x128_f8f6f4 v[102:105], v[10:17], v[244:251], v[102:105], v198, v169 op_sel_hi:[0,0,0]
	v_mfma_scale_f32_16x16x128_f8f6f4 v[98:101], v[2:9], v[244:251], v[98:101], v198, v169 op_sel_hi:[0,0,0]
	s_setprio 0
	s_barrier
	s_add_i32 s58, s76, s14
	v_lshl_add_u64 v[170:171], v[186:187], 0, s[56:57]
	s_mov_b32 m0, s58
	s_nop 0
	global_load_lds_dwordx4 v[170:171], off
	s_add_i32 m0, s58, 0x2000
	s_add_u32 s58, s62, 0x70080
	v_lshl_add_u64 v[170:171], v[188:189], 0, s[56:57]
	s_addc_u32 s59, s63, 0
	s_add_i32 s62, s77, s14
	global_load_lds_dwordx4 v[170:171], off
	v_lshl_add_u64 v[170:171], s[58:59], 0, v[166:167]
	s_mov_b32 m0, s62
	s_nop 0
	global_load_lds_dwordx4 v[170:171], off
	v_lshl_add_u64 v[170:171], s[58:59], 0, v[162:163]
	s_add_i32 m0, s62, 0x2000
	s_nop 0
	global_load_lds_dwordx4 v[170:171], off
	v_lshl_add_u64 v[170:171], v[190:191], 0, s[56:57]
	s_mov_b32 m0, s24
	s_nop 0
	global_load_lds_dwordx4 v[170:171], off
	v_lshl_add_u64 v[170:171], v[192:193], 0, s[56:57]
	s_mov_b32 m0, s25
	s_nop 0
	global_load_lds_dwordx4 v[170:171], off
	ds_read_b128 v[206:209], v204 offset:49152
	ds_read_b128 v[210:213], v204 offset:50176
	ds_read_b128 v[214:217], v204 offset:51200
	ds_read_b128 v[218:221], v204 offset:52224
	ds_read_b128 v[236:239], v204 offset:53248
	ds_read_b128 v[240:243], v204 offset:54272
	ds_read_b128 v[244:247], v204 offset:55296
	ds_read_b128 v[248:251], v204 offset:56320
	s_waitcnt vmcnt(8)
	s_waitcnt lgkmcnt(0)
	s_barrier
	s_setprio 1
	s_waitcnt lgkmcnt(0)
	v_mfma_scale_f32_16x16x128_f8f6f4 v[94:97], v[26:33], v[206:213], v[94:97], v198, v169 op_sel_hi:[0,0,0]
	v_mfma_scale_f32_16x16x128_f8f6f4 v[90:93], v[18:25], v[206:213], v[90:93], v198, v169 op_sel_hi:[0,0,0]
	v_mfma_scale_f32_16x16x128_f8f6f4 v[78:81], v[26:33], v[214:221], v[78:81], v198, v169 op_sel_hi:[0,0,0]
	v_mfma_scale_f32_16x16x128_f8f6f4 v[74:77], v[18:25], v[214:221], v[74:77], v198, v169 op_sel_hi:[0,0,0]
	v_mfma_scale_f32_16x16x128_f8f6f4 v[62:65], v[26:33], v[236:243], v[62:65], v198, v169 op_sel_hi:[0,0,0]
	v_mfma_scale_f32_16x16x128_f8f6f4 v[58:61], v[18:25], v[236:243], v[58:61], v198, v169 op_sel_hi:[0,0,0]
	v_mfma_scale_f32_16x16x128_f8f6f4 v[46:49], v[26:33], v[244:251], v[46:49], v198, v169 op_sel_hi:[0,0,0]
	v_mfma_scale_f32_16x16x128_f8f6f4 v[42:45], v[18:25], v[244:251], v[42:45], v198, v169 op_sel_hi:[0,0,0]
	s_setprio 0
	s_setprio 1
	v_mfma_scale_f32_16x16x128_f8f6f4 v[86:89], v[10:17], v[206:213], v[86:89], v198, v169 op_sel_hi:[0,0,0]
	v_mfma_scale_f32_16x16x128_f8f6f4 v[82:85], v[2:9], v[206:213], v[82:85], v198, v169 op_sel_hi:[0,0,0]
	v_mfma_scale_f32_16x16x128_f8f6f4 v[70:73], v[10:17], v[214:221], v[70:73], v198, v169 op_sel_hi:[0,0,0]
	v_mfma_scale_f32_16x16x128_f8f6f4 v[66:69], v[2:9], v[214:221], v[66:69], v198, v169 op_sel_hi:[0,0,0]
	v_mfma_scale_f32_16x16x128_f8f6f4 v[54:57], v[10:17], v[236:243], v[54:57], v198, v169 op_sel_hi:[0,0,0]
	v_mfma_scale_f32_16x16x128_f8f6f4 v[50:53], v[2:9], v[236:243], v[50:53], v198, v169 op_sel_hi:[0,0,0]
	v_mfma_scale_f32_16x16x128_f8f6f4 v[38:41], v[10:17], v[244:251], v[38:41], v198, v169 op_sel_hi:[0,0,0]
	v_mfma_scale_f32_16x16x128_f8f6f4 v[34:37], v[2:9], v[244:251], v[34:37], v198, v169 op_sel_hi:[0,0,0]
	s_setprio 0
	s_barrier
	s_add_u32 s73, s73, 0x100
	s_addc_u32 s74, s74, 0
	s_cmp_ge_i32 s75, s1
	s_mov_b64 s[58:59], s[60:61]
	s_mov_b32 s62, s75
	s_cbranch_scc0 .LBB0_924
	v_mov_b32_e32 v209, v1
	s_and_b64 vcc, exec, s[46:47]
	s_cbranch_vccz .LBB0_927

.LBB0_1016:
	s_add_i32 s27, s37, 2
	s_add_u32 s40, s38, 0xfffe0080
	s_addc_u32 s41, s39, -1
	s_add_i32 s65, 0, 0x10000
	s_cmp_eq_u32 s95, s37
	s_cselect_b32 s69, s0, s41
	s_cselect_b32 s68, s1, s40
	s_cselect_b32 s41, s8, s19
	s_cselect_b32 s40, s11, s16
	s_add_i32 s37, 0, 0x14000
	v_add_u32_e32 v2, s65, v221
	v_add_u32_e32 v6, s37, v221
	v_lshl_add_u64 v[170:171], s[38:39], 0, v[192:193]
	s_add_i32 m0, s21, 0xc000
	s_nop 0
	global_load_lds_dwordx4 v[170:171], off
	v_lshl_add_u64 v[170:171], s[38:39], 0, v[190:191]
	s_add_i32 m0, s21, 0xe000
	s_nop 0
	global_load_lds_dwordx4 v[170:171], off
	ds_read_b128 v[26:29], v2
	ds_read_b128 v[30:33], v2 offset:1024
	ds_read_b128 v[18:21], v2 offset:2048
	ds_read_b128 v[22:25], v2 offset:3072
	ds_read_b128 v[10:13], v6
	ds_read_b128 v[14:17], v6 offset:1024
	ds_read_b128 v[2:5], v6 offset:2048
	ds_read_b128 v[6:9], v6 offset:3072
	ds_read_b128 v[194:197], v222
	ds_read_b128 v[198:201], v222 offset:1024
	ds_read_b128 v[202:205], v222 offset:2048
	ds_read_b128 v[206:209], v222 offset:3072
	ds_read_b128 v[210:213], v222 offset:4096
	ds_read_b128 v[214:217], v222 offset:5120
	ds_read_b128 v[236:239], v222 offset:6144
	ds_read_b128 v[240:243], v222 offset:7168
	s_waitcnt vmcnt(8)
	s_waitcnt lgkmcnt(0)
	s_barrier
	s_setprio 1
	s_waitcnt lgkmcnt(0)
	v_mfma_scale_f32_16x16x128_f8f6f4 v[94:97], v[26:33], v[194:201], v[94:97], v183, v169 op_sel_hi:[0,0,0]
	v_mfma_scale_f32_16x16x128_f8f6f4 v[90:93], v[18:25], v[194:201], v[90:93], v183, v169 op_sel_hi:[0,0,0]
	v_mfma_scale_f32_16x16x128_f8f6f4 v[86:89], v[26:33], v[202:209], v[86:89], v183, v169 op_sel_hi:[0,0,0]
	v_mfma_scale_f32_16x16x128_f8f6f4 v[82:85], v[18:25], v[202:209], v[82:85], v183, v169 op_sel_hi:[0,0,0]
	v_mfma_scale_f32_16x16x128_f8f6f4 v[78:81], v[26:33], v[210:217], v[78:81], v183, v169 op_sel_hi:[0,0,0]
	v_mfma_scale_f32_16x16x128_f8f6f4 v[74:77], v[18:25], v[210:217], v[74:77], v183, v169 op_sel_hi:[0,0,0]
	v_mfma_scale_f32_16x16x128_f8f6f4 v[70:73], v[26:33], v[236:243], v[70:73], v183, v169 op_sel_hi:[0,0,0]
	v_mfma_scale_f32_16x16x128_f8f6f4 v[66:69], v[18:25], v[236:243], v[66:69], v183, v169 op_sel_hi:[0,0,0]
	s_setprio 0
	s_setprio 1
	v_mfma_scale_f32_16x16x128_f8f6f4 v[158:161], v[10:17], v[194:201], v[158:161], v183, v169 op_sel_hi:[0,0,0]
	v_mfma_scale_f32_16x16x128_f8f6f4 v[154:157], v[2:9], v[194:201], v[154:157], v183, v169 op_sel_hi:[0,0,0]
	v_mfma_scale_f32_16x16x128_f8f6f4 v[150:153], v[10:17], v[202:209], v[150:153], v183, v169 op_sel_hi:[0,0,0]
	v_mfma_scale_f32_16x16x128_f8f6f4 v[146:149], v[2:9], v[202:209], v[146:149], v183, v169 op_sel_hi:[0,0,0]
	v_mfma_scale_f32_16x16x128_f8f6f4 v[142:145], v[10:17], v[210:217], v[142:145], v183, v169 op_sel_hi:[0,0,0]
	v_mfma_scale_f32_16x16x128_f8f6f4 v[138:141], v[2:9], v[210:217], v[138:141], v183, v169 op_sel_hi:[0,0,0]
	v_mfma_scale_f32_16x16x128_f8f6f4 v[134:137], v[10:17], v[236:243], v[134:137], v183, v169 op_sel_hi:[0,0,0]
	v_mfma_scale_f32_16x16x128_f8f6f4 v[130:133], v[2:9], v[236:243], v[130:133], v183, v169 op_sel_hi:[0,0,0]
	s_setprio 0
	s_barrier
	s_add_i32 s65, s65, s20
	v_lshl_add_u64 v[194:195], s[40:41], 0, v[162:163]
	s_mov_b32 m0, s65
	s_nop 0
	global_load_lds_dwordx4 v[194:195], off
	s_add_i32 m0, s65, 0x2000
	s_add_u32 s70, s40, 0x20000
	v_lshl_add_u64 v[196:197], s[40:41], 0, v[164:165]
	s_addc_u32 s71, s41, 0
	s_add_i32 s37, s37, s20
	global_load_lds_dwordx4 v[196:197], off
	v_lshl_add_u64 v[170:171], s[70:71], 0, v[162:163]
	s_mov_b32 m0, s37
	v_lshl_add_u64 v[198:199], s[68:69], 0, v[178:179]
	global_load_lds_dwordx4 v[170:171], off
	v_lshl_add_u64 v[170:171], s[70:71], 0, v[164:165]
	s_add_i32 m0, s37, 0x2000
	v_lshl_add_u64 v[200:201], s[68:69], 0, v[180:181]
	global_load_lds_dwordx4 v[170:171], off
	s_mov_b32 m0, s21
	s_nop 0
	global_load_lds_dwordx4 v[198:199], off
	s_mov_b32 m0, s22
	s_nop 0
	global_load_lds_dwordx4 v[200:201], off
	ds_read_b128 v[202:205], v222 offset:16384
	ds_read_b128 v[206:209], v222 offset:17408
	ds_read_b128 v[210:213], v222 offset:18432
	ds_read_b128 v[214:217], v222 offset:19456
	ds_read_b128 v[236:239], v222 offset:20480
	ds_read_b128 v[240:243], v222 offset:21504
	ds_read_b128 v[244:247], v222 offset:22528
	ds_read_b128 v[248:251], v222 offset:23552
	s_waitcnt vmcnt(8)
	s_waitcnt lgkmcnt(0)
	s_barrier
	s_setprio 1
	s_waitcnt lgkmcnt(0)
	v_mfma_scale_f32_16x16x128_f8f6f4 v[62:65], v[26:33], v[202:209], v[62:65], v183, v169 op_sel_hi:[0,0,0]
	v_mfma_scale_f32_16x16x128_f8f6f4 v[58:61], v[18:25], v[202:209], v[58:61], v183, v169 op_sel_hi:[0,0,0]
	v_mfma_scale_f32_16x16x128_f8f6f4 v[54:57], v[26:33], v[210:217], v[54:57], v183, v169 op_sel_hi:[0,0,0]
	v_mfma_scale_f32_16x16x128_f8f6f4 v[50:53], v[18:25], v[210:217], v[50:53], v183, v169 op_sel_hi:[0,0,0]
	v_mfma_scale_f32_16x16x128_f8f6f4 v[46:49], v[26:33], v[236:243], v[46:49], v183, v169 op_sel_hi:[0,0,0]
	v_mfma_scale_f32_16x16x128_f8f6f4 v[42:45], v[18:25], v[236:243], v[42:45], v183, v169 op_sel_hi:[0,0,0]
	v_mfma_scale_f32_16x16x128_f8f6f4 v[38:41], v[26:33], v[244:251], v[38:41], v183, v169 op_sel_hi:[0,0,0]
	v_mfma_scale_f32_16x16x128_f8f6f4 v[34:37], v[18:25], v[244:251], v[34:37], v183, v169 op_sel_hi:[0,0,0]
	s_setprio 0
	s_setprio 1
	v_mfma_scale_f32_16x16x128_f8f6f4 v[126:129], v[10:17], v[202:209], v[126:129], v183, v169 op_sel_hi:[0,0,0]
	v_mfma_scale_f32_16x16x128_f8f6f4 v[122:125], v[2:9], v[202:209], v[122:125], v183, v169 op_sel_hi:[0,0,0]
	v_mfma_scale_f32_16x16x128_f8f6f4 v[118:121], v[10:17], v[210:217], v[118:121], v183, v169 op_sel_hi:[0,0,0]
	v_mfma_scale_f32_16x16x128_f8f6f4 v[114:117], v[2:9], v[210:217], v[114:117], v183, v169 op_sel_hi:[0,0,0]
	v_mfma_scale_f32_16x16x128_f8f6f4 v[110:113], v[10:17], v[236:243], v[110:113], v183, v169 op_sel_hi:[0,0,0]
	v_mfma_scale_f32_16x16x128_f8f6f4 v[106:109], v[2:9], v[236:243], v[106:109], v183, v169 op_sel_hi:[0,0,0]
	v_mfma_scale_f32_16x16x128_f8f6f4 v[102:105], v[10:17], v[244:251], v[102:105], v183, v169 op_sel_hi:[0,0,0]
	v_mfma_scale_f32_16x16x128_f8f6f4 v[98:101], v[2:9], v[244:251], v[98:101], v183, v169 op_sel_hi:[0,0,0]
	s_setprio 0
	s_barrier
	s_add_i32 s37, 0, 0x18000
	s_add_i32 s65, 0, 0x1c000
	v_add_u32_e32 v2, s37, v221
	v_add_u32_e32 v6, s65, v221
	s_add_u32 s68, s68, 0x20000
	s_addc_u32 s69, s69, 0
	s_mov_b32 m0, s23
	v_lshl_add_u64 v[170:171], s[68:69], 0, v[178:179]
	global_load_lds_dwordx4 v[170:171], off
	v_lshl_add_u64 v[170:171], s[68:69], 0, v[180:181]
	s_mov_b32 m0, s12
	s_nop 0
	global_load_lds_dwordx4 v[170:171], off
	ds_read_b128 v[26:29], v2
	ds_read_b128 v[30:33], v2 offset:1024
	ds_read_b128 v[18:21], v2 offset:2048
	ds_read_b128 v[22:25], v2 offset:3072
	ds_read_b128 v[10:13], v6
	ds_read_b128 v[14:17], v6 offset:1024
	ds_read_b128 v[2:5], v6 offset:2048
	ds_read_b128 v[6:9], v6 offset:3072
	ds_read_b128 v[202:205], v222 offset:32768
	ds_read_b128 v[206:209], v222 offset:33792
	ds_read_b128 v[210:213], v222 offset:34816
	ds_read_b128 v[214:217], v222 offset:35840
	ds_read_b128 v[236:239], v222 offset:36864
	ds_read_b128 v[240:243], v222 offset:37888
	ds_read_b128 v[244:247], v222 offset:38912
	ds_read_b128 v[248:251], v222 offset:39936
	s_waitcnt vmcnt(8)
	s_waitcnt lgkmcnt(0)
	s_barrier
	s_setprio 1
	s_waitcnt lgkmcnt(0)
	v_mfma_scale_f32_16x16x128_f8f6f4 v[94:97], v[26:33], v[202:209], v[94:97], v183, v169 op_sel_hi:[0,0,0]
	v_mfma_scale_f32_16x16x128_f8f6f4 v[90:93], v[18:25], v[202:209], v[90:93], v183, v169 op_sel_hi:[0,0,0]
	v_mfma_scale_f32_16x16x128_f8f6f4 v[86:89], v[26:33], v[210:217], v[86:89], v183, v169 op_sel_hi:[0,0,0]
	v_mfma_scale_f32_16x16x128_f8f6f4 v[82:85], v[18:25], v[210:217], v[82:85], v183, v169 op_sel_hi:[0,0,0]
	v_mfma_scale_f32_16x16x128_f8f6f4 v[78:81], v[26:33], v[236:243], v[78:81], v183, v169 op_sel_hi:[0,0,0]
	v_mfma_scale_f32_16x16x128_f8f6f4 v[74:77], v[18:25], v[236:243], v[74:77], v183, v169 op_sel_hi:[0,0,0]
	v_mfma_scale_f32_16x16x128_f8f6f4 v[70:73], v[26:33], v[244:251], v[70:73], v183, v169 op_sel_hi:[0,0,0]
	v_mfma_scale_f32_16x16x128_f8f6f4 v[66:69], v[18:25], v[244:251], v[66:69], v183, v169 op_sel_hi:[0,0,0]
	s_setprio 0
	s_setprio 1
	v_mfma_scale_f32_16x16x128_f8f6f4 v[158:161], v[10:17], v[202:209], v[158:161], v183, v169 op_sel_hi:[0,0,0]
	v_mfma_scale_f32_16x16x128_f8f6f4 v[154:157], v[2:9], v[202:209], v[154:157], v183, v169 op_sel_hi:[0,0,0]
	v_mfma_scale_f32_16x16x128_f8f6f4 v[150:153], v[10:17], v[210:217], v[150:153], v183, v169 op_sel_hi:[0,0,0]
	v_mfma_scale_f32_16x16x128_f8f6f4 v[146:149], v[2:9], v[210:217], v[146:149], v183, v169 op_sel_hi:[0,0,0]
	v_mfma_scale_f32_16x16x128_f8f6f4 v[142:145], v[10:17], v[236:243], v[142:145], v183, v169 op_sel_hi:[0,0,0]
	v_mfma_scale_f32_16x16x128_f8f6f4 v[138:141], v[2:9], v[236:243], v[138:141], v183, v169 op_sel_hi:[0,0,0]
	v_mfma_scale_f32_16x16x128_f8f6f4 v[134:137], v[10:17], v[244:251], v[134:137], v183, v169 op_sel_hi:[0,0,0]
	v_mfma_scale_f32_16x16x128_f8f6f4 v[130:133], v[2:9], v[244:251], v[130:133], v183, v169 op_sel_hi:[0,0,0]
	s_setprio 0
	s_barrier
	s_add_i32 s37, s37, s20
	v_lshl_add_u64 v[170:171], v[194:195], 0, s[56:57]
	s_mov_b32 m0, s37
	s_nop 0
	global_load_lds_dwordx4 v[170:171], off
	s_add_i32 m0, s37, 0x2000
	s_add_u32 s40, s40, 0x20080
	v_lshl_add_u64 v[170:171], v[196:197], 0, s[56:57]
	s_addc_u32 s41, s41, 0
	s_add_i32 s37, s65, s20
	global_load_lds_dwordx4 v[170:171], off
	v_lshl_add_u64 v[170:171], s[40:41], 0, v[162:163]
	s_mov_b32 m0, s37
	s_nop 0
	global_load_lds_dwordx4 v[170:171], off
	v_lshl_add_u64 v[170:171], s[40:41], 0, v[164:165]
	s_add_i32 m0, s37, 0x2000
	s_nop 0
	global_load_lds_dwordx4 v[170:171], off
	v_lshl_add_u64 v[170:171], v[198:199], 0, s[56:57]
	s_mov_b32 m0, s92
	s_nop 0
	global_load_lds_dwordx4 v[170:171], off
	v_lshl_add_u64 v[170:171], v[200:201], 0, s[56:57]
	s_mov_b32 m0, s93
	s_nop 0
	global_load_lds_dwordx4 v[170:171], off
	ds_read_b128 v[202:205], v222 offset:49152
	ds_read_b128 v[206:209], v222 offset:50176
	ds_read_b128 v[210:213], v222 offset:51200
	ds_read_b128 v[214:217], v222 offset:52224
	ds_read_b128 v[236:239], v222 offset:53248
	ds_read_b128 v[240:243], v222 offset:54272
	ds_read_b128 v[244:247], v222 offset:55296
	ds_read_b128 v[248:251], v222 offset:56320
	s_waitcnt vmcnt(8)
	s_waitcnt lgkmcnt(0)
	s_barrier
	s_setprio 1
	s_waitcnt lgkmcnt(0)
	v_mfma_scale_f32_16x16x128_f8f6f4 v[62:65], v[26:33], v[202:209], v[62:65], v183, v169 op_sel_hi:[0,0,0]
	v_mfma_scale_f32_16x16x128_f8f6f4 v[58:61], v[18:25], v[202:209], v[58:61], v183, v169 op_sel_hi:[0,0,0]
	v_mfma_scale_f32_16x16x128_f8f6f4 v[54:57], v[26:33], v[210:217], v[54:57], v183, v169 op_sel_hi:[0,0,0]
	v_mfma_scale_f32_16x16x128_f8f6f4 v[50:53], v[18:25], v[210:217], v[50:53], v183, v169 op_sel_hi:[0,0,0]
	v_mfma_scale_f32_16x16x128_f8f6f4 v[46:49], v[26:33], v[236:243], v[46:49], v183, v169 op_sel_hi:[0,0,0]
	v_mfma_scale_f32_16x16x128_f8f6f4 v[42:45], v[18:25], v[236:243], v[42:45], v183, v169 op_sel_hi:[0,0,0]
	v_mfma_scale_f32_16x16x128_f8f6f4 v[38:41], v[26:33], v[244:251], v[38:41], v183, v169 op_sel_hi:[0,0,0]
	v_mfma_scale_f32_16x16x128_f8f6f4 v[34:37], v[18:25], v[244:251], v[34:37], v183, v169 op_sel_hi:[0,0,0]
	s_setprio 0
	s_setprio 1
	v_mfma_scale_f32_16x16x128_f8f6f4 v[126:129], v[10:17], v[202:209], v[126:129], v183, v169 op_sel_hi:[0,0,0]
	v_mfma_scale_f32_16x16x128_f8f6f4 v[122:125], v[2:9], v[202:209], v[122:125], v183, v169 op_sel_hi:[0,0,0]
	v_mfma_scale_f32_16x16x128_f8f6f4 v[118:121], v[10:17], v[210:217], v[118:121], v183, v169 op_sel_hi:[0,0,0]
	v_mfma_scale_f32_16x16x128_f8f6f4 v[114:117], v[2:9], v[210:217], v[114:117], v183, v169 op_sel_hi:[0,0,0]
	v_mfma_scale_f32_16x16x128_f8f6f4 v[110:113], v[10:17], v[236:243], v[110:113], v183, v169 op_sel_hi:[0,0,0]
	v_mfma_scale_f32_16x16x128_f8f6f4 v[106:109], v[2:9], v[236:243], v[106:109], v183, v169 op_sel_hi:[0,0,0]
	v_mfma_scale_f32_16x16x128_f8f6f4 v[102:105], v[10:17], v[244:251], v[102:105], v183, v169 op_sel_hi:[0,0,0]
	v_mfma_scale_f32_16x16x128_f8f6f4 v[98:101], v[2:9], v[244:251], v[98:101], v183, v169 op_sel_hi:[0,0,0]
	s_setprio 0
	s_barrier
	s_add_u32 s16, s16, 0x100
	s_addc_u32 s19, s19, 0
	s_add_u32 s38, s38, 0x100
	s_addc_u32 s39, s39, 0
	s_cmp_ge_i32 s27, s74
	s_mov_b32 s37, s27
	s_cbranch_scc0 .LBB0_1016
	s_mov_b64 s[70:71], 0xe800800
	v_mov_b32_e32 v209, v1
	s_and_b64 vcc, exec, s[52:53]
	s_cbranch_vccz .LBB0_1019

.LBB0_1438:
	s_add_i32 s66, s54, 2
	s_add_u32 s55, s52, 0xfffc0080
	s_addc_u32 s58, s53, -1
	s_add_i32 s68, 0, 0x10000
	s_cmp_eq_u32 s60, s54
	s_cselect_b32 s59, s41, s58
	s_cselect_b32 s58, s43, s55
	v_add_u32_e32 v144, s68, v147
	s_cselect_b32 s55, s62, s65
	s_cselect_b32 s54, s63, s64
	s_add_i32 s70, 0, 0x14000
	ds_read_b128 v[140:143], v144
	ds_read_b128 v[150:153], v144 offset:1024
	ds_read_b128 v[154:157], v144 offset:2048
	ds_read_b128 v[158:161], v144 offset:3072
	v_add_u32_e32 v144, s70, v147
	ds_read_b128 v[162:165], v144
	ds_read_b128 v[170:173], v144 offset:1024
	ds_read_b128 v[174:177], v144 offset:2048
	ds_read_b128 v[178:181], v144 offset:3072
	v_lshl_add_u64 v[144:145], s[52:53], 0, v[138:139]
	s_add_i32 m0, s16, 0xc000
	ds_read_b128 v[182:185], v149
	ds_read_b128 v[186:189], v149 offset:1024
	ds_read_b128 v[190:193], v149 offset:2048
	ds_read_b128 v[194:197], v149 offset:3072
	ds_read_b128 v[198:201], v149 offset:4096
	ds_read_b128 v[202:205], v149 offset:5120
	ds_read_b128 v[206:209], v149 offset:6144
	ds_read_b128 v[210:213], v149 offset:7168
	global_load_lds_dwordx4 v[144:145], off
	v_lshl_add_u64 v[144:145], s[52:53], 0, v[136:137]
	s_add_i32 m0, s16, 0xe000
	s_nop 0
	global_load_lds_dwordx4 v[144:145], off
	s_waitcnt vmcnt(8)
	s_waitcnt lgkmcnt(0)
	s_barrier
	s_setprio 1
	s_waitcnt lgkmcnt(0)
	v_mfma_f32_16x16x32_bf16 v[126:129], v[140:143], v[182:185], v[126:129]
	v_mfma_f32_16x16x32_bf16 v[122:125], v[154:157], v[182:185], v[122:125]
	v_mfma_f32_16x16x32_bf16 v[110:113], v[140:143], v[190:193], v[110:113]
	v_mfma_f32_16x16x32_bf16 v[106:109], v[154:157], v[190:193], v[106:109]
	v_mfma_f32_16x16x32_bf16 v[94:97], v[140:143], v[198:201], v[94:97]
	v_mfma_f32_16x16x32_bf16 v[90:93], v[154:157], v[198:201], v[90:93]
	v_mfma_f32_16x16x32_bf16 v[78:81], v[140:143], v[206:209], v[78:81]
	v_mfma_f32_16x16x32_bf16 v[74:77], v[154:157], v[206:209], v[74:77]
	v_mfma_f32_16x16x32_bf16 v[126:129], v[150:153], v[186:189], v[126:129]
	v_mfma_f32_16x16x32_bf16 v[122:125], v[158:161], v[186:189], v[122:125]
	v_mfma_f32_16x16x32_bf16 v[110:113], v[150:153], v[194:197], v[110:113]
	v_mfma_f32_16x16x32_bf16 v[106:109], v[158:161], v[194:197], v[106:109]
	v_mfma_f32_16x16x32_bf16 v[94:97], v[150:153], v[202:205], v[94:97]
	v_mfma_f32_16x16x32_bf16 v[90:93], v[158:161], v[202:205], v[90:93]
	v_mfma_f32_16x16x32_bf16 v[78:81], v[150:153], v[210:213], v[78:81]
	v_mfma_f32_16x16x32_bf16 v[74:77], v[158:161], v[210:213], v[74:77]
	s_setprio 0
	s_setprio 1
	v_mfma_f32_16x16x32_bf16 v[118:121], v[162:165], v[182:185], v[118:121]
	v_mfma_f32_16x16x32_bf16 v[114:117], v[174:177], v[182:185], v[114:117]
	v_mfma_f32_16x16x32_bf16 v[102:105], v[162:165], v[190:193], v[102:105]
	v_mfma_f32_16x16x32_bf16 v[98:101], v[174:177], v[190:193], v[98:101]
	v_mfma_f32_16x16x32_bf16 v[86:89], v[162:165], v[198:201], v[86:89]
	v_mfma_f32_16x16x32_bf16 v[82:85], v[174:177], v[198:201], v[82:85]
	v_mfma_f32_16x16x32_bf16 v[70:73], v[162:165], v[206:209], v[70:73]
	v_mfma_f32_16x16x32_bf16 v[66:69], v[174:177], v[206:209], v[66:69]
	v_mfma_f32_16x16x32_bf16 v[118:121], v[170:173], v[186:189], v[118:121]
	v_mfma_f32_16x16x32_bf16 v[114:117], v[178:181], v[186:189], v[114:117]
	v_mfma_f32_16x16x32_bf16 v[102:105], v[170:173], v[194:197], v[102:105]
	v_mfma_f32_16x16x32_bf16 v[98:101], v[178:181], v[194:197], v[98:101]
	v_mfma_f32_16x16x32_bf16 v[86:89], v[170:173], v[202:205], v[86:89]
	v_mfma_f32_16x16x32_bf16 v[82:85], v[178:181], v[202:205], v[82:85]
	v_mfma_f32_16x16x32_bf16 v[70:73], v[170:173], v[210:213], v[70:73]
	v_mfma_f32_16x16x32_bf16 v[66:69], v[178:181], v[210:213], v[66:69]
	s_setprio 0
	s_barrier
	s_add_i32 s68, s68, s15
	v_lshl_add_u64 v[144:145], s[54:55], 0, v[166:167]
	s_mov_b32 m0, s68
	s_nop 0
	global_load_lds_dwordx4 v[144:145], off
	s_add_i32 m0, s68, 0x2000
	s_add_u32 s68, s54, 0x40000
	v_lshl_add_u64 v[214:215], s[54:55], 0, v[130:131]
	s_addc_u32 s69, s55, 0
	s_add_i32 s70, s70, s15
	global_load_lds_dwordx4 v[214:215], off
	v_lshl_add_u64 v[216:217], s[68:69], 0, v[166:167]
	s_mov_b32 m0, s70
	v_lshl_add_u64 v[218:219], s[58:59], 0, v[134:135]
	global_load_lds_dwordx4 v[216:217], off
	v_lshl_add_u64 v[216:217], s[68:69], 0, v[130:131]
	s_add_i32 m0, s70, 0x2000
	s_nop 0
	global_load_lds_dwordx4 v[216:217], off
	v_lshl_add_u64 v[216:217], s[58:59], 0, v[132:133]
	s_mov_b32 m0, s16
	s_nop 0
	global_load_lds_dwordx4 v[216:217], off
	s_mov_b32 m0, s20
	s_nop 0
	global_load_lds_dwordx4 v[218:219], off
	ds_read_b128 v[182:185], v149 offset:16384
	ds_read_b128 v[186:189], v149 offset:17408
	ds_read_b128 v[190:193], v149 offset:18432
	ds_read_b128 v[194:197], v149 offset:19456
	ds_read_b128 v[198:201], v149 offset:20480
	ds_read_b128 v[202:205], v149 offset:21504
	ds_read_b128 v[206:209], v149 offset:22528
	ds_read_b128 v[210:213], v149 offset:23552
	s_waitcnt vmcnt(8)
	s_waitcnt lgkmcnt(0)
	s_barrier
	s_setprio 1
	s_waitcnt lgkmcnt(0)
	v_mfma_f32_16x16x32_bf16 v[62:65], v[140:143], v[182:185], v[62:65]
	v_mfma_f32_16x16x32_bf16 v[58:61], v[154:157], v[182:185], v[58:61]
	v_mfma_f32_16x16x32_bf16 v[46:49], v[140:143], v[190:193], v[46:49]
	v_mfma_f32_16x16x32_bf16 v[42:45], v[154:157], v[190:193], v[42:45]
	v_mfma_f32_16x16x32_bf16 v[30:33], v[140:143], v[198:201], v[30:33]
	v_mfma_f32_16x16x32_bf16 v[26:29], v[154:157], v[198:201], v[26:29]
	v_mfma_f32_16x16x32_bf16 v[14:17], v[140:143], v[206:209], v[14:17]
	v_mfma_f32_16x16x32_bf16 v[10:13], v[154:157], v[206:209], v[10:13]
	v_mfma_f32_16x16x32_bf16 v[62:65], v[150:153], v[186:189], v[62:65]
	v_mfma_f32_16x16x32_bf16 v[58:61], v[158:161], v[186:189], v[58:61]
	v_mfma_f32_16x16x32_bf16 v[46:49], v[150:153], v[194:197], v[46:49]
	v_mfma_f32_16x16x32_bf16 v[42:45], v[158:161], v[194:197], v[42:45]
	v_mfma_f32_16x16x32_bf16 v[30:33], v[150:153], v[202:205], v[30:33]
	v_mfma_f32_16x16x32_bf16 v[26:29], v[158:161], v[202:205], v[26:29]
	v_mfma_f32_16x16x32_bf16 v[14:17], v[150:153], v[210:213], v[14:17]
	v_mfma_f32_16x16x32_bf16 v[10:13], v[158:161], v[210:213], v[10:13]
	s_setprio 0
	s_setprio 1
	v_mfma_f32_16x16x32_bf16 v[54:57], v[162:165], v[182:185], v[54:57]
	v_mfma_f32_16x16x32_bf16 v[50:53], v[174:177], v[182:185], v[50:53]
	v_mfma_f32_16x16x32_bf16 v[38:41], v[162:165], v[190:193], v[38:41]
	v_mfma_f32_16x16x32_bf16 v[34:37], v[174:177], v[190:193], v[34:37]
	v_mfma_f32_16x16x32_bf16 v[22:25], v[162:165], v[198:201], v[22:25]
	v_mfma_f32_16x16x32_bf16 v[18:21], v[174:177], v[198:201], v[18:21]
	v_mfma_f32_16x16x32_bf16 v[6:9], v[162:165], v[206:209], v[6:9]
	v_mfma_f32_16x16x32_bf16 v[2:5], v[174:177], v[206:209], v[2:5]
	v_mfma_f32_16x16x32_bf16 v[54:57], v[170:173], v[186:189], v[54:57]
	v_mfma_f32_16x16x32_bf16 v[50:53], v[178:181], v[186:189], v[50:53]
	v_mfma_f32_16x16x32_bf16 v[38:41], v[170:173], v[194:197], v[38:41]
	v_mfma_f32_16x16x32_bf16 v[34:37], v[178:181], v[194:197], v[34:37]
	v_mfma_f32_16x16x32_bf16 v[22:25], v[170:173], v[202:205], v[22:25]
	v_mfma_f32_16x16x32_bf16 v[18:21], v[178:181], v[202:205], v[18:21]
	v_mfma_f32_16x16x32_bf16 v[6:9], v[170:173], v[210:213], v[6:9]
	v_mfma_f32_16x16x32_bf16 v[2:5], v[178:181], v[210:213], v[2:5]
	s_setprio 0
	s_barrier
	s_add_i32 s68, 0, 0x18000
	s_add_i32 s69, 0, 0x1c000
	v_add_u32_e32 v158, s68, v147
	v_add_u32_e32 v169, s69, v147
	s_add_u32 s58, s58, 0x40000
	s_addc_u32 s59, s59, 0
	s_mov_b32 m0, s21
	v_lshl_add_u64 v[220:221], s[58:59], 0, v[132:133]
	global_load_lds_dwordx4 v[220:221], off
	v_lshl_add_u64 v[220:221], s[58:59], 0, v[134:135]
	s_mov_b32 m0, s22
	s_nop 0
	global_load_lds_dwordx4 v[220:221], off
	ds_read_b128 v[140:143], v158
	ds_read_b128 v[150:153], v158 offset:1024
	ds_read_b128 v[154:157], v158 offset:2048
	ds_read_b128 v[158:161], v158 offset:3072
	ds_read_b128 v[162:165], v169
	ds_read_b128 v[170:173], v169 offset:1024
	ds_read_b128 v[174:177], v169 offset:2048
	ds_read_b128 v[178:181], v169 offset:3072
	ds_read_b128 v[182:185], v149 offset:32768
	ds_read_b128 v[186:189], v149 offset:33792
	ds_read_b128 v[190:193], v149 offset:34816
	ds_read_b128 v[194:197], v149 offset:35840
	ds_read_b128 v[198:201], v149 offset:36864
	ds_read_b128 v[202:205], v149 offset:37888
	ds_read_b128 v[206:209], v149 offset:38912
	ds_read_b128 v[210:213], v149 offset:39936
	s_waitcnt vmcnt(8)
	s_waitcnt lgkmcnt(0)
	s_barrier
	s_setprio 1
	s_waitcnt lgkmcnt(0)
	v_mfma_f32_16x16x32_bf16 v[126:129], v[140:143], v[182:185], v[126:129]
	v_mfma_f32_16x16x32_bf16 v[122:125], v[154:157], v[182:185], v[122:125]
	v_mfma_f32_16x16x32_bf16 v[110:113], v[140:143], v[190:193], v[110:113]
	v_mfma_f32_16x16x32_bf16 v[106:109], v[154:157], v[190:193], v[106:109]
	v_mfma_f32_16x16x32_bf16 v[94:97], v[140:143], v[198:201], v[94:97]
	v_mfma_f32_16x16x32_bf16 v[90:93], v[154:157], v[198:201], v[90:93]
	v_mfma_f32_16x16x32_bf16 v[78:81], v[140:143], v[206:209], v[78:81]
	v_mfma_f32_16x16x32_bf16 v[74:77], v[154:157], v[206:209], v[74:77]
	v_mfma_f32_16x16x32_bf16 v[126:129], v[150:153], v[186:189], v[126:129]
	v_mfma_f32_16x16x32_bf16 v[122:125], v[158:161], v[186:189], v[122:125]
	v_mfma_f32_16x16x32_bf16 v[110:113], v[150:153], v[194:197], v[110:113]
	v_mfma_f32_16x16x32_bf16 v[106:109], v[158:161], v[194:197], v[106:109]
	v_mfma_f32_16x16x32_bf16 v[94:97], v[150:153], v[202:205], v[94:97]
	v_mfma_f32_16x16x32_bf16 v[90:93], v[158:161], v[202:205], v[90:93]
	v_mfma_f32_16x16x32_bf16 v[78:81], v[150:153], v[210:213], v[78:81]
	v_mfma_f32_16x16x32_bf16 v[74:77], v[158:161], v[210:213], v[74:77]
	s_setprio 0
	s_setprio 1
	v_mfma_f32_16x16x32_bf16 v[118:121], v[162:165], v[182:185], v[118:121]
	v_mfma_f32_16x16x32_bf16 v[114:117], v[174:177], v[182:185], v[114:117]
	v_mfma_f32_16x16x32_bf16 v[102:105], v[162:165], v[190:193], v[102:105]
	v_mfma_f32_16x16x32_bf16 v[98:101], v[174:177], v[190:193], v[98:101]
	v_mfma_f32_16x16x32_bf16 v[86:89], v[162:165], v[198:201], v[86:89]
	v_mfma_f32_16x16x32_bf16 v[82:85], v[174:177], v[198:201], v[82:85]
	v_mfma_f32_16x16x32_bf16 v[70:73], v[162:165], v[206:209], v[70:73]
	v_mfma_f32_16x16x32_bf16 v[66:69], v[174:177], v[206:209], v[66:69]
	v_mfma_f32_16x16x32_bf16 v[118:121], v[170:173], v[186:189], v[118:121]
	v_mfma_f32_16x16x32_bf16 v[114:117], v[178:181], v[186:189], v[114:117]
	v_mfma_f32_16x16x32_bf16 v[102:105], v[170:173], v[194:197], v[102:105]
	v_mfma_f32_16x16x32_bf16 v[98:101], v[178:181], v[194:197], v[98:101]
	v_mfma_f32_16x16x32_bf16 v[86:89], v[170:173], v[202:205], v[86:89]
	v_mfma_f32_16x16x32_bf16 v[82:85], v[178:181], v[202:205], v[82:85]
	v_mfma_f32_16x16x32_bf16 v[70:73], v[170:173], v[210:213], v[70:73]
	v_mfma_f32_16x16x32_bf16 v[66:69], v[178:181], v[210:213], v[66:69]
	s_setprio 0
	s_barrier
	s_add_i32 s58, s68, s15
	v_lshl_add_u64 v[144:145], v[144:145], 0, s[56:57]
	s_mov_b32 m0, s58
	s_nop 0
	global_load_lds_dwordx4 v[144:145], off
	s_add_i32 m0, s58, 0x2000
	s_add_u32 s54, s54, 0x40080
	v_lshl_add_u64 v[144:145], v[214:215], 0, s[56:57]
	s_addc_u32 s55, s55, 0
	s_add_i32 s58, s69, s15
	global_load_lds_dwordx4 v[144:145], off
	v_lshl_add_u64 v[144:145], s[54:55], 0, v[166:167]
	s_mov_b32 m0, s58
	s_nop 0
	global_load_lds_dwordx4 v[144:145], off
	v_lshl_add_u64 v[144:145], s[54:55], 0, v[130:131]
	s_add_i32 m0, s58, 0x2000
	s_nop 0
	global_load_lds_dwordx4 v[144:145], off
	v_lshl_add_u64 v[144:145], v[216:217], 0, s[56:57]
	s_mov_b32 m0, s23
	s_nop 0
	global_load_lds_dwordx4 v[144:145], off
	v_lshl_add_u64 v[144:145], v[218:219], 0, s[56:57]
	s_mov_b32 m0, s24
	s_nop 0
	global_load_lds_dwordx4 v[144:145], off
	ds_read_b128 v[182:185], v149 offset:49152
	ds_read_b128 v[186:189], v149 offset:50176
	ds_read_b128 v[190:193], v149 offset:51200
	ds_read_b128 v[194:197], v149 offset:52224
	ds_read_b128 v[198:201], v149 offset:53248
	ds_read_b128 v[202:205], v149 offset:54272
	ds_read_b128 v[206:209], v149 offset:55296
	ds_read_b128 v[210:213], v149 offset:56320
	s_waitcnt vmcnt(8)
	s_waitcnt lgkmcnt(0)
	s_barrier
	s_setprio 1
	s_waitcnt lgkmcnt(0)
	v_mfma_f32_16x16x32_bf16 v[62:65], v[140:143], v[182:185], v[62:65]
	v_mfma_f32_16x16x32_bf16 v[58:61], v[154:157], v[182:185], v[58:61]
	v_mfma_f32_16x16x32_bf16 v[46:49], v[140:143], v[190:193], v[46:49]
	v_mfma_f32_16x16x32_bf16 v[42:45], v[154:157], v[190:193], v[42:45]
	v_mfma_f32_16x16x32_bf16 v[30:33], v[140:143], v[198:201], v[30:33]
	v_mfma_f32_16x16x32_bf16 v[26:29], v[154:157], v[198:201], v[26:29]
	v_mfma_f32_16x16x32_bf16 v[14:17], v[140:143], v[206:209], v[14:17]
	v_mfma_f32_16x16x32_bf16 v[10:13], v[154:157], v[206:209], v[10:13]
	v_mfma_f32_16x16x32_bf16 v[62:65], v[150:153], v[186:189], v[62:65]
	v_mfma_f32_16x16x32_bf16 v[58:61], v[158:161], v[186:189], v[58:61]
	v_mfma_f32_16x16x32_bf16 v[46:49], v[150:153], v[194:197], v[46:49]
	v_mfma_f32_16x16x32_bf16 v[42:45], v[158:161], v[194:197], v[42:45]
	v_mfma_f32_16x16x32_bf16 v[30:33], v[150:153], v[202:205], v[30:33]
	v_mfma_f32_16x16x32_bf16 v[26:29], v[158:161], v[202:205], v[26:29]
	v_mfma_f32_16x16x32_bf16 v[14:17], v[150:153], v[210:213], v[14:17]
	v_mfma_f32_16x16x32_bf16 v[10:13], v[158:161], v[210:213], v[10:13]
	s_setprio 0
	s_setprio 1
	v_mfma_f32_16x16x32_bf16 v[54:57], v[162:165], v[182:185], v[54:57]
	v_mfma_f32_16x16x32_bf16 v[50:53], v[174:177], v[182:185], v[50:53]
	v_mfma_f32_16x16x32_bf16 v[38:41], v[162:165], v[190:193], v[38:41]
	v_mfma_f32_16x16x32_bf16 v[34:37], v[174:177], v[190:193], v[34:37]
	v_mfma_f32_16x16x32_bf16 v[22:25], v[162:165], v[198:201], v[22:25]
	v_mfma_f32_16x16x32_bf16 v[18:21], v[174:177], v[198:201], v[18:21]
	v_mfma_f32_16x16x32_bf16 v[6:9], v[162:165], v[206:209], v[6:9]
	v_mfma_f32_16x16x32_bf16 v[2:5], v[174:177], v[206:209], v[2:5]
	v_mfma_f32_16x16x32_bf16 v[54:57], v[170:173], v[186:189], v[54:57]
	v_mfma_f32_16x16x32_bf16 v[50:53], v[178:181], v[186:189], v[50:53]
	v_mfma_f32_16x16x32_bf16 v[38:41], v[170:173], v[194:197], v[38:41]
	v_mfma_f32_16x16x32_bf16 v[34:37], v[178:181], v[194:197], v[34:37]
	v_mfma_f32_16x16x32_bf16 v[22:25], v[170:173], v[202:205], v[22:25]
	v_mfma_f32_16x16x32_bf16 v[18:21], v[178:181], v[202:205], v[18:21]
	v_mfma_f32_16x16x32_bf16 v[6:9], v[170:173], v[210:213], v[6:9]
	v_mfma_f32_16x16x32_bf16 v[2:5], v[178:181], v[210:213], v[2:5]
	s_setprio 0
	s_barrier
	s_add_u32 s64, s64, 0x100
	s_addc_u32 s65, s65, 0
	s_add_u32 s52, s52, 0x100
	s_addc_u32 s53, s53, 0
	s_cmp_ge_i32 s66, s1
	s_mov_b32 s54, s66
	s_cbranch_scc0 .LBB0_1438
	s_mov_b64 s[70:71], 0xe800800
	v_mov_b32_e32 v209, v1
	s_and_b64 vcc, exec, s[34:35]
	s_cbranch_vccz .LBB0_1441

.LBB0_1693:
	s_add_i32 s91, s91, 2
	s_add_u32 s64, s70, 0x100
	s_addc_u32 s65, s71, 0
	s_and_b64 s[74:75], s[68:69], exec
	s_cselect_b32 s74, 0, s64
	s_cselect_b32 s75, 0, s65
	s_add_u32 s74, s28, s74
	s_addc_u32 s75, s29, s75
	s_add_u32 s92, s51, s70
	s_addc_u32 s93, s53, s71
	s_and_b64 s[68:69], s[68:69], exec
	s_cselect_b32 s69, s55, s93
	s_cselect_b32 s68, s54, s92
	s_add_i32 s93, 0, 0x10000
	s_add_i32 s92, 0, 0x14000
	v_add_u32_e32 v2, s93, v210
	v_add_u32_e32 v6, s92, v210
	v_lshl_add_u64 v[170:171], v[194:195], 0, s[70:71]
	s_add_i32 m0, s59, 0xc000
	s_nop 0
	global_load_lds_dwordx4 v[170:171], off
	v_lshl_add_u64 v[170:171], v[192:193], 0, s[70:71]
	s_add_i32 m0, s59, 0xe000
	s_nop 0
	global_load_lds_dwordx4 v[170:171], off
	ds_read_b128 v[26:29], v2
	ds_read_b128 v[30:33], v2 offset:1024
	ds_read_b128 v[18:21], v2 offset:2048
	ds_read_b128 v[22:25], v2 offset:3072
	ds_read_b128 v[10:13], v6
	ds_read_b128 v[14:17], v6 offset:1024
	ds_read_b128 v[2:5], v6 offset:2048
	ds_read_b128 v[6:9], v6 offset:3072
	ds_read_b128 v[196:199], v212
	ds_read_b128 v[200:203], v212 offset:1024
	ds_read_b128 v[214:217], v212 offset:2048
	ds_read_b128 v[218:221], v212 offset:3072
	ds_read_b128 v[236:239], v212 offset:4096
	ds_read_b128 v[240:243], v212 offset:5120
	ds_read_b128 v[244:247], v212 offset:6144
	ds_read_b128 v[248:251], v212 offset:7168
	s_waitcnt vmcnt(8)
	s_waitcnt lgkmcnt(0)
	s_barrier
	s_setprio 1
	s_waitcnt lgkmcnt(0)
	v_mfma_scale_f32_16x16x128_f8f6f4 v[154:157], v[26:33], v[196:203], v[154:157], v208, v207 op_sel_hi:[0,0,0]
	v_mfma_scale_f32_16x16x128_f8f6f4 v[150:153], v[18:25], v[196:203], v[150:153], v208, v207 op_sel_hi:[0,0,0]
	v_mfma_scale_f32_16x16x128_f8f6f4 v[142:145], v[26:33], v[214:221], v[142:145], v208, v207 op_sel_hi:[0,0,0]
	v_mfma_scale_f32_16x16x128_f8f6f4 v[134:137], v[18:25], v[214:221], v[134:137], v208, v207 op_sel_hi:[0,0,0]
	v_mfma_scale_f32_16x16x128_f8f6f4 v[126:129], v[26:33], v[236:243], v[126:129], v208, v207 op_sel_hi:[0,0,0]
	v_mfma_scale_f32_16x16x128_f8f6f4 v[118:121], v[18:25], v[236:243], v[118:121], v208, v207 op_sel_hi:[0,0,0]
	v_mfma_scale_f32_16x16x128_f8f6f4 v[110:113], v[26:33], v[244:251], v[110:113], v208, v207 op_sel_hi:[0,0,0]
	v_mfma_scale_f32_16x16x128_f8f6f4 v[102:105], v[18:25], v[244:251], v[102:105], v208, v207 op_sel_hi:[0,0,0]
	s_setprio 0
	s_setprio 1
	v_mfma_scale_f32_16x16x128_f8f6f4 v[158:161], v[10:17], v[196:203], v[158:161], v208, v207 op_sel_hi:[0,0,0]
	v_mfma_scale_f32_16x16x128_f8f6f4 v[146:149], v[2:9], v[196:203], v[146:149], v208, v207 op_sel_hi:[0,0,0]
	v_mfma_scale_f32_16x16x128_f8f6f4 v[138:141], v[10:17], v[214:221], v[138:141], v208, v207 op_sel_hi:[0,0,0]
	v_mfma_scale_f32_16x16x128_f8f6f4 v[130:133], v[2:9], v[214:221], v[130:133], v208, v207 op_sel_hi:[0,0,0]
	v_mfma_scale_f32_16x16x128_f8f6f4 v[122:125], v[10:17], v[236:243], v[122:125], v208, v207 op_sel_hi:[0,0,0]
	v_mfma_scale_f32_16x16x128_f8f6f4 v[114:117], v[2:9], v[236:243], v[114:117], v208, v207 op_sel_hi:[0,0,0]
	v_mfma_scale_f32_16x16x128_f8f6f4 v[106:109], v[10:17], v[244:251], v[106:109], v208, v207 op_sel_hi:[0,0,0]
	v_mfma_scale_f32_16x16x128_f8f6f4 v[98:101], v[2:9], v[244:251], v[98:101], v208, v207 op_sel_hi:[0,0,0]
	s_setprio 0
	s_barrier
	s_add_i32 s70, s93, s72
	v_lshl_add_u64 v[196:197], s[68:69], 0, v[162:163]
	s_mov_b32 m0, s70
	s_nop 0
	global_load_lds_dwordx4 v[196:197], off
	s_add_i32 m0, s70, 0x2000
	s_add_u32 s70, s68, 0x20000
	v_lshl_add_u64 v[198:199], s[68:69], 0, v[164:165]
	s_addc_u32 s71, s69, 0
	s_add_i32 s92, s92, s72
	global_load_lds_dwordx4 v[198:199], off
	v_lshl_add_u64 v[200:201], s[70:71], 0, v[162:163]
	s_mov_b32 m0, s92
	s_nop 0
	global_load_lds_dwordx4 v[200:201], off
	v_lshl_add_u64 v[200:201], s[70:71], 0, v[164:165]
	s_add_i32 m0, s92, 0x2000
	s_nop 0
	global_load_lds_dwordx4 v[200:201], off
	s_mov_b32 m0, s59
	s_nop 0
	global_load_lds_dwordx4 v166, s[74:75]
	s_mov_b32 m0, s61
	s_nop 0
	global_load_lds_dwordx4 v178, s[74:75]
	ds_read_b128 v[214:217], v212 offset:16384
	ds_read_b128 v[218:221], v212 offset:17408
	ds_read_b128 v[236:239], v212 offset:18432
	ds_read_b128 v[240:243], v212 offset:19456
	ds_read_b128 v[244:247], v212 offset:20480
	ds_read_b128 v[248:251], v212 offset:21504
	ds_read_b128 v[170:173], v212 offset:22528
	ds_read_b128 v[174:177], v212 offset:23552
	v_mov_b32_e32 v179, v167
	v_lshl_add_u64 v[202:203], s[74:75], 0, v[166:167]
	v_lshl_add_u64 v[200:201], s[74:75], 0, v[178:179]
	s_waitcnt vmcnt(8)
	s_waitcnt lgkmcnt(0)
	s_barrier
	s_setprio 1
	s_waitcnt lgkmcnt(0)
	v_mfma_scale_f32_16x16x128_f8f6f4 v[94:97], v[26:33], v[214:221], v[94:97], v208, v207 op_sel_hi:[0,0,0]
	v_mfma_scale_f32_16x16x128_f8f6f4 v[86:89], v[18:25], v[214:221], v[86:89], v208, v207 op_sel_hi:[0,0,0]
	v_mfma_scale_f32_16x16x128_f8f6f4 v[78:81], v[26:33], v[236:243], v[78:81], v208, v207 op_sel_hi:[0,0,0]
	v_mfma_scale_f32_16x16x128_f8f6f4 v[70:73], v[18:25], v[236:243], v[70:73], v208, v207 op_sel_hi:[0,0,0]
	v_mfma_scale_f32_16x16x128_f8f6f4 v[62:65], v[26:33], v[244:251], v[62:65], v208, v207 op_sel_hi:[0,0,0]
	v_mfma_scale_f32_16x16x128_f8f6f4 v[54:57], v[18:25], v[244:251], v[54:57], v208, v207 op_sel_hi:[0,0,0]
	v_mfma_scale_f32_16x16x128_f8f6f4 v[46:49], v[26:33], v[170:177], v[46:49], v208, v207 op_sel_hi:[0,0,0]
	v_mfma_scale_f32_16x16x128_f8f6f4 v[38:41], v[18:25], v[170:177], v[38:41], v208, v207 op_sel_hi:[0,0,0]
	s_setprio 0
	s_setprio 1
	v_mfma_scale_f32_16x16x128_f8f6f4 v[90:93], v[10:17], v[214:221], v[90:93], v208, v207 op_sel_hi:[0,0,0]
	v_mfma_scale_f32_16x16x128_f8f6f4 v[82:85], v[2:9], v[214:221], v[82:85], v208, v207 op_sel_hi:[0,0,0]
	v_mfma_scale_f32_16x16x128_f8f6f4 v[74:77], v[10:17], v[236:243], v[74:77], v208, v207 op_sel_hi:[0,0,0]
	v_mfma_scale_f32_16x16x128_f8f6f4 v[66:69], v[2:9], v[236:243], v[66:69], v208, v207 op_sel_hi:[0,0,0]
	v_mfma_scale_f32_16x16x128_f8f6f4 v[58:61], v[10:17], v[244:251], v[58:61], v208, v207 op_sel_hi:[0,0,0]
	v_mfma_scale_f32_16x16x128_f8f6f4 v[50:53], v[2:9], v[244:251], v[50:53], v208, v207 op_sel_hi:[0,0,0]
	v_mfma_scale_f32_16x16x128_f8f6f4 v[42:45], v[10:17], v[170:177], v[42:45], v208, v207 op_sel_hi:[0,0,0]
	v_mfma_scale_f32_16x16x128_f8f6f4 v[34:37], v[2:9], v[170:177], v[34:37], v208, v207 op_sel_hi:[0,0,0]
	s_setprio 0
	s_barrier
	s_add_i32 s70, 0, 0x18000
	s_add_i32 s71, 0, 0x1c000
	v_add_u32_e32 v2, s70, v210
	v_add_u32_e32 v6, s71, v210
	s_mov_b32 m0, s73
	s_nop 0
	global_load_lds_dwordx4 v180, s[74:75]
	s_mov_b32 m0, s76
	s_nop 0
	global_load_lds_dwordx4 v182, s[74:75]
	ds_read_b128 v[26:29], v2
	ds_read_b128 v[30:33], v2 offset:1024
	ds_read_b128 v[18:21], v2 offset:2048
	ds_read_b128 v[22:25], v2 offset:3072
	ds_read_b128 v[10:13], v6
	ds_read_b128 v[14:17], v6 offset:1024
	ds_read_b128 v[2:5], v6 offset:2048
	ds_read_b128 v[6:9], v6 offset:3072
	ds_read_b128 v[170:173], v212 offset:32768
	ds_read_b128 v[174:177], v212 offset:33792
	ds_read_b128 v[214:217], v212 offset:34816
	ds_read_b128 v[218:221], v212 offset:35840
	ds_read_b128 v[236:239], v212 offset:36864
	ds_read_b128 v[240:243], v212 offset:37888
	ds_read_b128 v[244:247], v212 offset:38912
	ds_read_b128 v[248:251], v212 offset:39936
	s_waitcnt vmcnt(8)
	s_waitcnt lgkmcnt(0)
	s_barrier
	s_setprio 1
	s_waitcnt lgkmcnt(0)
	v_mfma_scale_f32_16x16x128_f8f6f4 v[154:157], v[26:33], v[170:177], v[154:157], v208, v207 op_sel_hi:[0,0,0]
	v_mfma_scale_f32_16x16x128_f8f6f4 v[150:153], v[18:25], v[170:177], v[150:153], v208, v207 op_sel_hi:[0,0,0]
	v_mfma_scale_f32_16x16x128_f8f6f4 v[142:145], v[26:33], v[214:221], v[142:145], v208, v207 op_sel_hi:[0,0,0]
	v_mfma_scale_f32_16x16x128_f8f6f4 v[134:137], v[18:25], v[214:221], v[134:137], v208, v207 op_sel_hi:[0,0,0]
	v_mfma_scale_f32_16x16x128_f8f6f4 v[126:129], v[26:33], v[236:243], v[126:129], v208, v207 op_sel_hi:[0,0,0]
	v_mfma_scale_f32_16x16x128_f8f6f4 v[118:121], v[18:25], v[236:243], v[118:121], v208, v207 op_sel_hi:[0,0,0]
	v_mfma_scale_f32_16x16x128_f8f6f4 v[110:113], v[26:33], v[244:251], v[110:113], v208, v207 op_sel_hi:[0,0,0]
	v_mfma_scale_f32_16x16x128_f8f6f4 v[102:105], v[18:25], v[244:251], v[102:105], v208, v207 op_sel_hi:[0,0,0]
	s_setprio 0
	s_setprio 1
	v_mfma_scale_f32_16x16x128_f8f6f4 v[158:161], v[10:17], v[170:177], v[158:161], v208, v207 op_sel_hi:[0,0,0]
	v_mfma_scale_f32_16x16x128_f8f6f4 v[146:149], v[2:9], v[170:177], v[146:149], v208, v207 op_sel_hi:[0,0,0]
	v_mfma_scale_f32_16x16x128_f8f6f4 v[138:141], v[10:17], v[214:221], v[138:141], v208, v207 op_sel_hi:[0,0,0]
	v_mfma_scale_f32_16x16x128_f8f6f4 v[130:133], v[2:9], v[214:221], v[130:133], v208, v207 op_sel_hi:[0,0,0]
	v_mfma_scale_f32_16x16x128_f8f6f4 v[122:125], v[10:17], v[236:243], v[122:125], v208, v207 op_sel_hi:[0,0,0]
	v_mfma_scale_f32_16x16x128_f8f6f4 v[114:117], v[2:9], v[236:243], v[114:117], v208, v207 op_sel_hi:[0,0,0]
	v_mfma_scale_f32_16x16x128_f8f6f4 v[106:109], v[10:17], v[244:251], v[106:109], v208, v207 op_sel_hi:[0,0,0]
	v_mfma_scale_f32_16x16x128_f8f6f4 v[98:101], v[2:9], v[244:251], v[98:101], v208, v207 op_sel_hi:[0,0,0]
	s_setprio 0
	s_barrier
	s_add_i32 s70, s70, s72
	v_lshl_add_u64 v[196:197], v[196:197], 0, s[56:57]
	s_mov_b32 m0, s70
	s_nop 0
	global_load_lds_dwordx4 v[196:197], off
	s_add_i32 m0, s70, 0x2000
	s_add_u32 s68, s68, 0x20080
	v_lshl_add_u64 v[196:197], v[198:199], 0, s[56:57]
	s_addc_u32 s69, s69, 0
	s_add_i32 s70, s71, s72
	global_load_lds_dwordx4 v[196:197], off
	v_lshl_add_u64 v[196:197], s[68:69], 0, v[162:163]
	s_mov_b32 m0, s70
	s_nop 0
	global_load_lds_dwordx4 v[196:197], off
	v_lshl_add_u64 v[196:197], s[68:69], 0, v[164:165]
	s_add_i32 m0, s70, 0x2000
	s_nop 0
	global_load_lds_dwordx4 v[196:197], off
	v_lshl_add_u64 v[196:197], v[202:203], 0, s[56:57]
	s_mov_b32 m0, s77
	s_nop 0
	global_load_lds_dwordx4 v[196:197], off
	v_lshl_add_u64 v[196:197], v[200:201], 0, s[56:57]
	s_mov_b32 m0, s79
	s_nop 0
	global_load_lds_dwordx4 v[196:197], off
	ds_read_b128 v[170:173], v212 offset:49152
	ds_read_b128 v[174:177], v212 offset:50176
	ds_read_b128 v[214:217], v212 offset:51200
	ds_read_b128 v[218:221], v212 offset:52224
	ds_read_b128 v[236:239], v212 offset:53248
	ds_read_b128 v[240:243], v212 offset:54272
	ds_read_b128 v[244:247], v212 offset:55296
	ds_read_b128 v[248:251], v212 offset:56320
	s_waitcnt vmcnt(8)
	s_waitcnt lgkmcnt(0)
	s_barrier
	s_setprio 1
	s_waitcnt lgkmcnt(0)
	v_mfma_scale_f32_16x16x128_f8f6f4 v[94:97], v[26:33], v[170:177], v[94:97], v208, v207 op_sel_hi:[0,0,0]
	v_mfma_scale_f32_16x16x128_f8f6f4 v[86:89], v[18:25], v[170:177], v[86:89], v208, v207 op_sel_hi:[0,0,0]
	v_mfma_scale_f32_16x16x128_f8f6f4 v[78:81], v[26:33], v[214:221], v[78:81], v208, v207 op_sel_hi:[0,0,0]
	v_mfma_scale_f32_16x16x128_f8f6f4 v[70:73], v[18:25], v[214:221], v[70:73], v208, v207 op_sel_hi:[0,0,0]
	v_mfma_scale_f32_16x16x128_f8f6f4 v[62:65], v[26:33], v[236:243], v[62:65], v208, v207 op_sel_hi:[0,0,0]
	v_mfma_scale_f32_16x16x128_f8f6f4 v[54:57], v[18:25], v[236:243], v[54:57], v208, v207 op_sel_hi:[0,0,0]
	v_mfma_scale_f32_16x16x128_f8f6f4 v[46:49], v[26:33], v[244:251], v[46:49], v208, v207 op_sel_hi:[0,0,0]
	v_mfma_scale_f32_16x16x128_f8f6f4 v[38:41], v[18:25], v[244:251], v[38:41], v208, v207 op_sel_hi:[0,0,0]
	s_setprio 0
	s_setprio 1
	v_mfma_scale_f32_16x16x128_f8f6f4 v[90:93], v[10:17], v[170:177], v[90:93], v208, v207 op_sel_hi:[0,0,0]
	v_mfma_scale_f32_16x16x128_f8f6f4 v[82:85], v[2:9], v[170:177], v[82:85], v208, v207 op_sel_hi:[0,0,0]
	v_mfma_scale_f32_16x16x128_f8f6f4 v[74:77], v[10:17], v[214:221], v[74:77], v208, v207 op_sel_hi:[0,0,0]
	v_mfma_scale_f32_16x16x128_f8f6f4 v[66:69], v[2:9], v[214:221], v[66:69], v208, v207 op_sel_hi:[0,0,0]
	v_mfma_scale_f32_16x16x128_f8f6f4 v[58:61], v[10:17], v[236:243], v[58:61], v208, v207 op_sel_hi:[0,0,0]
	v_mfma_scale_f32_16x16x128_f8f6f4 v[50:53], v[2:9], v[236:243], v[50:53], v208, v207 op_sel_hi:[0,0,0]
	v_mfma_scale_f32_16x16x128_f8f6f4 v[42:45], v[10:17], v[244:251], v[42:45], v208, v207 op_sel_hi:[0,0,0]
	v_mfma_scale_f32_16x16x128_f8f6f4 v[34:37], v[2:9], v[244:251], v[34:37], v208, v207 op_sel_hi:[0,0,0]
	s_setprio 0
	s_barrier
	s_cmp_ge_i32 s91, s11
	s_cbranch_scc1 .LBB0_1695
	s_mov_b64 s[70:71], s[64:65]
	s_branch .LBB0_1691

.LBB0_1777:
	s_add_i32 s91, s64, 2
	s_add_u32 s62, s60, 0x100
	s_addc_u32 s63, s61, 0
	s_add_i32 s92, 0, 0x10000
	s_cmp_eq_u32 s74, s64
	s_cselect_b32 s69, s53, s63
	s_cselect_b32 s68, s52, s62
	s_cselect_b32 s65, s55, s59
	s_cselect_b32 s64, s54, s51
	s_add_i32 s93, 0, 0x14000
	v_add_u32_e32 v2, s92, v196
	v_add_u32_e32 v6, s93, v196
	v_lshl_add_u64 v[216:217], s[60:61], 0, v[184:185]
	s_add_i32 m0, s21, 0xc000
	s_nop 0
	global_load_lds_dwordx4 v[216:217], off
	v_lshl_add_u64 v[216:217], s[60:61], 0, v[182:183]
	s_add_i32 m0, s21, 0xe000
	s_nop 0
	global_load_lds_dwordx4 v[216:217], off
	ds_read_b128 v[26:29], v2
	ds_read_b128 v[30:33], v2 offset:1024
	ds_read_b128 v[18:21], v2 offset:2048
	ds_read_b128 v[22:25], v2 offset:3072
	ds_read_b128 v[10:13], v6
	ds_read_b128 v[14:17], v6 offset:1024
	ds_read_b128 v[2:5], v6 offset:2048
	ds_read_b128 v[6:9], v6 offset:3072
	ds_read_b128 v[170:173], v198
	ds_read_b128 v[174:177], v198 offset:1024
	ds_read_b128 v[186:189], v198 offset:2048
	ds_read_b128 v[190:193], v198 offset:3072
	ds_read_b128 v[200:203], v198 offset:4096
	ds_read_b128 v[204:207], v198 offset:5120
	ds_read_b128 v[208:211], v198 offset:6144
	ds_read_b128 v[212:215], v198 offset:7168
	s_waitcnt vmcnt(8)
	s_waitcnt lgkmcnt(0)
	s_barrier
	s_setprio 1
	s_waitcnt lgkmcnt(0)
	v_mfma_scale_f32_16x16x128_f8f6f4 v[154:157], v[26:33], v[170:177], v[154:157], v194, v169 op_sel_hi:[0,0,0]
	v_mfma_scale_f32_16x16x128_f8f6f4 v[158:161], v[18:25], v[170:177], v[158:161], v194, v169 op_sel_hi:[0,0,0]
	v_mfma_scale_f32_16x16x128_f8f6f4 v[138:141], v[26:33], v[186:193], v[138:141], v194, v169 op_sel_hi:[0,0,0]
	v_mfma_scale_f32_16x16x128_f8f6f4 v[142:145], v[18:25], v[186:193], v[142:145], v194, v169 op_sel_hi:[0,0,0]
	v_mfma_scale_f32_16x16x128_f8f6f4 v[122:125], v[26:33], v[200:207], v[122:125], v194, v169 op_sel_hi:[0,0,0]
	v_mfma_scale_f32_16x16x128_f8f6f4 v[126:129], v[18:25], v[200:207], v[126:129], v194, v169 op_sel_hi:[0,0,0]
	v_mfma_scale_f32_16x16x128_f8f6f4 v[106:109], v[26:33], v[208:215], v[106:109], v194, v169 op_sel_hi:[0,0,0]
	v_mfma_scale_f32_16x16x128_f8f6f4 v[110:113], v[18:25], v[208:215], v[110:113], v194, v169 op_sel_hi:[0,0,0]
	s_setprio 0
	s_setprio 1
	v_mfma_scale_f32_16x16x128_f8f6f4 v[146:149], v[10:17], v[170:177], v[146:149], v194, v169 op_sel_hi:[0,0,0]
	v_mfma_scale_f32_16x16x128_f8f6f4 v[150:153], v[2:9], v[170:177], v[150:153], v194, v169 op_sel_hi:[0,0,0]
	v_mfma_scale_f32_16x16x128_f8f6f4 v[130:133], v[10:17], v[186:193], v[130:133], v194, v169 op_sel_hi:[0,0,0]
	v_mfma_scale_f32_16x16x128_f8f6f4 v[134:137], v[2:9], v[186:193], v[134:137], v194, v169 op_sel_hi:[0,0,0]
	v_mfma_scale_f32_16x16x128_f8f6f4 v[114:117], v[10:17], v[200:207], v[114:117], v194, v169 op_sel_hi:[0,0,0]
	v_mfma_scale_f32_16x16x128_f8f6f4 v[118:121], v[2:9], v[200:207], v[118:121], v194, v169 op_sel_hi:[0,0,0]
	v_mfma_scale_f32_16x16x128_f8f6f4 v[98:101], v[10:17], v[208:215], v[98:101], v194, v169 op_sel_hi:[0,0,0]
	v_mfma_scale_f32_16x16x128_f8f6f4 v[102:105], v[2:9], v[208:215], v[102:105], v194, v169 op_sel_hi:[0,0,0]
	s_setprio 0
	s_barrier
	s_add_i32 s60, s92, s20
	v_lshl_add_u64 v[186:187], s[64:65], 0, v[164:165]
	s_mov_b32 m0, s60
	s_nop 0
	global_load_lds_dwordx4 v[186:187], off
	s_add_i32 m0, s60, 0x2000
	s_add_u32 s60, s64, 0x70000
	v_lshl_add_u64 v[188:189], s[64:65], 0, v[180:181]
	s_addc_u32 s61, s65, 0
	s_add_i32 s92, s93, s20
	global_load_lds_dwordx4 v[188:189], off
	v_lshl_add_u64 v[190:191], s[60:61], 0, v[164:165]
	s_mov_b32 m0, s92
	v_lshl_add_u64 v[192:193], s[68:69], 0, v[178:179]
	global_load_lds_dwordx4 v[190:191], off
	v_lshl_add_u64 v[190:191], s[60:61], 0, v[180:181]
	s_add_i32 m0, s92, 0x2000
	s_nop 0
	global_load_lds_dwordx4 v[190:191], off
	v_lshl_add_u64 v[190:191], s[68:69], 0, v[162:163]
	s_mov_b32 m0, s21
	s_nop 0
	global_load_lds_dwordx4 v[190:191], off
	s_mov_b32 m0, s22
	s_nop 0
	global_load_lds_dwordx4 v[192:193], off
	ds_read_b128 v[170:173], v198 offset:16384
	ds_read_b128 v[174:177], v198 offset:17408
	ds_read_b128 v[200:203], v198 offset:18432
	ds_read_b128 v[204:207], v198 offset:19456
	ds_read_b128 v[208:211], v198 offset:20480
	ds_read_b128 v[212:215], v198 offset:21504
	ds_read_b128 v[216:219], v198 offset:22528
	ds_read_b128 v[220:223], v198 offset:23552
	s_waitcnt vmcnt(8)
	s_waitcnt lgkmcnt(0)
	s_barrier
	s_setprio 1
	s_waitcnt lgkmcnt(0)
	v_mfma_scale_f32_16x16x128_f8f6f4 v[90:93], v[26:33], v[170:177], v[90:93], v194, v169 op_sel_hi:[0,0,0]
	v_mfma_scale_f32_16x16x128_f8f6f4 v[94:97], v[18:25], v[170:177], v[94:97], v194, v169 op_sel_hi:[0,0,0]
	v_mfma_scale_f32_16x16x128_f8f6f4 v[74:77], v[26:33], v[200:207], v[74:77], v194, v169 op_sel_hi:[0,0,0]
	v_mfma_scale_f32_16x16x128_f8f6f4 v[78:81], v[18:25], v[200:207], v[78:81], v194, v169 op_sel_hi:[0,0,0]
	v_mfma_scale_f32_16x16x128_f8f6f4 v[58:61], v[26:33], v[208:215], v[58:61], v194, v169 op_sel_hi:[0,0,0]
	v_mfma_scale_f32_16x16x128_f8f6f4 v[62:65], v[18:25], v[208:215], v[62:65], v194, v169 op_sel_hi:[0,0,0]
	v_mfma_scale_f32_16x16x128_f8f6f4 v[42:45], v[26:33], v[216:223], v[42:45], v194, v169 op_sel_hi:[0,0,0]
	v_mfma_scale_f32_16x16x128_f8f6f4 v[46:49], v[18:25], v[216:223], v[46:49], v194, v169 op_sel_hi:[0,0,0]
	s_setprio 0
	s_setprio 1
	v_mfma_scale_f32_16x16x128_f8f6f4 v[82:85], v[10:17], v[170:177], v[82:85], v194, v169 op_sel_hi:[0,0,0]
	v_mfma_scale_f32_16x16x128_f8f6f4 v[86:89], v[2:9], v[170:177], v[86:89], v194, v169 op_sel_hi:[0,0,0]
	v_mfma_scale_f32_16x16x128_f8f6f4 v[66:69], v[10:17], v[200:207], v[66:69], v194, v169 op_sel_hi:[0,0,0]
	v_mfma_scale_f32_16x16x128_f8f6f4 v[70:73], v[2:9], v[200:207], v[70:73], v194, v169 op_sel_hi:[0,0,0]
	v_mfma_scale_f32_16x16x128_f8f6f4 v[50:53], v[10:17], v[208:215], v[50:53], v194, v169 op_sel_hi:[0,0,0]
	v_mfma_scale_f32_16x16x128_f8f6f4 v[54:57], v[2:9], v[208:215], v[54:57], v194, v169 op_sel_hi:[0,0,0]
	v_mfma_scale_f32_16x16x128_f8f6f4 v[34:37], v[10:17], v[216:223], v[34:37], v194, v169 op_sel_hi:[0,0,0]
	v_mfma_scale_f32_16x16x128_f8f6f4 v[38:41], v[2:9], v[216:223], v[38:41], v194, v169 op_sel_hi:[0,0,0]
	s_setprio 0
	s_barrier
	s_add_i32 s92, 0, 0x18000
	s_add_i32 s93, 0, 0x1c000
	v_add_u32_e32 v2, s92, v196
	v_add_u32_e32 v6, s93, v196
	s_add_u32 s60, s68, 0x70000
	s_addc_u32 s61, s69, 0
	s_mov_b32 m0, s23
	v_lshl_add_u64 v[232:233], s[60:61], 0, v[162:163]
	global_load_lds_dwordx4 v[232:233], off
	v_lshl_add_u64 v[232:233], s[60:61], 0, v[178:179]
	s_mov_b32 m0, s70
	s_nop 0
	global_load_lds_dwordx4 v[232:233], off
	ds_read_b128 v[26:29], v2
	ds_read_b128 v[30:33], v2 offset:1024
	ds_read_b128 v[18:21], v2 offset:2048
	ds_read_b128 v[22:25], v2 offset:3072
	ds_read_b128 v[10:13], v6
	ds_read_b128 v[14:17], v6 offset:1024
	ds_read_b128 v[2:5], v6 offset:2048
	ds_read_b128 v[6:9], v6 offset:3072
	ds_read_b128 v[170:173], v198 offset:32768
	ds_read_b128 v[174:177], v198 offset:33792
	ds_read_b128 v[200:203], v198 offset:34816
	ds_read_b128 v[204:207], v198 offset:35840
	ds_read_b128 v[208:211], v198 offset:36864
	ds_read_b128 v[212:215], v198 offset:37888
	ds_read_b128 v[216:219], v198 offset:38912
	ds_read_b128 v[220:223], v198 offset:39936
	s_waitcnt vmcnt(8)
	s_waitcnt lgkmcnt(0)
	s_barrier
	s_setprio 1
	s_waitcnt lgkmcnt(0)
	v_mfma_scale_f32_16x16x128_f8f6f4 v[154:157], v[26:33], v[170:177], v[154:157], v194, v169 op_sel_hi:[0,0,0]
	v_mfma_scale_f32_16x16x128_f8f6f4 v[158:161], v[18:25], v[170:177], v[158:161], v194, v169 op_sel_hi:[0,0,0]
	v_mfma_scale_f32_16x16x128_f8f6f4 v[138:141], v[26:33], v[200:207], v[138:141], v194, v169 op_sel_hi:[0,0,0]
	v_mfma_scale_f32_16x16x128_f8f6f4 v[142:145], v[18:25], v[200:207], v[142:145], v194, v169 op_sel_hi:[0,0,0]
	v_mfma_scale_f32_16x16x128_f8f6f4 v[122:125], v[26:33], v[208:215], v[122:125], v194, v169 op_sel_hi:[0,0,0]
	v_mfma_scale_f32_16x16x128_f8f6f4 v[126:129], v[18:25], v[208:215], v[126:129], v194, v169 op_sel_hi:[0,0,0]
	v_mfma_scale_f32_16x16x128_f8f6f4 v[106:109], v[26:33], v[216:223], v[106:109], v194, v169 op_sel_hi:[0,0,0]
	v_mfma_scale_f32_16x16x128_f8f6f4 v[110:113], v[18:25], v[216:223], v[110:113], v194, v169 op_sel_hi:[0,0,0]
	s_setprio 0
	s_setprio 1
	v_mfma_scale_f32_16x16x128_f8f6f4 v[146:149], v[10:17], v[170:177], v[146:149], v194, v169 op_sel_hi:[0,0,0]
	v_mfma_scale_f32_16x16x128_f8f6f4 v[150:153], v[2:9], v[170:177], v[150:153], v194, v169 op_sel_hi:[0,0,0]
	v_mfma_scale_f32_16x16x128_f8f6f4 v[130:133], v[10:17], v[200:207], v[130:133], v194, v169 op_sel_hi:[0,0,0]
	v_mfma_scale_f32_16x16x128_f8f6f4 v[134:137], v[2:9], v[200:207], v[134:137], v194, v169 op_sel_hi:[0,0,0]
	v_mfma_scale_f32_16x16x128_f8f6f4 v[114:117], v[10:17], v[208:215], v[114:117], v194, v169 op_sel_hi:[0,0,0]
	v_mfma_scale_f32_16x16x128_f8f6f4 v[118:121], v[2:9], v[208:215], v[118:121], v194, v169 op_sel_hi:[0,0,0]
	v_mfma_scale_f32_16x16x128_f8f6f4 v[98:101], v[10:17], v[216:223], v[98:101], v194, v169 op_sel_hi:[0,0,0]
	v_mfma_scale_f32_16x16x128_f8f6f4 v[102:105], v[2:9], v[216:223], v[102:105], v194, v169 op_sel_hi:[0,0,0]
	s_setprio 0
	s_barrier
	s_add_i32 s60, s92, s20
	v_lshl_add_u64 v[186:187], v[186:187], 0, s[56:57]
	s_mov_b32 m0, s60
	s_nop 0
	global_load_lds_dwordx4 v[186:187], off
	s_add_i32 m0, s60, 0x2000
	s_add_u32 s60, s64, 0x70080
	v_lshl_add_u64 v[186:187], v[188:189], 0, s[56:57]
	s_addc_u32 s61, s65, 0
	s_add_i32 s64, s93, s20
	global_load_lds_dwordx4 v[186:187], off
	v_lshl_add_u64 v[186:187], s[60:61], 0, v[164:165]
	s_mov_b32 m0, s64
	s_nop 0
	global_load_lds_dwordx4 v[186:187], off
	v_lshl_add_u64 v[186:187], s[60:61], 0, v[180:181]
	s_add_i32 m0, s64, 0x2000
	s_nop 0
	global_load_lds_dwordx4 v[186:187], off
	v_lshl_add_u64 v[186:187], v[190:191], 0, s[56:57]
	s_mov_b32 m0, s71
	s_nop 0
	global_load_lds_dwordx4 v[186:187], off
	v_lshl_add_u64 v[186:187], v[192:193], 0, s[56:57]
	s_mov_b32 m0, s72
	s_nop 0
	global_load_lds_dwordx4 v[186:187], off
	ds_read_b128 v[170:173], v198 offset:49152
	ds_read_b128 v[174:177], v198 offset:50176
	ds_read_b128 v[200:203], v198 offset:51200
	ds_read_b128 v[204:207], v198 offset:52224
	ds_read_b128 v[208:211], v198 offset:53248
	ds_read_b128 v[212:215], v198 offset:54272
	ds_read_b128 v[216:219], v198 offset:55296
	ds_read_b128 v[220:223], v198 offset:56320
	s_waitcnt vmcnt(8)
	s_waitcnt lgkmcnt(0)
	s_barrier
	s_setprio 1
	s_waitcnt lgkmcnt(0)
	v_mfma_scale_f32_16x16x128_f8f6f4 v[90:93], v[26:33], v[170:177], v[90:93], v194, v169 op_sel_hi:[0,0,0]
	v_mfma_scale_f32_16x16x128_f8f6f4 v[94:97], v[18:25], v[170:177], v[94:97], v194, v169 op_sel_hi:[0,0,0]
	v_mfma_scale_f32_16x16x128_f8f6f4 v[74:77], v[26:33], v[200:207], v[74:77], v194, v169 op_sel_hi:[0,0,0]
	v_mfma_scale_f32_16x16x128_f8f6f4 v[78:81], v[18:25], v[200:207], v[78:81], v194, v169 op_sel_hi:[0,0,0]
	v_mfma_scale_f32_16x16x128_f8f6f4 v[58:61], v[26:33], v[208:215], v[58:61], v194, v169 op_sel_hi:[0,0,0]
	v_mfma_scale_f32_16x16x128_f8f6f4 v[62:65], v[18:25], v[208:215], v[62:65], v194, v169 op_sel_hi:[0,0,0]
	v_mfma_scale_f32_16x16x128_f8f6f4 v[42:45], v[26:33], v[216:223], v[42:45], v194, v169 op_sel_hi:[0,0,0]
	v_mfma_scale_f32_16x16x128_f8f6f4 v[46:49], v[18:25], v[216:223], v[46:49], v194, v169 op_sel_hi:[0,0,0]
	s_setprio 0
	s_setprio 1
	v_mfma_scale_f32_16x16x128_f8f6f4 v[82:85], v[10:17], v[170:177], v[82:85], v194, v169 op_sel_hi:[0,0,0]
	v_mfma_scale_f32_16x16x128_f8f6f4 v[86:89], v[2:9], v[170:177], v[86:89], v194, v169 op_sel_hi:[0,0,0]
	v_mfma_scale_f32_16x16x128_f8f6f4 v[66:69], v[10:17], v[200:207], v[66:69], v194, v169 op_sel_hi:[0,0,0]
	v_mfma_scale_f32_16x16x128_f8f6f4 v[70:73], v[2:9], v[200:207], v[70:73], v194, v169 op_sel_hi:[0,0,0]
	v_mfma_scale_f32_16x16x128_f8f6f4 v[50:53], v[10:17], v[208:215], v[50:53], v194, v169 op_sel_hi:[0,0,0]
	v_mfma_scale_f32_16x16x128_f8f6f4 v[54:57], v[2:9], v[208:215], v[54:57], v194, v169 op_sel_hi:[0,0,0]
	v_mfma_scale_f32_16x16x128_f8f6f4 v[34:37], v[10:17], v[216:223], v[34:37], v194, v169 op_sel_hi:[0,0,0]
	v_mfma_scale_f32_16x16x128_f8f6f4 v[38:41], v[2:9], v[216:223], v[38:41], v194, v169 op_sel_hi:[0,0,0]
	s_setprio 0
	s_barrier
	s_add_u32 s51, s51, 0x100
	s_addc_u32 s59, s59, 0
	s_cmp_ge_i32 s91, s8
	s_mov_b64 s[60:61], s[62:63]
	s_mov_b32 s64, s91
	s_cbranch_scc0 .LBB0_1777
	s_movk_i32 s93, 0x1000
	v_mov_b32_e32 v209, v1
	s_and_b64 vcc, exec, s[44:45]
	s_cbranch_vccz .LBB0_1780

.LBB0_1838:
	s_add_i32 s55, s55, 2
	s_add_u32 s60, s64, 0x100
	s_addc_u32 s61, s65, 0
	s_and_b64 s[68:69], s[62:63], exec
	s_cselect_b32 s68, 0, s60
	s_cselect_b32 s69, 0, s61
	s_add_u32 s68, s30, s68
	s_addc_u32 s69, s31, s69
	s_add_u32 s91, s47, s64
	s_addc_u32 s92, s49, s65
	s_and_b64 s[62:63], s[62:63], exec
	s_cselect_b32 s63, s53, s92
	s_cselect_b32 s62, s52, s91
	s_add_i32 s92, 0, 0x10000
	s_add_i32 s91, 0, 0x14000
	v_add_u32_e32 v2, s92, v210
	v_add_u32_e32 v6, s91, v210
	v_lshl_add_u64 v[222:223], v[194:195], 0, s[64:65]
	s_add_i32 m0, s59, 0xc000
	s_nop 0
	global_load_lds_dwordx4 v[222:223], off
	v_lshl_add_u64 v[222:223], v[192:193], 0, s[64:65]
	s_add_i32 m0, s59, 0xe000
	s_nop 0
	global_load_lds_dwordx4 v[222:223], off
	ds_read_b128 v[26:29], v2
	ds_read_b128 v[30:33], v2 offset:1024
	ds_read_b128 v[18:21], v2 offset:2048
	ds_read_b128 v[22:25], v2 offset:3072
	ds_read_b128 v[10:13], v6
	ds_read_b128 v[14:17], v6 offset:1024
	ds_read_b128 v[2:5], v6 offset:2048
	ds_read_b128 v[6:9], v6 offset:3072
	ds_read_b128 v[170:173], v212
	ds_read_b128 v[174:177], v212 offset:1024
	ds_read_b128 v[196:199], v212 offset:2048
	ds_read_b128 v[200:203], v212 offset:3072
	ds_read_b128 v[214:217], v212 offset:4096
	ds_read_b128 v[218:221], v212 offset:5120
	ds_read_b128 v[236:239], v212 offset:6144
	ds_read_b128 v[240:243], v212 offset:7168
	s_waitcnt vmcnt(8)
	s_waitcnt lgkmcnt(0)
	s_barrier
	s_setprio 1
	s_waitcnt lgkmcnt(0)
	v_mfma_scale_f32_16x16x128_f8f6f4 v[154:157], v[26:33], v[170:177], v[154:157], v208, v207 op_sel_hi:[0,0,0]
	v_mfma_scale_f32_16x16x128_f8f6f4 v[150:153], v[18:25], v[170:177], v[150:153], v208, v207 op_sel_hi:[0,0,0]
	v_mfma_scale_f32_16x16x128_f8f6f4 v[142:145], v[26:33], v[196:203], v[142:145], v208, v207 op_sel_hi:[0,0,0]
	v_mfma_scale_f32_16x16x128_f8f6f4 v[134:137], v[18:25], v[196:203], v[134:137], v208, v207 op_sel_hi:[0,0,0]
	v_mfma_scale_f32_16x16x128_f8f6f4 v[126:129], v[26:33], v[214:221], v[126:129], v208, v207 op_sel_hi:[0,0,0]
	v_mfma_scale_f32_16x16x128_f8f6f4 v[118:121], v[18:25], v[214:221], v[118:121], v208, v207 op_sel_hi:[0,0,0]
	v_mfma_scale_f32_16x16x128_f8f6f4 v[110:113], v[26:33], v[236:243], v[110:113], v208, v207 op_sel_hi:[0,0,0]
	v_mfma_scale_f32_16x16x128_f8f6f4 v[102:105], v[18:25], v[236:243], v[102:105], v208, v207 op_sel_hi:[0,0,0]
	s_setprio 0
	s_setprio 1
	v_mfma_scale_f32_16x16x128_f8f6f4 v[158:161], v[10:17], v[170:177], v[158:161], v208, v207 op_sel_hi:[0,0,0]
	v_mfma_scale_f32_16x16x128_f8f6f4 v[146:149], v[2:9], v[170:177], v[146:149], v208, v207 op_sel_hi:[0,0,0]
	v_mfma_scale_f32_16x16x128_f8f6f4 v[138:141], v[10:17], v[196:203], v[138:141], v208, v207 op_sel_hi:[0,0,0]
	v_mfma_scale_f32_16x16x128_f8f6f4 v[130:133], v[2:9], v[196:203], v[130:133], v208, v207 op_sel_hi:[0,0,0]
	v_mfma_scale_f32_16x16x128_f8f6f4 v[122:125], v[10:17], v[214:221], v[122:125], v208, v207 op_sel_hi:[0,0,0]
	v_mfma_scale_f32_16x16x128_f8f6f4 v[114:117], v[2:9], v[214:221], v[114:117], v208, v207 op_sel_hi:[0,0,0]
	v_mfma_scale_f32_16x16x128_f8f6f4 v[106:109], v[10:17], v[236:243], v[106:109], v208, v207 op_sel_hi:[0,0,0]
	v_mfma_scale_f32_16x16x128_f8f6f4 v[98:101], v[2:9], v[236:243], v[98:101], v208, v207 op_sel_hi:[0,0,0]
	s_setprio 0
	s_barrier
	s_add_i32 s64, s92, s22
	v_lshl_add_u64 v[196:197], s[62:63], 0, v[162:163]
	s_mov_b32 m0, s64
	s_nop 0
	global_load_lds_dwordx4 v[196:197], off
	s_add_i32 m0, s64, 0x2000
	s_add_u32 s64, s62, 0x20000
	v_lshl_add_u64 v[198:199], s[62:63], 0, v[164:165]
	s_addc_u32 s65, s63, 0
	s_add_i32 s91, s91, s22
	global_load_lds_dwordx4 v[198:199], off
	v_lshl_add_u64 v[200:201], s[64:65], 0, v[162:163]
	s_mov_b32 m0, s91
	s_nop 0
	global_load_lds_dwordx4 v[200:201], off
	v_lshl_add_u64 v[200:201], s[64:65], 0, v[164:165]
	s_add_i32 m0, s91, 0x2000
	s_nop 0
	global_load_lds_dwordx4 v[200:201], off
	s_mov_b32 m0, s59
	s_nop 0
	global_load_lds_dwordx4 v166, s[68:69]
	s_mov_b32 m0, s71
	s_nop 0
	global_load_lds_dwordx4 v178, s[68:69]
	ds_read_b128 v[170:173], v212 offset:16384
	ds_read_b128 v[174:177], v212 offset:17408
	ds_read_b128 v[214:217], v212 offset:18432
	ds_read_b128 v[218:221], v212 offset:19456
	ds_read_b128 v[236:239], v212 offset:20480
	ds_read_b128 v[240:243], v212 offset:21504
	ds_read_b128 v[244:247], v212 offset:22528
	ds_read_b128 v[248:251], v212 offset:23552
	v_mov_b32_e32 v179, v167
	v_lshl_add_u64 v[202:203], s[68:69], 0, v[166:167]
	v_lshl_add_u64 v[200:201], s[68:69], 0, v[178:179]
	s_waitcnt vmcnt(8)
	s_waitcnt lgkmcnt(0)
	s_barrier
	s_setprio 1
	s_waitcnt lgkmcnt(0)
	v_mfma_scale_f32_16x16x128_f8f6f4 v[94:97], v[26:33], v[170:177], v[94:97], v208, v207 op_sel_hi:[0,0,0]
	v_mfma_scale_f32_16x16x128_f8f6f4 v[86:89], v[18:25], v[170:177], v[86:89], v208, v207 op_sel_hi:[0,0,0]
	v_mfma_scale_f32_16x16x128_f8f6f4 v[78:81], v[26:33], v[214:221], v[78:81], v208, v207 op_sel_hi:[0,0,0]
	v_mfma_scale_f32_16x16x128_f8f6f4 v[70:73], v[18:25], v[214:221], v[70:73], v208, v207 op_sel_hi:[0,0,0]
	v_mfma_scale_f32_16x16x128_f8f6f4 v[62:65], v[26:33], v[236:243], v[62:65], v208, v207 op_sel_hi:[0,0,0]
	v_mfma_scale_f32_16x16x128_f8f6f4 v[54:57], v[18:25], v[236:243], v[54:57], v208, v207 op_sel_hi:[0,0,0]
	v_mfma_scale_f32_16x16x128_f8f6f4 v[46:49], v[26:33], v[244:251], v[46:49], v208, v207 op_sel_hi:[0,0,0]
	v_mfma_scale_f32_16x16x128_f8f6f4 v[38:41], v[18:25], v[244:251], v[38:41], v208, v207 op_sel_hi:[0,0,0]
	s_setprio 0
	s_setprio 1
	v_mfma_scale_f32_16x16x128_f8f6f4 v[90:93], v[10:17], v[170:177], v[90:93], v208, v207 op_sel_hi:[0,0,0]
	v_mfma_scale_f32_16x16x128_f8f6f4 v[82:85], v[2:9], v[170:177], v[82:85], v208, v207 op_sel_hi:[0,0,0]
	v_mfma_scale_f32_16x16x128_f8f6f4 v[74:77], v[10:17], v[214:221], v[74:77], v208, v207 op_sel_hi:[0,0,0]
	v_mfma_scale_f32_16x16x128_f8f6f4 v[66:69], v[2:9], v[214:221], v[66:69], v208, v207 op_sel_hi:[0,0,0]
	v_mfma_scale_f32_16x16x128_f8f6f4 v[58:61], v[10:17], v[236:243], v[58:61], v208, v207 op_sel_hi:[0,0,0]
	v_mfma_scale_f32_16x16x128_f8f6f4 v[50:53], v[2:9], v[236:243], v[50:53], v208, v207 op_sel_hi:[0,0,0]
	v_mfma_scale_f32_16x16x128_f8f6f4 v[42:45], v[10:17], v[244:251], v[42:45], v208, v207 op_sel_hi:[0,0,0]
	v_mfma_scale_f32_16x16x128_f8f6f4 v[34:37], v[2:9], v[244:251], v[34:37], v208, v207 op_sel_hi:[0,0,0]
	s_setprio 0
	s_barrier
	s_add_i32 s64, 0, 0x18000
	s_add_i32 s65, 0, 0x1c000
	v_add_u32_e32 v2, s64, v210
	v_add_u32_e32 v6, s65, v210
	s_mov_b32 m0, s72
	s_nop 0
	global_load_lds_dwordx4 v180, s[68:69]
	s_mov_b32 m0, s73
	s_nop 0
	global_load_lds_dwordx4 v182, s[68:69]
	ds_read_b128 v[26:29], v2
	ds_read_b128 v[30:33], v2 offset:1024
	ds_read_b128 v[18:21], v2 offset:2048
	ds_read_b128 v[22:25], v2 offset:3072
	ds_read_b128 v[10:13], v6
	ds_read_b128 v[14:17], v6 offset:1024
	ds_read_b128 v[2:5], v6 offset:2048
	ds_read_b128 v[6:9], v6 offset:3072
	ds_read_b128 v[170:173], v212 offset:32768
	ds_read_b128 v[174:177], v212 offset:33792
	ds_read_b128 v[214:217], v212 offset:34816
	ds_read_b128 v[218:221], v212 offset:35840
	ds_read_b128 v[236:239], v212 offset:36864
	ds_read_b128 v[240:243], v212 offset:37888
	ds_read_b128 v[244:247], v212 offset:38912
	ds_read_b128 v[248:251], v212 offset:39936
	s_waitcnt vmcnt(8)
	s_waitcnt lgkmcnt(0)
	s_barrier
	s_setprio 1
	s_waitcnt lgkmcnt(0)
	v_mfma_scale_f32_16x16x128_f8f6f4 v[154:157], v[26:33], v[170:177], v[154:157], v208, v207 op_sel_hi:[0,0,0]
	v_mfma_scale_f32_16x16x128_f8f6f4 v[150:153], v[18:25], v[170:177], v[150:153], v208, v207 op_sel_hi:[0,0,0]
	v_mfma_scale_f32_16x16x128_f8f6f4 v[142:145], v[26:33], v[214:221], v[142:145], v208, v207 op_sel_hi:[0,0,0]
	v_mfma_scale_f32_16x16x128_f8f6f4 v[134:137], v[18:25], v[214:221], v[134:137], v208, v207 op_sel_hi:[0,0,0]
	v_mfma_scale_f32_16x16x128_f8f6f4 v[126:129], v[26:33], v[236:243], v[126:129], v208, v207 op_sel_hi:[0,0,0]
	v_mfma_scale_f32_16x16x128_f8f6f4 v[118:121], v[18:25], v[236:243], v[118:121], v208, v207 op_sel_hi:[0,0,0]
	v_mfma_scale_f32_16x16x128_f8f6f4 v[110:113], v[26:33], v[244:251], v[110:113], v208, v207 op_sel_hi:[0,0,0]
	v_mfma_scale_f32_16x16x128_f8f6f4 v[102:105], v[18:25], v[244:251], v[102:105], v208, v207 op_sel_hi:[0,0,0]
	s_setprio 0
	s_setprio 1
	v_mfma_scale_f32_16x16x128_f8f6f4 v[158:161], v[10:17], v[170:177], v[158:161], v208, v207 op_sel_hi:[0,0,0]
	v_mfma_scale_f32_16x16x128_f8f6f4 v[146:149], v[2:9], v[170:177], v[146:149], v208, v207 op_sel_hi:[0,0,0]
	v_mfma_scale_f32_16x16x128_f8f6f4 v[138:141], v[10:17], v[214:221], v[138:141], v208, v207 op_sel_hi:[0,0,0]
	v_mfma_scale_f32_16x16x128_f8f6f4 v[130:133], v[2:9], v[214:221], v[130:133], v208, v207 op_sel_hi:[0,0,0]
	v_mfma_scale_f32_16x16x128_f8f6f4 v[122:125], v[10:17], v[236:243], v[122:125], v208, v207 op_sel_hi:[0,0,0]
	v_mfma_scale_f32_16x16x128_f8f6f4 v[114:117], v[2:9], v[236:243], v[114:117], v208, v207 op_sel_hi:[0,0,0]
	v_mfma_scale_f32_16x16x128_f8f6f4 v[106:109], v[10:17], v[244:251], v[106:109], v208, v207 op_sel_hi:[0,0,0]
	v_mfma_scale_f32_16x16x128_f8f6f4 v[98:101], v[2:9], v[244:251], v[98:101], v208, v207 op_sel_hi:[0,0,0]
	s_setprio 0
	s_barrier
	s_add_i32 s64, s64, s22
	v_lshl_add_u64 v[196:197], v[196:197], 0, s[56:57]
	s_mov_b32 m0, s64
	s_nop 0
	global_load_lds_dwordx4 v[196:197], off
	s_add_i32 m0, s64, 0x2000
	s_add_u32 s62, s62, 0x20080
	v_lshl_add_u64 v[196:197], v[198:199], 0, s[56:57]
	s_addc_u32 s63, s63, 0
	s_add_i32 s64, s65, s22
	global_load_lds_dwordx4 v[196:197], off
	v_lshl_add_u64 v[196:197], s[62:63], 0, v[162:163]
	s_mov_b32 m0, s64
	s_nop 0
	global_load_lds_dwordx4 v[196:197], off
	v_lshl_add_u64 v[196:197], s[62:63], 0, v[164:165]
	s_add_i32 m0, s64, 0x2000
	s_nop 0
	global_load_lds_dwordx4 v[196:197], off
	v_lshl_add_u64 v[196:197], v[202:203], 0, s[56:57]
	s_mov_b32 m0, s74
	s_nop 0
	global_load_lds_dwordx4 v[196:197], off
	v_lshl_add_u64 v[196:197], v[200:201], 0, s[56:57]
	s_mov_b32 m0, s75
	s_nop 0
	global_load_lds_dwordx4 v[196:197], off
	ds_read_b128 v[170:173], v212 offset:49152
	ds_read_b128 v[174:177], v212 offset:50176
	ds_read_b128 v[214:217], v212 offset:51200
	ds_read_b128 v[218:221], v212 offset:52224
	ds_read_b128 v[236:239], v212 offset:53248
	ds_read_b128 v[240:243], v212 offset:54272
	ds_read_b128 v[244:247], v212 offset:55296
	ds_read_b128 v[248:251], v212 offset:56320
	s_waitcnt vmcnt(8)
	s_waitcnt lgkmcnt(0)
	s_barrier
	s_setprio 1
	s_waitcnt lgkmcnt(0)
	v_mfma_scale_f32_16x16x128_f8f6f4 v[94:97], v[26:33], v[170:177], v[94:97], v208, v207 op_sel_hi:[0,0,0]
	v_mfma_scale_f32_16x16x128_f8f6f4 v[86:89], v[18:25], v[170:177], v[86:89], v208, v207 op_sel_hi:[0,0,0]
	v_mfma_scale_f32_16x16x128_f8f6f4 v[78:81], v[26:33], v[214:221], v[78:81], v208, v207 op_sel_hi:[0,0,0]
	v_mfma_scale_f32_16x16x128_f8f6f4 v[70:73], v[18:25], v[214:221], v[70:73], v208, v207 op_sel_hi:[0,0,0]
	v_mfma_scale_f32_16x16x128_f8f6f4 v[62:65], v[26:33], v[236:243], v[62:65], v208, v207 op_sel_hi:[0,0,0]
	v_mfma_scale_f32_16x16x128_f8f6f4 v[54:57], v[18:25], v[236:243], v[54:57], v208, v207 op_sel_hi:[0,0,0]
	v_mfma_scale_f32_16x16x128_f8f6f4 v[46:49], v[26:33], v[244:251], v[46:49], v208, v207 op_sel_hi:[0,0,0]
	v_mfma_scale_f32_16x16x128_f8f6f4 v[38:41], v[18:25], v[244:251], v[38:41], v208, v207 op_sel_hi:[0,0,0]
	s_setprio 0
	s_setprio 1
	v_mfma_scale_f32_16x16x128_f8f6f4 v[90:93], v[10:17], v[170:177], v[90:93], v208, v207 op_sel_hi:[0,0,0]
	v_mfma_scale_f32_16x16x128_f8f6f4 v[82:85], v[2:9], v[170:177], v[82:85], v208, v207 op_sel_hi:[0,0,0]
	v_mfma_scale_f32_16x16x128_f8f6f4 v[74:77], v[10:17], v[214:221], v[74:77], v208, v207 op_sel_hi:[0,0,0]
	v_mfma_scale_f32_16x16x128_f8f6f4 v[66:69], v[2:9], v[214:221], v[66:69], v208, v207 op_sel_hi:[0,0,0]
	v_mfma_scale_f32_16x16x128_f8f6f4 v[58:61], v[10:17], v[236:243], v[58:61], v208, v207 op_sel_hi:[0,0,0]
	v_mfma_scale_f32_16x16x128_f8f6f4 v[50:53], v[2:9], v[236:243], v[50:53], v208, v207 op_sel_hi:[0,0,0]
	v_mfma_scale_f32_16x16x128_f8f6f4 v[42:45], v[10:17], v[244:251], v[42:45], v208, v207 op_sel_hi:[0,0,0]
	v_mfma_scale_f32_16x16x128_f8f6f4 v[34:37], v[2:9], v[244:251], v[34:37], v208, v207 op_sel_hi:[0,0,0]
	s_setprio 0
	s_barrier
	s_cmp_lt_i32 s55, s11
	s_cbranch_scc0 .LBB0_1841
	s_mov_b64 s[64:65], s[60:61]
	s_branch .LBB0_1836

.LBB0_1923:
	s_add_i32 s75, s70, 2
	s_add_u32 s42, s18, 0x100
	s_addc_u32 s43, s19, 0
	s_add_i32 s46, 0, 0x10000
	s_cmp_eq_u32 s14, s70
	s_cselect_b32 vcc_hi, s69, s43
	s_cselect_b32 vcc_lo, s68, s42
	s_cselect_b32 s71, s37, s45
	s_cselect_b32 s70, s36, s35
	s_add_i32 s47, 0, 0x14000
	v_add_u32_e32 v2, s46, v196
	v_add_u32_e32 v6, s47, v196
	v_lshl_add_u64 v[218:219], s[18:19], 0, v[184:185]
	s_add_i32 m0, s73, 0xc000
	s_nop 0
	global_load_lds_dwordx4 v[218:219], off
	v_lshl_add_u64 v[218:219], s[18:19], 0, v[182:183]
	s_add_i32 m0, s73, 0xe000
	s_nop 0
	global_load_lds_dwordx4 v[218:219], off
	ds_read_b128 v[26:29], v2
	ds_read_b128 v[30:33], v2 offset:1024
	ds_read_b128 v[18:21], v2 offset:2048
	ds_read_b128 v[22:25], v2 offset:3072
	ds_read_b128 v[10:13], v6
	ds_read_b128 v[14:17], v6 offset:1024
	ds_read_b128 v[2:5], v6 offset:2048
	ds_read_b128 v[6:9], v6 offset:3072
	ds_read_b128 v[170:173], v201
	ds_read_b128 v[174:177], v201 offset:1024
	ds_read_b128 v[186:189], v201 offset:2048
	ds_read_b128 v[190:193], v201 offset:3072
	ds_read_b128 v[202:205], v201 offset:4096
	ds_read_b128 v[206:209], v201 offset:5120
	ds_read_b128 v[210:213], v201 offset:6144
	ds_read_b128 v[214:217], v201 offset:7168
	s_waitcnt vmcnt(8)
	s_waitcnt lgkmcnt(0)
	s_barrier
	s_setprio 1
	s_waitcnt lgkmcnt(0)
	v_mfma_scale_f32_16x16x128_f8f6f4 v[158:161], v[26:33], v[170:177], v[158:161], v194, v169 op_sel_hi:[0,0,0]
	v_mfma_scale_f32_16x16x128_f8f6f4 v[154:157], v[18:25], v[170:177], v[154:157], v194, v169 op_sel_hi:[0,0,0]
	v_mfma_scale_f32_16x16x128_f8f6f4 v[142:145], v[26:33], v[186:193], v[142:145], v194, v169 op_sel_hi:[0,0,0]
	v_mfma_scale_f32_16x16x128_f8f6f4 v[138:141], v[18:25], v[186:193], v[138:141], v194, v169 op_sel_hi:[0,0,0]
	v_mfma_scale_f32_16x16x128_f8f6f4 v[126:129], v[26:33], v[202:209], v[126:129], v194, v169 op_sel_hi:[0,0,0]
	v_mfma_scale_f32_16x16x128_f8f6f4 v[122:125], v[18:25], v[202:209], v[122:125], v194, v169 op_sel_hi:[0,0,0]
	v_mfma_scale_f32_16x16x128_f8f6f4 v[110:113], v[26:33], v[210:217], v[110:113], v194, v169 op_sel_hi:[0,0,0]
	v_mfma_scale_f32_16x16x128_f8f6f4 v[106:109], v[18:25], v[210:217], v[106:109], v194, v169 op_sel_hi:[0,0,0]
	s_setprio 0
	s_setprio 1
	v_mfma_scale_f32_16x16x128_f8f6f4 v[150:153], v[10:17], v[170:177], v[150:153], v194, v169 op_sel_hi:[0,0,0]
	v_mfma_scale_f32_16x16x128_f8f6f4 v[146:149], v[2:9], v[170:177], v[146:149], v194, v169 op_sel_hi:[0,0,0]
	v_mfma_scale_f32_16x16x128_f8f6f4 v[134:137], v[10:17], v[186:193], v[134:137], v194, v169 op_sel_hi:[0,0,0]
	v_mfma_scale_f32_16x16x128_f8f6f4 v[130:133], v[2:9], v[186:193], v[130:133], v194, v169 op_sel_hi:[0,0,0]
	v_mfma_scale_f32_16x16x128_f8f6f4 v[118:121], v[10:17], v[202:209], v[118:121], v194, v169 op_sel_hi:[0,0,0]
	v_mfma_scale_f32_16x16x128_f8f6f4 v[114:117], v[2:9], v[202:209], v[114:117], v194, v169 op_sel_hi:[0,0,0]
	v_mfma_scale_f32_16x16x128_f8f6f4 v[102:105], v[10:17], v[210:217], v[102:105], v194, v169 op_sel_hi:[0,0,0]
	v_mfma_scale_f32_16x16x128_f8f6f4 v[98:101], v[2:9], v[210:217], v[98:101], v194, v169 op_sel_hi:[0,0,0]
	s_setprio 0
	s_barrier
	s_add_i32 s18, s46, s95
	v_lshl_add_u64 v[186:187], s[70:71], 0, v[164:165]
	s_mov_b32 m0, s18
	s_nop 0
	global_load_lds_dwordx4 v[186:187], off
	s_add_i32 m0, s18, 0x2000
	s_add_u32 s18, s70, 0x70000
	v_lshl_add_u64 v[188:189], s[70:71], 0, v[180:181]
	s_addc_u32 s19, s71, 0
	s_add_i32 s46, s47, s95
	global_load_lds_dwordx4 v[188:189], off
	v_lshl_add_u64 v[190:191], s[18:19], 0, v[164:165]
	s_mov_b32 m0, s46
	v_lshl_add_u64 v[192:193], vcc, 0, v[178:179]
	global_load_lds_dwordx4 v[190:191], off
	v_lshl_add_u64 v[190:191], s[18:19], 0, v[180:181]
	s_add_i32 m0, s46, 0x2000
	s_nop 0
	global_load_lds_dwordx4 v[190:191], off
	v_lshl_add_u64 v[190:191], vcc, 0, v[162:163]
	s_mov_b32 m0, s73
	s_nop 0
	global_load_lds_dwordx4 v[190:191], off
	s_mov_b32 m0, s8
	s_nop 0
	global_load_lds_dwordx4 v[192:193], off
	ds_read_b128 v[170:173], v201 offset:16384
	ds_read_b128 v[174:177], v201 offset:17408
	ds_read_b128 v[202:205], v201 offset:18432
	ds_read_b128 v[206:209], v201 offset:19456
	ds_read_b128 v[210:213], v201 offset:20480
	ds_read_b128 v[214:217], v201 offset:21504
	ds_read_b128 v[236:239], v201 offset:22528
	ds_read_b128 v[240:243], v201 offset:23552
	s_waitcnt vmcnt(8)
	s_waitcnt lgkmcnt(0)
	s_barrier
	s_setprio 1
	s_waitcnt lgkmcnt(0)
	v_mfma_scale_f32_16x16x128_f8f6f4 v[94:97], v[26:33], v[170:177], v[94:97], v194, v169 op_sel_hi:[0,0,0]
	v_mfma_scale_f32_16x16x128_f8f6f4 v[90:93], v[18:25], v[170:177], v[90:93], v194, v169 op_sel_hi:[0,0,0]
	v_mfma_scale_f32_16x16x128_f8f6f4 v[78:81], v[26:33], v[202:209], v[78:81], v194, v169 op_sel_hi:[0,0,0]
	v_mfma_scale_f32_16x16x128_f8f6f4 v[74:77], v[18:25], v[202:209], v[74:77], v194, v169 op_sel_hi:[0,0,0]
	v_mfma_scale_f32_16x16x128_f8f6f4 v[62:65], v[26:33], v[210:217], v[62:65], v194, v169 op_sel_hi:[0,0,0]
	v_mfma_scale_f32_16x16x128_f8f6f4 v[58:61], v[18:25], v[210:217], v[58:61], v194, v169 op_sel_hi:[0,0,0]
	v_mfma_scale_f32_16x16x128_f8f6f4 v[46:49], v[26:33], v[236:243], v[46:49], v194, v169 op_sel_hi:[0,0,0]
	v_mfma_scale_f32_16x16x128_f8f6f4 v[42:45], v[18:25], v[236:243], v[42:45], v194, v169 op_sel_hi:[0,0,0]
	s_setprio 0
	s_setprio 1
	v_mfma_scale_f32_16x16x128_f8f6f4 v[86:89], v[10:17], v[170:177], v[86:89], v194, v169 op_sel_hi:[0,0,0]
	v_mfma_scale_f32_16x16x128_f8f6f4 v[82:85], v[2:9], v[170:177], v[82:85], v194, v169 op_sel_hi:[0,0,0]
	v_mfma_scale_f32_16x16x128_f8f6f4 v[70:73], v[10:17], v[202:209], v[70:73], v194, v169 op_sel_hi:[0,0,0]
	v_mfma_scale_f32_16x16x128_f8f6f4 v[66:69], v[2:9], v[202:209], v[66:69], v194, v169 op_sel_hi:[0,0,0]
	v_mfma_scale_f32_16x16x128_f8f6f4 v[54:57], v[10:17], v[210:217], v[54:57], v194, v169 op_sel_hi:[0,0,0]
	v_mfma_scale_f32_16x16x128_f8f6f4 v[50:53], v[2:9], v[210:217], v[50:53], v194, v169 op_sel_hi:[0,0,0]
	v_mfma_scale_f32_16x16x128_f8f6f4 v[38:41], v[10:17], v[236:243], v[38:41], v194, v169 op_sel_hi:[0,0,0]
	v_mfma_scale_f32_16x16x128_f8f6f4 v[34:37], v[2:9], v[236:243], v[34:37], v194, v169 op_sel_hi:[0,0,0]
	s_setprio 0
	s_barrier
	s_add_i32 s46, 0, 0x18000
	s_add_i32 s47, 0, 0x1c000
	v_add_u32_e32 v2, s46, v196
	v_add_u32_e32 v6, s47, v196
	s_add_u32 s18, vcc_lo, 0x70000
	s_addc_u32 s19, vcc_hi, 0
	s_mov_b32 m0, s11
	v_lshl_add_u64 v[218:219], s[18:19], 0, v[162:163]
	global_load_lds_dwordx4 v[218:219], off
	v_lshl_add_u64 v[218:219], s[18:19], 0, v[178:179]
	s_mov_b32 m0, s84
	s_nop 0
	global_load_lds_dwordx4 v[218:219], off
	ds_read_b128 v[26:29], v2
	ds_read_b128 v[30:33], v2 offset:1024
	ds_read_b128 v[18:21], v2 offset:2048
	ds_read_b128 v[22:25], v2 offset:3072
	ds_read_b128 v[10:13], v6
	ds_read_b128 v[14:17], v6 offset:1024
	ds_read_b128 v[2:5], v6 offset:2048
	ds_read_b128 v[6:9], v6 offset:3072
	ds_read_b128 v[170:173], v201 offset:32768
	ds_read_b128 v[174:177], v201 offset:33792
	ds_read_b128 v[202:205], v201 offset:34816
	ds_read_b128 v[206:209], v201 offset:35840
	ds_read_b128 v[210:213], v201 offset:36864
	ds_read_b128 v[214:217], v201 offset:37888
	ds_read_b128 v[236:239], v201 offset:38912
	ds_read_b128 v[240:243], v201 offset:39936
	s_waitcnt vmcnt(8)
	s_waitcnt lgkmcnt(0)
	s_barrier
	s_setprio 1
	s_waitcnt lgkmcnt(0)
	v_mfma_scale_f32_16x16x128_f8f6f4 v[158:161], v[26:33], v[170:177], v[158:161], v194, v169 op_sel_hi:[0,0,0]
	v_mfma_scale_f32_16x16x128_f8f6f4 v[154:157], v[18:25], v[170:177], v[154:157], v194, v169 op_sel_hi:[0,0,0]
	v_mfma_scale_f32_16x16x128_f8f6f4 v[142:145], v[26:33], v[202:209], v[142:145], v194, v169 op_sel_hi:[0,0,0]
	v_mfma_scale_f32_16x16x128_f8f6f4 v[138:141], v[18:25], v[202:209], v[138:141], v194, v169 op_sel_hi:[0,0,0]
	v_mfma_scale_f32_16x16x128_f8f6f4 v[126:129], v[26:33], v[210:217], v[126:129], v194, v169 op_sel_hi:[0,0,0]
	v_mfma_scale_f32_16x16x128_f8f6f4 v[122:125], v[18:25], v[210:217], v[122:125], v194, v169 op_sel_hi:[0,0,0]
	v_mfma_scale_f32_16x16x128_f8f6f4 v[110:113], v[26:33], v[236:243], v[110:113], v194, v169 op_sel_hi:[0,0,0]
	v_mfma_scale_f32_16x16x128_f8f6f4 v[106:109], v[18:25], v[236:243], v[106:109], v194, v169 op_sel_hi:[0,0,0]
	s_setprio 0
	s_setprio 1
	v_mfma_scale_f32_16x16x128_f8f6f4 v[150:153], v[10:17], v[170:177], v[150:153], v194, v169 op_sel_hi:[0,0,0]
	v_mfma_scale_f32_16x16x128_f8f6f4 v[146:149], v[2:9], v[170:177], v[146:149], v194, v169 op_sel_hi:[0,0,0]
	v_mfma_scale_f32_16x16x128_f8f6f4 v[134:137], v[10:17], v[202:209], v[134:137], v194, v169 op_sel_hi:[0,0,0]
	v_mfma_scale_f32_16x16x128_f8f6f4 v[130:133], v[2:9], v[202:209], v[130:133], v194, v169 op_sel_hi:[0,0,0]
	v_mfma_scale_f32_16x16x128_f8f6f4 v[118:121], v[10:17], v[210:217], v[118:121], v194, v169 op_sel_hi:[0,0,0]
	v_mfma_scale_f32_16x16x128_f8f6f4 v[114:117], v[2:9], v[210:217], v[114:117], v194, v169 op_sel_hi:[0,0,0]
	v_mfma_scale_f32_16x16x128_f8f6f4 v[102:105], v[10:17], v[236:243], v[102:105], v194, v169 op_sel_hi:[0,0,0]
	v_mfma_scale_f32_16x16x128_f8f6f4 v[98:101], v[2:9], v[236:243], v[98:101], v194, v169 op_sel_hi:[0,0,0]
	s_setprio 0
	s_barrier
	s_add_i32 s18, s46, s95
	v_lshl_add_u64 v[186:187], v[186:187], 0, s[56:57]
	s_mov_b32 m0, s18
	s_nop 0
	global_load_lds_dwordx4 v[186:187], off
	s_add_i32 m0, s18, 0x2000
	s_add_u32 s18, s70, 0x70080
	v_lshl_add_u64 v[186:187], v[188:189], 0, s[56:57]
	s_addc_u32 s19, s71, 0
	s_add_i32 s46, s47, s95
	global_load_lds_dwordx4 v[186:187], off
	v_lshl_add_u64 v[186:187], s[18:19], 0, v[164:165]
	s_mov_b32 m0, s46
	s_nop 0
	global_load_lds_dwordx4 v[186:187], off
	v_lshl_add_u64 v[186:187], s[18:19], 0, v[180:181]
	s_add_i32 m0, s46, 0x2000
	s_nop 0
	global_load_lds_dwordx4 v[186:187], off
	v_lshl_add_u64 v[186:187], v[190:191], 0, s[56:57]
	s_mov_b32 m0, s0
	s_nop 0
	global_load_lds_dwordx4 v[186:187], off
	v_lshl_add_u64 v[186:187], v[192:193], 0, s[56:57]
	s_mov_b32 m0, s88
	s_nop 0
	global_load_lds_dwordx4 v[186:187], off
	ds_read_b128 v[170:173], v201 offset:49152
	ds_read_b128 v[174:177], v201 offset:50176
	ds_read_b128 v[202:205], v201 offset:51200
	ds_read_b128 v[206:209], v201 offset:52224
	ds_read_b128 v[210:213], v201 offset:53248
	ds_read_b128 v[214:217], v201 offset:54272
	ds_read_b128 v[236:239], v201 offset:55296
	ds_read_b128 v[240:243], v201 offset:56320
	s_waitcnt vmcnt(8)
	s_waitcnt lgkmcnt(0)
	s_barrier
	s_setprio 1
	s_waitcnt lgkmcnt(0)
	v_mfma_scale_f32_16x16x128_f8f6f4 v[94:97], v[26:33], v[170:177], v[94:97], v194, v169 op_sel_hi:[0,0,0]
	v_mfma_scale_f32_16x16x128_f8f6f4 v[90:93], v[18:25], v[170:177], v[90:93], v194, v169 op_sel_hi:[0,0,0]
	v_mfma_scale_f32_16x16x128_f8f6f4 v[78:81], v[26:33], v[202:209], v[78:81], v194, v169 op_sel_hi:[0,0,0]
	v_mfma_scale_f32_16x16x128_f8f6f4 v[74:77], v[18:25], v[202:209], v[74:77], v194, v169 op_sel_hi:[0,0,0]
	v_mfma_scale_f32_16x16x128_f8f6f4 v[62:65], v[26:33], v[210:217], v[62:65], v194, v169 op_sel_hi:[0,0,0]
	v_mfma_scale_f32_16x16x128_f8f6f4 v[58:61], v[18:25], v[210:217], v[58:61], v194, v169 op_sel_hi:[0,0,0]
	v_mfma_scale_f32_16x16x128_f8f6f4 v[46:49], v[26:33], v[236:243], v[46:49], v194, v169 op_sel_hi:[0,0,0]
	v_mfma_scale_f32_16x16x128_f8f6f4 v[42:45], v[18:25], v[236:243], v[42:45], v194, v169 op_sel_hi:[0,0,0]
	s_setprio 0
	s_setprio 1
	v_mfma_scale_f32_16x16x128_f8f6f4 v[86:89], v[10:17], v[170:177], v[86:89], v194, v169 op_sel_hi:[0,0,0]
	v_mfma_scale_f32_16x16x128_f8f6f4 v[82:85], v[2:9], v[170:177], v[82:85], v194, v169 op_sel_hi:[0,0,0]
	v_mfma_scale_f32_16x16x128_f8f6f4 v[70:73], v[10:17], v[202:209], v[70:73], v194, v169 op_sel_hi:[0,0,0]
	v_mfma_scale_f32_16x16x128_f8f6f4 v[66:69], v[2:9], v[202:209], v[66:69], v194, v169 op_sel_hi:[0,0,0]
	v_mfma_scale_f32_16x16x128_f8f6f4 v[54:57], v[10:17], v[210:217], v[54:57], v194, v169 op_sel_hi:[0,0,0]
	v_mfma_scale_f32_16x16x128_f8f6f4 v[50:53], v[2:9], v[210:217], v[50:53], v194, v169 op_sel_hi:[0,0,0]
	v_mfma_scale_f32_16x16x128_f8f6f4 v[38:41], v[10:17], v[236:243], v[38:41], v194, v169 op_sel_hi:[0,0,0]
	v_mfma_scale_f32_16x16x128_f8f6f4 v[34:37], v[2:9], v[236:243], v[34:37], v194, v169 op_sel_hi:[0,0,0]
	s_setprio 0
	s_barrier
	s_add_u32 s35, s35, 0x100
	s_addc_u32 s45, s45, 0
	s_cmp_lt_i32 s75, s16
	s_mov_b64 s[18:19], s[42:43]
	s_mov_b32 s70, s75
	s_cbranch_scc1 .LBB0_1923
	v_mov_b32_e32 v209, v1
	s_andn2_b64 vcc, exec, s[58:59]
	s_cbranch_vccnz .LBB0_1926
